# v43 + K-loop back-edge rotation: head scalar block and loop-carried updates moved to the end of the last load phase (7 GEMM loops)
# baseline (speedup 1.0000x reference)
; #define PG8_STAGE(bufoff, gbase, voff) do { _Pragma("unroll") for (int _i = 0; _i < 2; ++_i) \
;         __builtin_amdgcn_global_load_lds((const __attribute__((address_space(1))) unsigned*)((const __attribute__((address_space(1))) char*)(gbase) + (unsigned)lnd_v((int)(voff)[_i])), (LAS unsigned*)(lds + (bufoff) + ldsw + _i * 8192), 16, 0, 0); } while (0)
; #define PG8_LDA(dst, b, h) do { _Pragma("unroll") for (int m = 0; m < 4; ++m) _Pragma("unroll") for (int k = 0; k < 2; ++k) dst[m][k] = *(const LAS bf16x8*)(lds + PG8_SA(b, h) + aoff + m * 2048 + k * 1024); } while (0)
; #define PG8_LDB(dst, b, h) do { _Pragma("unroll") for (int n = 0; n < 2; ++n) _Pragma("unroll") for (int k = 0; k < 2; ++k) dst[n][k] = *(const LAS bf16x8*)(lds + PG8_SB(b, h) + boff + n * 2048 + k * 1024); } while (0)
; #define PG8_MMA(ai, bj, At, Bt) do { __builtin_amdgcn_s_setprio(1); _Pragma("unroll") for (int m = 0; m < 4; ++m) _Pragma("unroll") for (int n = 0; n < 2; ++n) _Pragma("unroll") for (int k = 0; k < 2; ++k) \
;         acc[ai][bj][m][n] = __builtin_amdgcn_mfma_f32_16x16x32_bf16(Bt[n][k], At[m][k], acc[ai][bj][m][n], 0, 0, 0); __builtin_amdgcn_s_setprio(0); } while (0)
; #define PG8_WAIT_V(n) asm volatile("s_waitcnt vmcnt(" #n ")" ::: "memory")
; #define PG8_WAIT_L(n) asm volatile("s_waitcnt lgkmcnt(" #n ")" ::: "memory")
; #define PG8_BAR __builtin_amdgcn_s_barrier()
; #define PG8_SCHED __builtin_amdgcn_sched_barrier(0)
; template <class Desc, class Epi>
; __device__ __forceinline__ void gemm_phase(const int wv_, LAS unsigned char* lds, const Desc& d, const Epi& E) {
;     ...
;             PG8_LDB(B0, 0, 0); PG8_LDB(B1, 0, 1); PG8_SCHED; PG8_LDA(At, 0, 0); PG8_STAGE(PG8_SA(1, 1), a1, voffA1);
;             PG8_WAIT_V(8); PG8_WAIT_L(0); PG8_BAR; PG8_MMA(0, 0, At, B0); PG8_MMA(0, 1, At, B1); PG8_BAR; PG8_SCHED;
;             PG8_LDA(At, 0, 1); PG8_STAGE(PG8_SB(0, 0), b2, voffB); PG8_STAGE(PG8_SB(0, 1), b2 + hstepB, voffB); PG8_STAGE(PG8_SA(0, 0), a2, sA0);
;             PG8_WAIT_V(8); PG8_WAIT_L(0); PG8_BAR; PG8_MMA(1, 0, At, B0); PG8_MMA(1, 1, At, B1); PG8_BAR; PG8_SCHED;
.Lkrot_747:
	ds_read_b128 v[150:153], v96
	ds_read_b128 v[154:157], v96 offset:1024
	ds_read_b128 v[158:161], v96 offset:2048
	ds_read_b128 v[162:165], v96 offset:3072
	v_add_u32_e32 v96, s66, v139
	ds_read_b128 v[166:169], v96
	ds_read_b128 v[170:173], v96 offset:1024
	ds_read_b128 v[174:177], v96 offset:2048
	ds_read_b128 v[178:181], v96 offset:3072
	v_mov_b32_e32 v96, v133
	ds_read_b128 v[182:185], v149
	ds_read_b128 v[186:189], v149 offset:1024
	ds_read_b128 v[190:193], v149 offset:2048
	ds_read_b128 v[194:197], v149 offset:3072
	ds_read_b128 v[198:201], v149 offset:4096
	ds_read_b128 v[202:205], v149 offset:5120
	ds_read_b128 v[206:209], v149 offset:6144
	ds_read_b128 v[210:213], v149 offset:7168
	s_add_i32 m0, s55, 0xc000
	s_nop 0
	global_load_lds_dwordx4 v96, s[2:3]
	v_mov_b32_e32 v96, v136
	s_add_i32 m0, s55, 0xe000
	s_nop 0
	global_load_lds_dwordx4 v96, s[2:3]
	s_waitcnt vmcnt(8)
	s_waitcnt lgkmcnt(0)
	s_barrier
	s_waitcnt lgkmcnt(0)
	v_mfma_f32_16x16x32_bf16 v[126:129], v[150:153], v[182:185], v[126:129]
	v_mfma_f32_16x16x32_bf16 v[122:125], v[158:161], v[182:185], v[122:125]
	v_mfma_f32_16x16x32_bf16 v[110:113], v[150:153], v[190:193], v[110:113]
	v_mfma_f32_16x16x32_bf16 v[106:109], v[158:161], v[190:193], v[106:109]
	v_mfma_f32_16x16x32_bf16 v[92:95], v[150:153], v[198:201], v[92:95]
	v_mfma_f32_16x16x32_bf16 v[88:91], v[158:161], v[198:201], v[88:91]
	v_mfma_f32_16x16x32_bf16 v[76:79], v[150:153], v[206:209], v[76:79]
	v_mfma_f32_16x16x32_bf16 v[72:75], v[158:161], v[206:209], v[72:75]
	v_mfma_f32_16x16x32_bf16 v[126:129], v[154:157], v[186:189], v[126:129]
	v_mfma_f32_16x16x32_bf16 v[122:125], v[162:165], v[186:189], v[122:125]
	v_mfma_f32_16x16x32_bf16 v[110:113], v[154:157], v[194:197], v[110:113]
	v_mfma_f32_16x16x32_bf16 v[106:109], v[162:165], v[194:197], v[106:109]
	v_mfma_f32_16x16x32_bf16 v[92:95], v[154:157], v[202:205], v[92:95]
	v_mfma_f32_16x16x32_bf16 v[88:91], v[162:165], v[202:205], v[88:91]
	v_mfma_f32_16x16x32_bf16 v[76:79], v[154:157], v[210:213], v[76:79]
	v_mfma_f32_16x16x32_bf16 v[72:75], v[162:165], v[210:213], v[72:75]
	v_mfma_f32_16x16x32_bf16 v[118:121], v[166:169], v[182:185], v[118:121]
	v_mfma_f32_16x16x32_bf16 v[114:117], v[174:177], v[182:185], v[114:117]
	v_mfma_f32_16x16x32_bf16 v[102:105], v[166:169], v[190:193], v[102:105]
	v_mfma_f32_16x16x32_bf16 v[98:101], v[174:177], v[190:193], v[98:101]
	v_mfma_f32_16x16x32_bf16 v[84:87], v[166:169], v[198:201], v[84:87]
	v_mfma_f32_16x16x32_bf16 v[80:83], v[174:177], v[198:201], v[80:83]
	v_mfma_f32_16x16x32_bf16 v[68:71], v[166:169], v[206:209], v[68:71]
	v_mfma_f32_16x16x32_bf16 v[64:67], v[174:177], v[206:209], v[64:67]
	v_mfma_f32_16x16x32_bf16 v[118:121], v[170:173], v[186:189], v[118:121]
	v_mfma_f32_16x16x32_bf16 v[114:117], v[178:181], v[186:189], v[114:117]
	v_mfma_f32_16x16x32_bf16 v[102:105], v[170:173], v[194:197], v[102:105]
	v_mfma_f32_16x16x32_bf16 v[98:101], v[178:181], v[194:197], v[98:101]
	v_mfma_f32_16x16x32_bf16 v[84:87], v[170:173], v[202:205], v[84:87]
	v_mfma_f32_16x16x32_bf16 v[80:83], v[178:181], v[202:205], v[80:83]
	v_mfma_f32_16x16x32_bf16 v[68:71], v[170:173], v[210:213], v[68:71]
	v_mfma_f32_16x16x32_bf16 v[64:67], v[178:181], v[210:213], v[64:67]
	s_barrier
	v_mov_b32_e32 v96, v134
	s_add_i32 s63, s63, s54
	ds_read_b128 v[182:185], v149 offset:16384
	ds_read_b128 v[186:189], v149 offset:17408
	ds_read_b128 v[190:193], v149 offset:18432
	ds_read_b128 v[194:197], v149 offset:19456
	ds_read_b128 v[198:201], v149 offset:20480
	ds_read_b128 v[202:205], v149 offset:21504
	ds_read_b128 v[206:209], v149 offset:22528
	ds_read_b128 v[210:213], v149 offset:23552
	s_mov_b32 m0, s63
	s_nop 0
	global_load_lds_dwordx4 v96, s[20:21]
	v_mov_b32_e32 v96, v137
	s_add_i32 m0, s63, 0x2000
	s_add_u32 s64, s20, 0x40000
	global_load_lds_dwordx4 v96, s[20:21]
	s_addc_u32 s65, s21, 0
	v_mov_b32_e32 v96, v134
	s_add_i32 s63, s66, s54
	s_mov_b32 m0, s63
	s_nop 0
	global_load_lds_dwordx4 v96, s[64:65]
	v_mov_b32_e32 v96, v137
	s_add_i32 m0, s63, 0x2000
	s_nop 0
	global_load_lds_dwordx4 v96, s[64:65]
	v_mov_b32_e32 v96, v132
	s_mov_b32 m0, s55
	s_nop 0
	global_load_lds_dwordx4 v96, s[4:5]
	v_mov_b32_e32 v96, v135
	s_mov_b32 m0, s56
	s_nop 0
	global_load_lds_dwordx4 v96, s[4:5]
	s_waitcnt vmcnt(8)
	s_waitcnt lgkmcnt(0)
	s_barrier
	s_waitcnt lgkmcnt(0)
	v_mfma_f32_16x16x32_bf16 v[60:63], v[150:153], v[182:185], v[60:63]
	v_mfma_f32_16x16x32_bf16 v[56:59], v[158:161], v[182:185], v[56:59]
	v_mfma_f32_16x16x32_bf16 v[44:47], v[150:153], v[190:193], v[44:47]
	v_mfma_f32_16x16x32_bf16 v[32:35], v[158:161], v[190:193], v[32:35]
	v_mfma_f32_16x16x32_bf16 v[16:19], v[150:153], v[198:201], v[16:19]
	v_mfma_f32_16x16x32_bf16 v[8:11], v[158:161], v[198:201], v[8:11]
	v_mfma_f32_16x16x32_bf16 v[4:7], v[150:153], v[206:209], v[4:7]
	v_mfma_f32_16x16x32_bf16 v[0:3], v[158:161], v[206:209], v[0:3]
	v_mfma_f32_16x16x32_bf16 v[60:63], v[154:157], v[186:189], v[60:63]
	v_mfma_f32_16x16x32_bf16 v[56:59], v[162:165], v[186:189], v[56:59]
	v_mfma_f32_16x16x32_bf16 v[44:47], v[154:157], v[194:197], v[44:47]
	v_mfma_f32_16x16x32_bf16 v[32:35], v[162:165], v[194:197], v[32:35]
	v_mfma_f32_16x16x32_bf16 v[16:19], v[154:157], v[202:205], v[16:19]
	v_mfma_f32_16x16x32_bf16 v[8:11], v[162:165], v[202:205], v[8:11]
	v_mfma_f32_16x16x32_bf16 v[4:7], v[154:157], v[210:213], v[4:7]
	v_mfma_f32_16x16x32_bf16 v[0:3], v[162:165], v[210:213], v[0:3]
	v_mfma_f32_16x16x32_bf16 v[52:55], v[166:169], v[182:185], v[52:55]
	v_mfma_f32_16x16x32_bf16 v[48:51], v[174:177], v[182:185], v[48:51]
	v_mfma_f32_16x16x32_bf16 v[28:31], v[166:169], v[190:193], v[28:31]
	v_mfma_f32_16x16x32_bf16 v[12:15], v[174:177], v[190:193], v[12:15]
	v_mfma_f32_16x16x32_bf16 v[36:39], v[166:169], v[198:201], v[36:39]
	v_mfma_f32_16x16x32_bf16 v[40:43], v[174:177], v[198:201], v[40:43]
	v_mfma_f32_16x16x32_bf16 v[20:23], v[166:169], v[206:209], v[20:23]
	v_mfma_f32_16x16x32_bf16 v[24:27], v[174:177], v[206:209], v[24:27]
	v_mfma_f32_16x16x32_bf16 v[52:55], v[170:173], v[186:189], v[52:55]
	v_mfma_f32_16x16x32_bf16 v[48:51], v[178:181], v[186:189], v[48:51]
	v_mfma_f32_16x16x32_bf16 v[28:31], v[170:173], v[194:197], v[28:31]
	v_mfma_f32_16x16x32_bf16 v[12:15], v[178:181], v[194:197], v[12:15]
	v_mfma_f32_16x16x32_bf16 v[36:39], v[170:173], v[202:205], v[36:39]
	v_mfma_f32_16x16x32_bf16 v[40:43], v[178:181], v[202:205], v[40:43]
	v_mfma_f32_16x16x32_bf16 v[20:23], v[170:173], v[210:213], v[20:23]
	v_mfma_f32_16x16x32_bf16 v[24:27], v[178:181], v[210:213], v[24:27]
	s_barrier
; #define PG8_STAGE(bufoff, gbase, voff) do { _Pragma("unroll") for (int _i = 0; _i < 2; ++_i) \
;         __builtin_amdgcn_global_load_lds((const __attribute__((address_space(1))) unsigned*)((const __attribute__((address_space(1))) char*)(gbase) + (unsigned)lnd_v((int)(voff)[_i])), (LAS unsigned*)(lds + (bufoff) + ldsw + _i * 8192), 16, 0, 0); } while (0)
; #define PG8_LDA(dst, b, h) do { _Pragma("unroll") for (int m = 0; m < 4; ++m) _Pragma("unroll") for (int k = 0; k < 2; ++k) dst[m][k] = *(const LAS bf16x8*)(lds + PG8_SA(b, h) + aoff + m * 2048 + k * 1024); } while (0)
; #define PG8_LDB(dst, b, h) do { _Pragma("unroll") for (int n = 0; n < 2; ++n) _Pragma("unroll") for (int k = 0; k < 2; ++k) dst[n][k] = *(const LAS bf16x8*)(lds + PG8_SB(b, h) + boff + n * 2048 + k * 1024); } while (0)
; #define PG8_MMA(ai, bj, At, Bt) do { __builtin_amdgcn_s_setprio(1); _Pragma("unroll") for (int m = 0; m < 4; ++m) _Pragma("unroll") for (int n = 0; n < 2; ++n) _Pragma("unroll") for (int k = 0; k < 2; ++k) \
;         acc[ai][bj][m][n] = __builtin_amdgcn_mfma_f32_16x16x32_bf16(Bt[n][k], At[m][k], acc[ai][bj][m][n], 0, 0, 0); __builtin_amdgcn_s_setprio(0); } while (0)
; #define PG8_WAIT_V(n) asm volatile("s_waitcnt vmcnt(" #n ")" ::: "memory")
; #define PG8_WAIT_L(n) asm volatile("s_waitcnt lgkmcnt(" #n ")" ::: "memory")
; #define PG8_BAR __builtin_amdgcn_s_barrier()
; #define PG8_SCHED __builtin_amdgcn_sched_barrier(0)
; template <class Desc, class Epi>
; __device__ __forceinline__ void gemm_phase(const int wv_, LAS unsigned char* lds, const Desc& d, const Epi& E) {
;     ...
;             PG8_LDB(B0, 1, 0); PG8_LDB(B1, 1, 1); PG8_SCHED; PG8_LDA(At, 1, 0); PG8_STAGE(PG8_SA(0, 1), a2, sA1);
;             PG8_WAIT_V(8); PG8_WAIT_L(0); PG8_BAR; PG8_MMA(0, 0, At, B0); PG8_MMA(0, 1, At, B1); PG8_BAR; PG8_SCHED;
	s_add_i32 s63, 0, 0x18000
	v_add_u32_e32 v96, s63, v139
	s_add_i32 s64, 0, 0x1c000
	ds_read_b128 v[150:153], v96
	ds_read_b128 v[154:157], v96 offset:1024
	ds_read_b128 v[158:161], v96 offset:2048
	ds_read_b128 v[162:165], v96 offset:3072
	v_add_u32_e32 v96, s64, v139
	ds_read_b128 v[166:169], v96
	ds_read_b128 v[170:173], v96 offset:1024
	ds_read_b128 v[174:177], v96 offset:2048
	ds_read_b128 v[178:181], v96 offset:3072
	v_mov_b32_e32 v96, v133
	s_mov_b32 m0, s57
	ds_read_b128 v[182:185], v149 offset:32768
	ds_read_b128 v[186:189], v149 offset:33792
	ds_read_b128 v[190:193], v149 offset:34816
	ds_read_b128 v[194:197], v149 offset:35840
	ds_read_b128 v[198:201], v149 offset:36864
	ds_read_b128 v[202:205], v149 offset:37888
	ds_read_b128 v[206:209], v149 offset:38912
	ds_read_b128 v[210:213], v149 offset:39936
	s_nop 0
	global_load_lds_dwordx4 v96, s[4:5]
	v_mov_b32_e32 v96, v136
	s_mov_b32 m0, s58
	s_nop 0
	global_load_lds_dwordx4 v96, s[4:5]
	s_waitcnt vmcnt(8)
	s_waitcnt lgkmcnt(0)
	s_barrier
	s_waitcnt lgkmcnt(0)
	v_mfma_f32_16x16x32_bf16 v[126:129], v[150:153], v[182:185], v[126:129]
	v_mfma_f32_16x16x32_bf16 v[122:125], v[158:161], v[182:185], v[122:125]
	v_mfma_f32_16x16x32_bf16 v[110:113], v[150:153], v[190:193], v[110:113]
	v_mfma_f32_16x16x32_bf16 v[106:109], v[158:161], v[190:193], v[106:109]
	v_mfma_f32_16x16x32_bf16 v[92:95], v[150:153], v[198:201], v[92:95]
	v_mfma_f32_16x16x32_bf16 v[88:91], v[158:161], v[198:201], v[88:91]
	v_mfma_f32_16x16x32_bf16 v[76:79], v[150:153], v[206:209], v[76:79]
	v_mfma_f32_16x16x32_bf16 v[72:75], v[158:161], v[206:209], v[72:75]
	v_mfma_f32_16x16x32_bf16 v[126:129], v[154:157], v[186:189], v[126:129]
	v_mfma_f32_16x16x32_bf16 v[122:125], v[162:165], v[186:189], v[122:125]
	v_mfma_f32_16x16x32_bf16 v[110:113], v[154:157], v[194:197], v[110:113]
	v_mfma_f32_16x16x32_bf16 v[106:109], v[162:165], v[194:197], v[106:109]
	v_mfma_f32_16x16x32_bf16 v[92:95], v[154:157], v[202:205], v[92:95]
	v_mfma_f32_16x16x32_bf16 v[88:91], v[162:165], v[202:205], v[88:91]
	v_mfma_f32_16x16x32_bf16 v[76:79], v[154:157], v[210:213], v[76:79]
	v_mfma_f32_16x16x32_bf16 v[72:75], v[162:165], v[210:213], v[72:75]
	v_mfma_f32_16x16x32_bf16 v[118:121], v[166:169], v[182:185], v[118:121]
	v_mfma_f32_16x16x32_bf16 v[114:117], v[174:177], v[182:185], v[114:117]
	v_mfma_f32_16x16x32_bf16 v[102:105], v[166:169], v[190:193], v[102:105]
	v_mfma_f32_16x16x32_bf16 v[98:101], v[174:177], v[190:193], v[98:101]
	v_mfma_f32_16x16x32_bf16 v[84:87], v[166:169], v[198:201], v[84:87]
	v_mfma_f32_16x16x32_bf16 v[80:83], v[174:177], v[198:201], v[80:83]
	v_mfma_f32_16x16x32_bf16 v[68:71], v[166:169], v[206:209], v[68:71]
	v_mfma_f32_16x16x32_bf16 v[64:67], v[174:177], v[206:209], v[64:67]
	v_mfma_f32_16x16x32_bf16 v[118:121], v[170:173], v[186:189], v[118:121]
	v_mfma_f32_16x16x32_bf16 v[114:117], v[178:181], v[186:189], v[114:117]
	v_mfma_f32_16x16x32_bf16 v[102:105], v[170:173], v[194:197], v[102:105]
	v_mfma_f32_16x16x32_bf16 v[98:101], v[178:181], v[194:197], v[98:101]
	v_mfma_f32_16x16x32_bf16 v[84:87], v[170:173], v[202:205], v[84:87]
	v_mfma_f32_16x16x32_bf16 v[80:83], v[178:181], v[202:205], v[80:83]
	v_mfma_f32_16x16x32_bf16 v[68:71], v[170:173], v[210:213], v[68:71]
	v_mfma_f32_16x16x32_bf16 v[64:67], v[178:181], v[210:213], v[64:67]
	s_barrier
; #define PG8_STAGE(bufoff, gbase, voff) do { _Pragma("unroll") for (int _i = 0; _i < 2; ++_i) \
;         __builtin_amdgcn_global_load_lds((const __attribute__((address_space(1))) unsigned*)((const __attribute__((address_space(1))) char*)(gbase) + (unsigned)lnd_v((int)(voff)[_i])), (LAS unsigned*)(lds + (bufoff) + ldsw + _i * 8192), 16, 0, 0); } while (0)
; #define PG8_LDA(dst, b, h) do { _Pragma("unroll") for (int m = 0; m < 4; ++m) _Pragma("unroll") for (int k = 0; k < 2; ++k) dst[m][k] = *(const LAS bf16x8*)(lds + PG8_SA(b, h) + aoff + m * 2048 + k * 1024); } while (0)
; #define PG8_MMA(ai, bj, At, Bt) do { __builtin_amdgcn_s_setprio(1); _Pragma("unroll") for (int m = 0; m < 4; ++m) _Pragma("unroll") for (int n = 0; n < 2; ++n) _Pragma("unroll") for (int k = 0; k < 2; ++k) \
;         acc[ai][bj][m][n] = __builtin_amdgcn_mfma_f32_16x16x32_bf16(Bt[n][k], At[m][k], acc[ai][bj][m][n], 0, 0, 0); __builtin_amdgcn_s_setprio(0); } while (0)
; #define PG8_WAIT_V(n) asm volatile("s_waitcnt vmcnt(" #n ")" ::: "memory")
; #define PG8_WAIT_L(n) asm volatile("s_waitcnt lgkmcnt(" #n ")" ::: "memory")
; #define PG8_BAR __builtin_amdgcn_s_barrier()
; #define PG8_SCHED __builtin_amdgcn_sched_barrier(0)
; template <class Desc, class Epi>
; __device__ __forceinline__ void gemm_phase(const int wv_, LAS unsigned char* lds, const Desc& d, const Epi& E) {
;     ...
;         for (int t = 0; t < nt; t += 2) {
;             const bool last = (t == nt - 2);
;             unsigned sA0[2], sA1[2];
;             if constexpr (Desc::GATHER) { sA0[0] = last ? voffAn[0] : voffA[0]; sA0[1] = last ? voffAn[1] : voffA[1]; sA1[0] = last ? voffAn1[0] : voffA1[0]; sA1[1] = last ? voffAn1[1] : voffA1[1]; }
;             else { sA0[0] = voffA[0]; sA0[1] = voffA[1]; sA1[0] = voffA1[0]; sA1[1] = voffA1[1]; }
;             const char* a1 = cA + (size_t)(t + 1) * kstep;
;             const char* a2 = last ? nA : cA + (size_t)(t + 2) * kstep; const char* b2 = last ? nB : cB + (size_t)(t + 2) * kstep;
;     ...
;             PG8_LDA(At, 1, 1); PG8_STAGE(PG8_SB(1, 0), b3, voffB); PG8_STAGE(PG8_SB(1, 1), b3 + hstepB, voffB); PG8_STAGE(PG8_SA(1, 0), a3, sA0);
;             PG8_WAIT_V(8); PG8_WAIT_L(0); PG8_BAR; PG8_MMA(1, 0, At, B0); PG8_MMA(1, 1, At, B1); PG8_BAR; PG8_SCHED;
;         }
	v_mov_b32_e32 v96, v134
	ds_read_b128 v[182:185], v149 offset:49152
	ds_read_b128 v[186:189], v149 offset:50176
	ds_read_b128 v[190:193], v149 offset:51200
	ds_read_b128 v[194:197], v149 offset:52224
	ds_read_b128 v[198:201], v149 offset:53248
	ds_read_b128 v[202:205], v149 offset:54272
	ds_read_b128 v[206:209], v149 offset:55296
	ds_read_b128 v[210:213], v149 offset:56320
	s_add_i32 s63, s63, s54
	v_lshl_add_u64 v[130:131], s[20:21], 0, v[96:97]
	v_lshl_add_u64 v[130:131], v[130:131], 0, s[30:31]
	s_mov_b32 m0, s63
	v_mov_b32_e32 v96, v137
	global_load_lds_dwordx4 v[130:131], off
	s_add_i32 m0, s63, 0x2000
	s_nop 0
	v_lshl_add_u64 v[130:131], s[20:21], 0, v[96:97]
	s_add_u32 s20, s20, 0x40080
	v_lshl_add_u64 v[130:131], v[130:131], 0, s[30:31]
	s_addc_u32 s21, s21, 0
	v_mov_b32_e32 v96, v134
	s_add_i32 s63, s64, s54
	global_load_lds_dwordx4 v[130:131], off
	s_mov_b32 m0, s63
	s_nop 0
	global_load_lds_dwordx4 v96, s[20:21]
	v_mov_b32_e32 v96, v137
	s_add_i32 m0, s63, 0x2000
	s_nop 0
	global_load_lds_dwordx4 v96, s[20:21]
	v_mov_b32_e32 v96, v132
	s_mov_b32 m0, s59
	v_lshl_add_u64 v[130:131], s[4:5], 0, v[96:97]
	v_lshl_add_u64 v[130:131], v[130:131], 0, s[30:31]
	v_mov_b32_e32 v96, v135
	global_load_lds_dwordx4 v[130:131], off
	s_mov_b32 m0, s60
	v_lshl_add_u64 v[130:131], s[4:5], 0, v[96:97]
	v_lshl_add_u64 v[130:131], v[130:131], 0, s[30:31]
	global_load_lds_dwordx4 v[130:131], off
	s_add_i32 s45, s45, 2
	s_add_u32 s2, s2, 0x100
	s_addc_u32 s3, s3, 0
	s_add_u32 s29, s29, 0x100
	s_addc_u32 s43, s43, 0
	s_add_u32 s4, s2, 0x80
	s_addc_u32 s5, s3, 0
	s_add_i32 s63, 0, 0x10000
	s_cmp_eq_u32 s45, 12
	s_cselect_b32 s5, s47, s5
	s_cselect_b32 s4, s46, s4
	v_add_u32_e32 v96, s63, v139
	s_cselect_b32 s21, s49, s43
	s_cselect_b32 s20, s48, s29
	s_add_i32 s66, 0, 0x14000
	s_waitcnt vmcnt(8)
	s_waitcnt lgkmcnt(0)
	s_barrier
	s_waitcnt lgkmcnt(0)
	v_mfma_f32_16x16x32_bf16 v[60:63], v[150:153], v[182:185], v[60:63]
	v_mfma_f32_16x16x32_bf16 v[56:59], v[158:161], v[182:185], v[56:59]
	v_mfma_f32_16x16x32_bf16 v[44:47], v[150:153], v[190:193], v[44:47]
	v_mfma_f32_16x16x32_bf16 v[32:35], v[158:161], v[190:193], v[32:35]
	v_mfma_f32_16x16x32_bf16 v[16:19], v[150:153], v[198:201], v[16:19]
	v_mfma_f32_16x16x32_bf16 v[8:11], v[158:161], v[198:201], v[8:11]
	v_mfma_f32_16x16x32_bf16 v[4:7], v[150:153], v[206:209], v[4:7]
	v_mfma_f32_16x16x32_bf16 v[0:3], v[158:161], v[206:209], v[0:3]
	v_mfma_f32_16x16x32_bf16 v[60:63], v[154:157], v[186:189], v[60:63]
	v_mfma_f32_16x16x32_bf16 v[56:59], v[162:165], v[186:189], v[56:59]
	v_mfma_f32_16x16x32_bf16 v[44:47], v[154:157], v[194:197], v[44:47]
	v_mfma_f32_16x16x32_bf16 v[32:35], v[162:165], v[194:197], v[32:35]
	v_mfma_f32_16x16x32_bf16 v[16:19], v[154:157], v[202:205], v[16:19]
	v_mfma_f32_16x16x32_bf16 v[8:11], v[162:165], v[202:205], v[8:11]
	v_mfma_f32_16x16x32_bf16 v[4:7], v[154:157], v[210:213], v[4:7]
	v_mfma_f32_16x16x32_bf16 v[0:3], v[162:165], v[210:213], v[0:3]
	v_mfma_f32_16x16x32_bf16 v[52:55], v[166:169], v[182:185], v[52:55]
	v_mfma_f32_16x16x32_bf16 v[48:51], v[174:177], v[182:185], v[48:51]
	v_mfma_f32_16x16x32_bf16 v[28:31], v[166:169], v[190:193], v[28:31]
	v_mfma_f32_16x16x32_bf16 v[12:15], v[174:177], v[190:193], v[12:15]
	v_mfma_f32_16x16x32_bf16 v[36:39], v[166:169], v[198:201], v[36:39]
	v_mfma_f32_16x16x32_bf16 v[40:43], v[174:177], v[198:201], v[40:43]
	v_mfma_f32_16x16x32_bf16 v[20:23], v[166:169], v[206:209], v[20:23]
	v_mfma_f32_16x16x32_bf16 v[24:27], v[174:177], v[206:209], v[24:27]
	v_mfma_f32_16x16x32_bf16 v[52:55], v[170:173], v[186:189], v[52:55]
	v_mfma_f32_16x16x32_bf16 v[48:51], v[178:181], v[186:189], v[48:51]
	v_mfma_f32_16x16x32_bf16 v[28:31], v[170:173], v[194:197], v[28:31]
	v_mfma_f32_16x16x32_bf16 v[12:15], v[178:181], v[194:197], v[12:15]
	v_mfma_f32_16x16x32_bf16 v[36:39], v[170:173], v[202:205], v[36:39]
	v_mfma_f32_16x16x32_bf16 v[40:43], v[178:181], v[202:205], v[40:43]
	v_mfma_f32_16x16x32_bf16 v[20:23], v[170:173], v[210:213], v[20:23]
	v_mfma_f32_16x16x32_bf16 v[24:27], v[178:181], v[210:213], v[24:27]
	s_barrier
	s_cmp_gt_u32 s45, 13
	s_cbranch_scc0 .Lkrot_747
	s_and_b64 vcc, exec, s[40:41]
	s_cbranch_vccz .LBB0_750
	s_barrier

; #define PG8_STAGE(bufoff, gbase, voff) do { _Pragma("unroll") for (int _i = 0; _i < 2; ++_i) \
;         __builtin_amdgcn_global_load_lds((const __attribute__((address_space(1))) unsigned*)((const __attribute__((address_space(1))) char*)(gbase) + (unsigned)lnd_v((int)(voff)[_i])), (LAS unsigned*)(lds + (bufoff) + ldsw + _i * 8192), 16, 0, 0); } while (0)
; #define PG8_LDA(dst, b, h) do { _Pragma("unroll") for (int m = 0; m < 4; ++m) _Pragma("unroll") for (int k = 0; k < 2; ++k) dst[m][k] = *(const LAS bf16x8*)(lds + PG8_SA(b, h) + aoff + m * 2048 + k * 1024); } while (0)
; #define PG8_LDB(dst, b, h) do { _Pragma("unroll") for (int n = 0; n < 2; ++n) _Pragma("unroll") for (int k = 0; k < 2; ++k) dst[n][k] = *(const LAS bf16x8*)(lds + PG8_SB(b, h) + boff + n * 2048 + k * 1024); } while (0)
; #define PG8_MMA(ai, bj, At, Bt) do { __builtin_amdgcn_s_setprio(1); _Pragma("unroll") for (int m = 0; m < 4; ++m) _Pragma("unroll") for (int n = 0; n < 2; ++n) _Pragma("unroll") for (int k = 0; k < 2; ++k) \
;         acc[ai][bj][m][n] = __builtin_amdgcn_mfma_f32_16x16x32_bf16(Bt[n][k], At[m][k], acc[ai][bj][m][n], 0, 0, 0); __builtin_amdgcn_s_setprio(0); } while (0)
; #define PG8_WAIT_V(n) asm volatile("s_waitcnt vmcnt(" #n ")" ::: "memory")
; #define PG8_WAIT_L(n) asm volatile("s_waitcnt lgkmcnt(" #n ")" ::: "memory")
; #define PG8_BAR __builtin_amdgcn_s_barrier()
; #define PG8_SCHED __builtin_amdgcn_sched_barrier(0)
; template <class Desc, class Epi>
; __device__ __forceinline__ void gemm_phase(const int wv_, LAS unsigned char* lds, const Desc& d, const Epi& E) {
;     ...
;             PG8_LDB(B0, 0, 0); PG8_LDB(B1, 0, 1); PG8_SCHED; PG8_LDA(At, 0, 0); PG8_STAGE(PG8_SA(1, 1), a1, voffA1);
;             PG8_WAIT_V(8); PG8_WAIT_L(0); PG8_BAR; PG8_MMA(0, 0, At, B0); PG8_MMA(0, 1, At, B1); PG8_BAR; PG8_SCHED;
;             PG8_LDA(At, 0, 1); PG8_STAGE(PG8_SB(0, 0), b2, voffB); PG8_STAGE(PG8_SB(0, 1), b2 + hstepB, voffB); PG8_STAGE(PG8_SA(0, 0), a2, sA0);
;             PG8_WAIT_V(8); PG8_WAIT_L(0); PG8_BAR; PG8_MMA(1, 0, At, B0); PG8_MMA(1, 1, At, B1); PG8_BAR; PG8_SCHED;
.Lkrot_1075:
	ds_read_b128 v[118:121], v96
	ds_read_b128 v[126:129], v96 offset:1024
	ds_read_b128 v[130:133], v96 offset:2048
	ds_read_b128 v[134:137], v96 offset:3072
	v_add_u32_e32 v96, s49, v226
	ds_read_b128 v[142:145], v96
	ds_read_b128 v[150:153], v96 offset:1024
	ds_read_b128 v[154:157], v96 offset:2048
	ds_read_b128 v[158:161], v96 offset:3072
	v_mov_b32_e32 v96, v220
	ds_read_b128 v[162:165], v231
	ds_read_b128 v[166:169], v231 offset:1024
	ds_read_b128 v[170:173], v231 offset:2048
	ds_read_b128 v[174:177], v231 offset:3072
	ds_read_b128 v[178:181], v231 offset:4096
	ds_read_b128 v[182:185], v231 offset:5120
	ds_read_b128 v[186:189], v231 offset:6144
	ds_read_b128 v[190:193], v231 offset:7168
	s_add_i32 m0, s60, 0xc000
	s_nop 0
	global_load_lds_dwordx4 v96, s[2:3]
	v_mov_b32_e32 v96, v223
	s_add_i32 m0, s60, 0xe000
	s_nop 0
	global_load_lds_dwordx4 v96, s[2:3]
	s_waitcnt vmcnt(8)
	s_waitcnt lgkmcnt(0)
	s_barrier
	s_waitcnt lgkmcnt(0)
	v_mfma_f32_16x16x32_bf16 v[146:149], v[118:121], v[162:165], v[146:149]
	v_mfma_f32_16x16x32_bf16 v[138:141], v[130:133], v[162:165], v[138:141]
	v_mfma_f32_16x16x32_bf16 v[110:113], v[118:121], v[170:173], v[110:113]
	v_mfma_f32_16x16x32_bf16 v[106:109], v[130:133], v[170:173], v[106:109]
	v_mfma_f32_16x16x32_bf16 v[92:95], v[118:121], v[178:181], v[92:95]
	v_mfma_f32_16x16x32_bf16 v[88:91], v[130:133], v[178:181], v[88:91]
	v_mfma_f32_16x16x32_bf16 v[76:79], v[118:121], v[186:189], v[76:79]
	v_mfma_f32_16x16x32_bf16 v[72:75], v[130:133], v[186:189], v[72:75]
	v_mfma_f32_16x16x32_bf16 v[146:149], v[126:129], v[166:169], v[146:149]
	v_mfma_f32_16x16x32_bf16 v[138:141], v[134:137], v[166:169], v[138:141]
	v_mfma_f32_16x16x32_bf16 v[110:113], v[126:129], v[174:177], v[110:113]
	v_mfma_f32_16x16x32_bf16 v[106:109], v[134:137], v[174:177], v[106:109]
	v_mfma_f32_16x16x32_bf16 v[92:95], v[126:129], v[182:185], v[92:95]
	v_mfma_f32_16x16x32_bf16 v[88:91], v[134:137], v[182:185], v[88:91]
	v_mfma_f32_16x16x32_bf16 v[76:79], v[126:129], v[190:193], v[76:79]
	v_mfma_f32_16x16x32_bf16 v[72:75], v[134:137], v[190:193], v[72:75]
	v_mfma_f32_16x16x32_bf16 v[122:125], v[142:145], v[162:165], v[122:125]
	v_mfma_f32_16x16x32_bf16 v[114:117], v[154:157], v[162:165], v[114:117]
	v_mfma_f32_16x16x32_bf16 v[102:105], v[142:145], v[170:173], v[102:105]
	v_mfma_f32_16x16x32_bf16 v[98:101], v[154:157], v[170:173], v[98:101]
	v_mfma_f32_16x16x32_bf16 v[84:87], v[142:145], v[178:181], v[84:87]
	v_mfma_f32_16x16x32_bf16 v[80:83], v[154:157], v[178:181], v[80:83]
	v_mfma_f32_16x16x32_bf16 v[68:71], v[142:145], v[186:189], v[68:71]
	v_mfma_f32_16x16x32_bf16 v[64:67], v[154:157], v[186:189], v[64:67]
	v_mfma_f32_16x16x32_bf16 v[122:125], v[150:153], v[166:169], v[122:125]
	v_mfma_f32_16x16x32_bf16 v[114:117], v[158:161], v[166:169], v[114:117]
	v_mfma_f32_16x16x32_bf16 v[102:105], v[150:153], v[174:177], v[102:105]
	v_mfma_f32_16x16x32_bf16 v[98:101], v[158:161], v[174:177], v[98:101]
	v_mfma_f32_16x16x32_bf16 v[84:87], v[150:153], v[182:185], v[84:87]
	v_mfma_f32_16x16x32_bf16 v[80:83], v[158:161], v[182:185], v[80:83]
	v_mfma_f32_16x16x32_bf16 v[68:71], v[150:153], v[190:193], v[68:71]
	v_mfma_f32_16x16x32_bf16 v[64:67], v[158:161], v[190:193], v[64:67]
	s_barrier
	v_mov_b32_e32 v96, v221
	s_add_i32 s47, s47, s59
	ds_read_b128 v[162:165], v231 offset:16384
	ds_read_b128 v[166:169], v231 offset:17408
	ds_read_b128 v[170:173], v231 offset:18432
	ds_read_b128 v[174:177], v231 offset:19456
	ds_read_b128 v[178:181], v231 offset:20480
	ds_read_b128 v[182:185], v231 offset:21504
	ds_read_b128 v[186:189], v231 offset:22528
	ds_read_b128 v[190:193], v231 offset:23552
	s_mov_b32 m0, s47
	s_nop 0
	global_load_lds_dwordx4 v96, s[20:21]
	v_mov_b32_e32 v96, v224
	s_add_i32 m0, s47, 0x2000
	s_add_u32 s70, s20, 0x40000
	global_load_lds_dwordx4 v96, s[20:21]
	s_addc_u32 s71, s21, 0
	v_mov_b32_e32 v96, v221
	s_add_i32 s47, s49, s59
	s_mov_b32 m0, s47
	s_nop 0
	global_load_lds_dwordx4 v96, s[70:71]
	v_mov_b32_e32 v96, v224
	s_add_i32 m0, s47, 0x2000
	s_nop 0
	global_load_lds_dwordx4 v96, s[70:71]
	v_mov_b32_e32 v96, v219
	s_mov_b32 m0, s60
	s_nop 0
	global_load_lds_dwordx4 v96, s[4:5]
	v_mov_b32_e32 v96, v222
	s_mov_b32 m0, s62
	s_nop 0
	global_load_lds_dwordx4 v96, s[4:5]
	s_waitcnt vmcnt(8)
	s_waitcnt lgkmcnt(0)
	s_barrier
	s_waitcnt lgkmcnt(0)
	v_mfma_f32_16x16x32_bf16 v[60:63], v[118:121], v[162:165], v[60:63]
	v_mfma_f32_16x16x32_bf16 v[56:59], v[130:133], v[162:165], v[56:59]
	v_mfma_f32_16x16x32_bf16 v[44:47], v[118:121], v[170:173], v[44:47]
	v_mfma_f32_16x16x32_bf16 v[40:43], v[130:133], v[170:173], v[40:43]
	v_mfma_f32_16x16x32_bf16 v[20:23], v[118:121], v[178:181], v[20:23]
	v_mfma_f32_16x16x32_bf16 v[16:19], v[130:133], v[178:181], v[16:19]
	v_mfma_f32_16x16x32_bf16 v[4:7], v[118:121], v[186:189], v[4:7]
	v_mfma_f32_16x16x32_bf16 v[0:3], v[130:133], v[186:189], v[0:3]
	v_mfma_f32_16x16x32_bf16 v[60:63], v[126:129], v[166:169], v[60:63]
	v_mfma_f32_16x16x32_bf16 v[56:59], v[134:137], v[166:169], v[56:59]
	v_mfma_f32_16x16x32_bf16 v[44:47], v[126:129], v[174:177], v[44:47]
	v_mfma_f32_16x16x32_bf16 v[40:43], v[134:137], v[174:177], v[40:43]
	v_mfma_f32_16x16x32_bf16 v[20:23], v[126:129], v[182:185], v[20:23]
	v_mfma_f32_16x16x32_bf16 v[16:19], v[134:137], v[182:185], v[16:19]
	v_mfma_f32_16x16x32_bf16 v[4:7], v[126:129], v[190:193], v[4:7]
	v_mfma_f32_16x16x32_bf16 v[0:3], v[134:137], v[190:193], v[0:3]
	v_mfma_f32_16x16x32_bf16 v[52:55], v[142:145], v[162:165], v[52:55]
	v_mfma_f32_16x16x32_bf16 v[48:51], v[154:157], v[162:165], v[48:51]
	v_mfma_f32_16x16x32_bf16 v[36:39], v[142:145], v[170:173], v[36:39]
	v_mfma_f32_16x16x32_bf16 v[32:35], v[154:157], v[170:173], v[32:35]
	v_mfma_f32_16x16x32_bf16 v[28:31], v[142:145], v[178:181], v[28:31]
	v_mfma_f32_16x16x32_bf16 v[24:27], v[154:157], v[178:181], v[24:27]
	v_mfma_f32_16x16x32_bf16 v[12:15], v[142:145], v[186:189], v[12:15]
	v_mfma_f32_16x16x32_bf16 v[8:11], v[154:157], v[186:189], v[8:11]
	v_mfma_f32_16x16x32_bf16 v[52:55], v[150:153], v[166:169], v[52:55]
	v_mfma_f32_16x16x32_bf16 v[48:51], v[158:161], v[166:169], v[48:51]
	v_mfma_f32_16x16x32_bf16 v[36:39], v[150:153], v[174:177], v[36:39]
	v_mfma_f32_16x16x32_bf16 v[32:35], v[158:161], v[174:177], v[32:35]
	v_mfma_f32_16x16x32_bf16 v[28:31], v[150:153], v[182:185], v[28:31]
	v_mfma_f32_16x16x32_bf16 v[24:27], v[158:161], v[182:185], v[24:27]
	v_mfma_f32_16x16x32_bf16 v[12:15], v[150:153], v[190:193], v[12:15]
	v_mfma_f32_16x16x32_bf16 v[8:11], v[158:161], v[190:193], v[8:11]
	s_barrier
; #define PG8_STAGE(bufoff, gbase, voff) do { _Pragma("unroll") for (int _i = 0; _i < 2; ++_i) \
;         __builtin_amdgcn_global_load_lds((const __attribute__((address_space(1))) unsigned*)((const __attribute__((address_space(1))) char*)(gbase) + (unsigned)lnd_v((int)(voff)[_i])), (LAS unsigned*)(lds + (bufoff) + ldsw + _i * 8192), 16, 0, 0); } while (0)
; #define PG8_LDA(dst, b, h) do { _Pragma("unroll") for (int m = 0; m < 4; ++m) _Pragma("unroll") for (int k = 0; k < 2; ++k) dst[m][k] = *(const LAS bf16x8*)(lds + PG8_SA(b, h) + aoff + m * 2048 + k * 1024); } while (0)
; #define PG8_LDB(dst, b, h) do { _Pragma("unroll") for (int n = 0; n < 2; ++n) _Pragma("unroll") for (int k = 0; k < 2; ++k) dst[n][k] = *(const LAS bf16x8*)(lds + PG8_SB(b, h) + boff + n * 2048 + k * 1024); } while (0)
; #define PG8_MMA(ai, bj, At, Bt) do { __builtin_amdgcn_s_setprio(1); _Pragma("unroll") for (int m = 0; m < 4; ++m) _Pragma("unroll") for (int n = 0; n < 2; ++n) _Pragma("unroll") for (int k = 0; k < 2; ++k) \
;         acc[ai][bj][m][n] = __builtin_amdgcn_mfma_f32_16x16x32_bf16(Bt[n][k], At[m][k], acc[ai][bj][m][n], 0, 0, 0); __builtin_amdgcn_s_setprio(0); } while (0)
; #define PG8_WAIT_V(n) asm volatile("s_waitcnt vmcnt(" #n ")" ::: "memory")
; #define PG8_WAIT_L(n) asm volatile("s_waitcnt lgkmcnt(" #n ")" ::: "memory")
; #define PG8_BAR __builtin_amdgcn_s_barrier()
; #define PG8_SCHED __builtin_amdgcn_sched_barrier(0)
; template <class Desc, class Epi>
; __device__ __forceinline__ void gemm_phase(const int wv_, LAS unsigned char* lds, const Desc& d, const Epi& E) {
;     ...
;             PG8_LDB(B0, 1, 0); PG8_LDB(B1, 1, 1); PG8_SCHED; PG8_LDA(At, 1, 0); PG8_STAGE(PG8_SA(0, 1), a2, sA1);
;             PG8_WAIT_V(8); PG8_WAIT_L(0); PG8_BAR; PG8_MMA(0, 0, At, B0); PG8_MMA(0, 1, At, B1); PG8_BAR; PG8_SCHED;
	s_add_i32 s47, 0, 0x18000
	v_add_u32_e32 v96, s47, v226
	s_add_i32 s49, 0, 0x1c000
	ds_read_b128 v[118:121], v96
	ds_read_b128 v[126:129], v96 offset:1024
	ds_read_b128 v[130:133], v96 offset:2048
	ds_read_b128 v[134:137], v96 offset:3072
	v_add_u32_e32 v96, s49, v226
	ds_read_b128 v[142:145], v96
	ds_read_b128 v[150:153], v96 offset:1024
	ds_read_b128 v[154:157], v96 offset:2048
	ds_read_b128 v[158:161], v96 offset:3072
	v_mov_b32_e32 v96, v220
	s_mov_b32 m0, s63
	ds_read_b128 v[162:165], v231 offset:32768
	ds_read_b128 v[166:169], v231 offset:33792
	ds_read_b128 v[170:173], v231 offset:34816
	ds_read_b128 v[174:177], v231 offset:35840
	ds_read_b128 v[178:181], v231 offset:36864
	ds_read_b128 v[182:185], v231 offset:37888
	ds_read_b128 v[186:189], v231 offset:38912
	ds_read_b128 v[190:193], v231 offset:39936
	s_nop 0
	global_load_lds_dwordx4 v96, s[4:5]
	v_mov_b32_e32 v96, v223
	s_mov_b32 m0, s64
	s_nop 0
	global_load_lds_dwordx4 v96, s[4:5]
	s_waitcnt vmcnt(8)
	s_waitcnt lgkmcnt(0)
	s_barrier
	s_waitcnt lgkmcnt(0)
	v_mfma_f32_16x16x32_bf16 v[146:149], v[118:121], v[162:165], v[146:149]
	v_mfma_f32_16x16x32_bf16 v[138:141], v[130:133], v[162:165], v[138:141]
	v_mfma_f32_16x16x32_bf16 v[110:113], v[118:121], v[170:173], v[110:113]
	v_mfma_f32_16x16x32_bf16 v[106:109], v[130:133], v[170:173], v[106:109]
	v_mfma_f32_16x16x32_bf16 v[92:95], v[118:121], v[178:181], v[92:95]
	v_mfma_f32_16x16x32_bf16 v[88:91], v[130:133], v[178:181], v[88:91]
	v_mfma_f32_16x16x32_bf16 v[76:79], v[118:121], v[186:189], v[76:79]
	v_mfma_f32_16x16x32_bf16 v[72:75], v[130:133], v[186:189], v[72:75]
	v_mfma_f32_16x16x32_bf16 v[146:149], v[126:129], v[166:169], v[146:149]
	v_mfma_f32_16x16x32_bf16 v[138:141], v[134:137], v[166:169], v[138:141]
	v_mfma_f32_16x16x32_bf16 v[110:113], v[126:129], v[174:177], v[110:113]
	v_mfma_f32_16x16x32_bf16 v[106:109], v[134:137], v[174:177], v[106:109]
	v_mfma_f32_16x16x32_bf16 v[92:95], v[126:129], v[182:185], v[92:95]
	v_mfma_f32_16x16x32_bf16 v[88:91], v[134:137], v[182:185], v[88:91]
	v_mfma_f32_16x16x32_bf16 v[76:79], v[126:129], v[190:193], v[76:79]
	v_mfma_f32_16x16x32_bf16 v[72:75], v[134:137], v[190:193], v[72:75]
	v_mfma_f32_16x16x32_bf16 v[122:125], v[142:145], v[162:165], v[122:125]
	v_mfma_f32_16x16x32_bf16 v[114:117], v[154:157], v[162:165], v[114:117]
	v_mfma_f32_16x16x32_bf16 v[102:105], v[142:145], v[170:173], v[102:105]
	v_mfma_f32_16x16x32_bf16 v[98:101], v[154:157], v[170:173], v[98:101]
	v_mfma_f32_16x16x32_bf16 v[84:87], v[142:145], v[178:181], v[84:87]
	v_mfma_f32_16x16x32_bf16 v[80:83], v[154:157], v[178:181], v[80:83]
	v_mfma_f32_16x16x32_bf16 v[68:71], v[142:145], v[186:189], v[68:71]
	v_mfma_f32_16x16x32_bf16 v[64:67], v[154:157], v[186:189], v[64:67]
	v_mfma_f32_16x16x32_bf16 v[122:125], v[150:153], v[166:169], v[122:125]
	v_mfma_f32_16x16x32_bf16 v[114:117], v[158:161], v[166:169], v[114:117]
	v_mfma_f32_16x16x32_bf16 v[102:105], v[150:153], v[174:177], v[102:105]
	v_mfma_f32_16x16x32_bf16 v[98:101], v[158:161], v[174:177], v[98:101]
	v_mfma_f32_16x16x32_bf16 v[84:87], v[150:153], v[182:185], v[84:87]
	v_mfma_f32_16x16x32_bf16 v[80:83], v[158:161], v[182:185], v[80:83]
	v_mfma_f32_16x16x32_bf16 v[68:71], v[150:153], v[190:193], v[68:71]
	v_mfma_f32_16x16x32_bf16 v[64:67], v[158:161], v[190:193], v[64:67]
	s_barrier
; #define PG8_STAGE(bufoff, gbase, voff) do { _Pragma("unroll") for (int _i = 0; _i < 2; ++_i) \
;         __builtin_amdgcn_global_load_lds((const __attribute__((address_space(1))) unsigned*)((const __attribute__((address_space(1))) char*)(gbase) + (unsigned)lnd_v((int)(voff)[_i])), (LAS unsigned*)(lds + (bufoff) + ldsw + _i * 8192), 16, 0, 0); } while (0)
; #define PG8_LDA(dst, b, h) do { _Pragma("unroll") for (int m = 0; m < 4; ++m) _Pragma("unroll") for (int k = 0; k < 2; ++k) dst[m][k] = *(const LAS bf16x8*)(lds + PG8_SA(b, h) + aoff + m * 2048 + k * 1024); } while (0)
; #define PG8_MMA(ai, bj, At, Bt) do { __builtin_amdgcn_s_setprio(1); _Pragma("unroll") for (int m = 0; m < 4; ++m) _Pragma("unroll") for (int n = 0; n < 2; ++n) _Pragma("unroll") for (int k = 0; k < 2; ++k) \
;         acc[ai][bj][m][n] = __builtin_amdgcn_mfma_f32_16x16x32_bf16(Bt[n][k], At[m][k], acc[ai][bj][m][n], 0, 0, 0); __builtin_amdgcn_s_setprio(0); } while (0)
; #define PG8_WAIT_V(n) asm volatile("s_waitcnt vmcnt(" #n ")" ::: "memory")
; #define PG8_WAIT_L(n) asm volatile("s_waitcnt lgkmcnt(" #n ")" ::: "memory")
; #define PG8_BAR __builtin_amdgcn_s_barrier()
; #define PG8_SCHED __builtin_amdgcn_sched_barrier(0)
; template <class Desc, class Epi>
; __device__ __forceinline__ void gemm_phase(const int wv_, LAS unsigned char* lds, const Desc& d, const Epi& E) {
;     ...
;         for (int t = 0; t < nt; t += 2) {
;             const bool last = (t == nt - 2);
;             unsigned sA0[2], sA1[2];
;             if constexpr (Desc::GATHER) { sA0[0] = last ? voffAn[0] : voffA[0]; sA0[1] = last ? voffAn[1] : voffA[1]; sA1[0] = last ? voffAn1[0] : voffA1[0]; sA1[1] = last ? voffAn1[1] : voffA1[1]; }
;             else { sA0[0] = voffA[0]; sA0[1] = voffA[1]; sA1[0] = voffA1[0]; sA1[1] = voffA1[1]; }
;             const char* a1 = cA + (size_t)(t + 1) * kstep;
;             const char* a2 = last ? nA : cA + (size_t)(t + 2) * kstep; const char* b2 = last ? nB : cB + (size_t)(t + 2) * kstep;
;     ...
;             PG8_LDA(At, 1, 1); PG8_STAGE(PG8_SB(1, 0), b3, voffB); PG8_STAGE(PG8_SB(1, 1), b3 + hstepB, voffB); PG8_STAGE(PG8_SA(1, 0), a3, sA0);
;             PG8_WAIT_V(8); PG8_WAIT_L(0); PG8_BAR; PG8_MMA(1, 0, At, B0); PG8_MMA(1, 1, At, B1); PG8_BAR; PG8_SCHED;
;         }
	v_mov_b32_e32 v96, v221
	ds_read_b128 v[162:165], v231 offset:49152
	ds_read_b128 v[166:169], v231 offset:50176
	ds_read_b128 v[170:173], v231 offset:51200
	ds_read_b128 v[174:177], v231 offset:52224
	ds_read_b128 v[178:181], v231 offset:53248
	ds_read_b128 v[182:185], v231 offset:54272
	ds_read_b128 v[186:189], v231 offset:55296
	ds_read_b128 v[190:193], v231 offset:56320
	s_add_i32 s47, s47, s59
	v_lshl_add_u64 v[194:195], s[20:21], 0, v[96:97]
	v_lshl_add_u64 v[194:195], v[194:195], 0, s[30:31]
	s_mov_b32 m0, s47
	v_mov_b32_e32 v96, v224
	global_load_lds_dwordx4 v[194:195], off
	s_add_i32 m0, s47, 0x2000
	s_nop 0
	v_lshl_add_u64 v[194:195], s[20:21], 0, v[96:97]
	s_add_u32 s20, s20, 0x40080
	v_lshl_add_u64 v[194:195], v[194:195], 0, s[30:31]
	s_addc_u32 s21, s21, 0
	v_mov_b32_e32 v96, v221
	s_add_i32 s47, s49, s59
	global_load_lds_dwordx4 v[194:195], off
	s_mov_b32 m0, s47
	s_nop 0
	global_load_lds_dwordx4 v96, s[20:21]
	v_mov_b32_e32 v96, v224
	s_add_i32 m0, s47, 0x2000
	s_nop 0
	global_load_lds_dwordx4 v96, s[20:21]
	v_mov_b32_e32 v96, v219
	s_mov_b32 m0, s66
	v_lshl_add_u64 v[194:195], s[4:5], 0, v[96:97]
	v_lshl_add_u64 v[194:195], v[194:195], 0, s[30:31]
	v_mov_b32_e32 v96, v222
	global_load_lds_dwordx4 v[194:195], off
	s_mov_b32 m0, s67
	v_lshl_add_u64 v[194:195], s[4:5], 0, v[96:97]
	v_lshl_add_u64 v[194:195], v[194:195], 0, s[30:31]
	global_load_lds_dwordx4 v[194:195], off
	s_add_i32 s29, s29, 2
	s_add_u32 s2, s2, 0x100
	s_addc_u32 s3, s3, 0
	s_add_u32 s1, s1, 0x100
	s_addc_u32 s26, s26, 0
	s_add_u32 s4, s2, 0x80
	s_addc_u32 s5, s3, 0
	s_add_i32 s47, 0, 0x10000
	s_cmp_eq_u32 s29, 12
	s_cselect_b32 s5, s51, s5
	s_cselect_b32 s4, s50, s4
	v_add_u32_e32 v96, s47, v226
	s_cselect_b32 s21, s53, s26
	s_cselect_b32 s20, s52, s1
	s_add_i32 s49, 0, 0x14000
	s_waitcnt vmcnt(8)
	s_waitcnt lgkmcnt(0)
	s_barrier
	s_waitcnt lgkmcnt(0)
	v_mfma_f32_16x16x32_bf16 v[60:63], v[118:121], v[162:165], v[60:63]
	v_mfma_f32_16x16x32_bf16 v[56:59], v[130:133], v[162:165], v[56:59]
	v_mfma_f32_16x16x32_bf16 v[44:47], v[118:121], v[170:173], v[44:47]
	v_mfma_f32_16x16x32_bf16 v[40:43], v[130:133], v[170:173], v[40:43]
	v_mfma_f32_16x16x32_bf16 v[20:23], v[118:121], v[178:181], v[20:23]
	v_mfma_f32_16x16x32_bf16 v[16:19], v[130:133], v[178:181], v[16:19]
	v_mfma_f32_16x16x32_bf16 v[4:7], v[118:121], v[186:189], v[4:7]
	v_mfma_f32_16x16x32_bf16 v[0:3], v[130:133], v[186:189], v[0:3]
	v_mfma_f32_16x16x32_bf16 v[60:63], v[126:129], v[166:169], v[60:63]
	v_mfma_f32_16x16x32_bf16 v[56:59], v[134:137], v[166:169], v[56:59]
	v_mfma_f32_16x16x32_bf16 v[44:47], v[126:129], v[174:177], v[44:47]
	v_mfma_f32_16x16x32_bf16 v[40:43], v[134:137], v[174:177], v[40:43]
	v_mfma_f32_16x16x32_bf16 v[20:23], v[126:129], v[182:185], v[20:23]
	v_mfma_f32_16x16x32_bf16 v[16:19], v[134:137], v[182:185], v[16:19]
	v_mfma_f32_16x16x32_bf16 v[4:7], v[126:129], v[190:193], v[4:7]
	v_mfma_f32_16x16x32_bf16 v[0:3], v[134:137], v[190:193], v[0:3]
	v_mfma_f32_16x16x32_bf16 v[52:55], v[142:145], v[162:165], v[52:55]
	v_mfma_f32_16x16x32_bf16 v[48:51], v[154:157], v[162:165], v[48:51]
	v_mfma_f32_16x16x32_bf16 v[36:39], v[142:145], v[170:173], v[36:39]
	v_mfma_f32_16x16x32_bf16 v[32:35], v[154:157], v[170:173], v[32:35]
	v_mfma_f32_16x16x32_bf16 v[28:31], v[142:145], v[178:181], v[28:31]
	v_mfma_f32_16x16x32_bf16 v[24:27], v[154:157], v[178:181], v[24:27]
	v_mfma_f32_16x16x32_bf16 v[12:15], v[142:145], v[186:189], v[12:15]
	v_mfma_f32_16x16x32_bf16 v[8:11], v[154:157], v[186:189], v[8:11]
	v_mfma_f32_16x16x32_bf16 v[52:55], v[150:153], v[166:169], v[52:55]
	v_mfma_f32_16x16x32_bf16 v[48:51], v[158:161], v[166:169], v[48:51]
	v_mfma_f32_16x16x32_bf16 v[36:39], v[150:153], v[174:177], v[36:39]
	v_mfma_f32_16x16x32_bf16 v[32:35], v[158:161], v[174:177], v[32:35]
	v_mfma_f32_16x16x32_bf16 v[28:31], v[150:153], v[182:185], v[28:31]
	v_mfma_f32_16x16x32_bf16 v[24:27], v[158:161], v[182:185], v[24:27]
	v_mfma_f32_16x16x32_bf16 v[12:15], v[150:153], v[190:193], v[12:15]
	v_mfma_f32_16x16x32_bf16 v[8:11], v[158:161], v[190:193], v[8:11]
	s_barrier
	s_cmp_gt_u32 s29, 13
	s_cbranch_scc0 .Lkrot_1075
	s_and_b64 vcc, exec, s[44:45]
	s_cbranch_vccz .LBB0_1078
	s_barrier

; #define PG8_STAGE(bufoff, gbase, voff) do { _Pragma("unroll") for (int _i = 0; _i < 2; ++_i) \
;         __builtin_amdgcn_global_load_lds((const __attribute__((address_space(1))) unsigned*)((const __attribute__((address_space(1))) char*)(gbase) + (unsigned)lnd_v((int)(voff)[_i])), (LAS unsigned*)(lds + (bufoff) + ldsw + _i * 8192), 16, 0, 0); } while (0)
; #define PG8_LDA(dst, b, h) do { _Pragma("unroll") for (int m = 0; m < 4; ++m) _Pragma("unroll") for (int k = 0; k < 2; ++k) dst[m][k] = *(const LAS bf16x8*)(lds + PG8_SA(b, h) + aoff + m * 2048 + k * 1024); } while (0)
; #define PG8_LDB(dst, b, h) do { _Pragma("unroll") for (int n = 0; n < 2; ++n) _Pragma("unroll") for (int k = 0; k < 2; ++k) dst[n][k] = *(const LAS bf16x8*)(lds + PG8_SB(b, h) + boff + n * 2048 + k * 1024); } while (0)
; #define PG8_MMA(ai, bj, At, Bt) do { __builtin_amdgcn_s_setprio(1); _Pragma("unroll") for (int m = 0; m < 4; ++m) _Pragma("unroll") for (int n = 0; n < 2; ++n) _Pragma("unroll") for (int k = 0; k < 2; ++k) \
;         acc[ai][bj][m][n] = __builtin_amdgcn_mfma_f32_16x16x32_bf16(Bt[n][k], At[m][k], acc[ai][bj][m][n], 0, 0, 0); __builtin_amdgcn_s_setprio(0); } while (0)
; #define PG8_WAIT_V(n) asm volatile("s_waitcnt vmcnt(" #n ")" ::: "memory")
; #define PG8_WAIT_L(n) asm volatile("s_waitcnt lgkmcnt(" #n ")" ::: "memory")
; #define PG8_BAR __builtin_amdgcn_s_barrier()
; #define PG8_SCHED __builtin_amdgcn_sched_barrier(0)
; template <class Desc, class Epi>
; __device__ __forceinline__ void gemm_phase(const int wv_, LAS unsigned char* lds, const Desc& d, const Epi& E) {
;     ...
;             PG8_LDB(B0, 0, 0); PG8_LDB(B1, 0, 1); PG8_SCHED; PG8_LDA(At, 0, 0); PG8_STAGE(PG8_SA(1, 1), a1, voffA1);
;             PG8_WAIT_V(8); PG8_WAIT_L(0); PG8_BAR; PG8_MMA(0, 0, At, B0); PG8_MMA(0, 1, At, B1); PG8_BAR; PG8_SCHED;
;             PG8_LDA(At, 0, 1); PG8_STAGE(PG8_SB(0, 0), b2, voffB); PG8_STAGE(PG8_SB(0, 1), b2 + hstepB, voffB); PG8_STAGE(PG8_SA(0, 0), a2, sA0);
;             PG8_WAIT_V(8); PG8_WAIT_L(0); PG8_BAR; PG8_MMA(1, 0, At, B0); PG8_MMA(1, 1, At, B1); PG8_BAR; PG8_SCHED;
.Lkrot_1161:
	ds_read_b128 v[130:133], v96
	ds_read_b128 v[134:137], v96 offset:1024
	ds_read_b128 v[138:141], v96 offset:2048
	ds_read_b128 v[142:145], v96 offset:3072
	v_add_u32_e32 v96, s68, v197
	ds_read_b128 v[146:149], v96
	ds_read_b128 v[150:153], v96 offset:1024
	ds_read_b128 v[154:157], v96 offset:2048
	ds_read_b128 v[158:161], v96 offset:3072
	v_mov_b32_e32 v96, v191
	ds_read_b128 v[162:165], v228
	ds_read_b128 v[166:169], v228 offset:1024
	ds_read_b128 v[170:173], v228 offset:2048
	ds_read_b128 v[174:177], v228 offset:3072
	ds_read_b128 v[178:181], v228 offset:4096
	ds_read_b128 v[182:185], v228 offset:5120
	ds_read_b128 v[186:189], v228 offset:6144
	ds_read_b128 v[230:233], v228 offset:7168
	s_add_i32 m0, s55, 0xc000
	s_nop 0
	global_load_lds_dwordx4 v96, s[2:3]
	v_mov_b32_e32 v96, v194
	s_add_i32 m0, s55, 0xe000
	s_nop 0
	global_load_lds_dwordx4 v96, s[2:3]
	s_waitcnt vmcnt(8)
	s_waitcnt lgkmcnt(0)
	s_barrier
	s_waitcnt lgkmcnt(0)
	v_mfma_f32_16x16x32_bf16 v[126:129], v[130:133], v[162:165], v[126:129]
	v_mfma_f32_16x16x32_bf16 v[122:125], v[138:141], v[162:165], v[122:125]
	v_mfma_f32_16x16x32_bf16 v[114:117], v[130:133], v[170:173], v[114:117]
	v_mfma_f32_16x16x32_bf16 v[106:109], v[138:141], v[170:173], v[106:109]
	v_mfma_f32_16x16x32_bf16 v[98:101], v[130:133], v[178:181], v[98:101]
	v_mfma_f32_16x16x32_bf16 v[88:91], v[138:141], v[178:181], v[88:91]
	v_mfma_f32_16x16x32_bf16 v[80:83], v[130:133], v[186:189], v[80:83]
	v_mfma_f32_16x16x32_bf16 v[72:75], v[138:141], v[186:189], v[72:75]
	v_mfma_f32_16x16x32_bf16 v[126:129], v[134:137], v[166:169], v[126:129]
	v_mfma_f32_16x16x32_bf16 v[122:125], v[142:145], v[166:169], v[122:125]
	v_mfma_f32_16x16x32_bf16 v[114:117], v[134:137], v[174:177], v[114:117]
	v_mfma_f32_16x16x32_bf16 v[106:109], v[142:145], v[174:177], v[106:109]
	v_mfma_f32_16x16x32_bf16 v[98:101], v[134:137], v[182:185], v[98:101]
	v_mfma_f32_16x16x32_bf16 v[88:91], v[142:145], v[182:185], v[88:91]
	v_mfma_f32_16x16x32_bf16 v[80:83], v[134:137], v[230:233], v[80:83]
	v_mfma_f32_16x16x32_bf16 v[72:75], v[142:145], v[230:233], v[72:75]
	v_mfma_f32_16x16x32_bf16 v[118:121], v[146:149], v[162:165], v[118:121]
	v_mfma_f32_16x16x32_bf16 v[110:113], v[154:157], v[162:165], v[110:113]
	v_mfma_f32_16x16x32_bf16 v[102:105], v[146:149], v[170:173], v[102:105]
	v_mfma_f32_16x16x32_bf16 v[92:95], v[154:157], v[170:173], v[92:95]
	v_mfma_f32_16x16x32_bf16 v[84:87], v[146:149], v[178:181], v[84:87]
	v_mfma_f32_16x16x32_bf16 v[76:79], v[154:157], v[178:181], v[76:79]
	v_mfma_f32_16x16x32_bf16 v[68:71], v[146:149], v[186:189], v[68:71]
	v_mfma_f32_16x16x32_bf16 v[64:67], v[154:157], v[186:189], v[64:67]
	v_mfma_f32_16x16x32_bf16 v[118:121], v[150:153], v[166:169], v[118:121]
	v_mfma_f32_16x16x32_bf16 v[110:113], v[158:161], v[166:169], v[110:113]
	v_mfma_f32_16x16x32_bf16 v[102:105], v[150:153], v[174:177], v[102:105]
	v_mfma_f32_16x16x32_bf16 v[92:95], v[158:161], v[174:177], v[92:95]
	v_mfma_f32_16x16x32_bf16 v[84:87], v[150:153], v[182:185], v[84:87]
	v_mfma_f32_16x16x32_bf16 v[76:79], v[158:161], v[182:185], v[76:79]
	v_mfma_f32_16x16x32_bf16 v[68:71], v[150:153], v[230:233], v[68:71]
	v_mfma_f32_16x16x32_bf16 v[64:67], v[158:161], v[230:233], v[64:67]
	s_barrier
	v_mov_b32_e32 v96, v192
	s_add_i32 s65, s65, s54
	ds_read_b128 v[162:165], v228 offset:16384
	ds_read_b128 v[166:169], v228 offset:17408
	ds_read_b128 v[170:173], v228 offset:18432
	ds_read_b128 v[174:177], v228 offset:19456
	ds_read_b128 v[178:181], v228 offset:20480
	ds_read_b128 v[182:185], v228 offset:21504
	ds_read_b128 v[186:189], v228 offset:22528
	ds_read_b128 v[230:233], v228 offset:23552
	s_mov_b32 m0, s65
	s_nop 0
	global_load_lds_dwordx4 v96, s[20:21]
	v_mov_b32_e32 v96, v195
	s_add_i32 m0, s65, 0x2000
	s_add_u32 s66, s20, 0x40000
	global_load_lds_dwordx4 v96, s[20:21]
	s_addc_u32 s67, s21, 0
	v_mov_b32_e32 v96, v192
	s_add_i32 s65, s68, s54
	s_mov_b32 m0, s65
	s_nop 0
	global_load_lds_dwordx4 v96, s[66:67]
	v_mov_b32_e32 v96, v195
	s_add_i32 m0, s65, 0x2000
	s_nop 0
	global_load_lds_dwordx4 v96, s[66:67]
	v_mov_b32_e32 v96, v190
	s_mov_b32 m0, s55
	s_nop 0
	global_load_lds_dwordx4 v96, s[4:5]
	v_mov_b32_e32 v96, v193
	s_mov_b32 m0, s56
	s_nop 0
	global_load_lds_dwordx4 v96, s[4:5]
	s_waitcnt vmcnt(8)
	s_waitcnt lgkmcnt(0)
	s_barrier
	s_waitcnt lgkmcnt(0)
	v_mfma_f32_16x16x32_bf16 v[60:63], v[130:133], v[162:165], v[60:63]
	v_mfma_f32_16x16x32_bf16 v[56:59], v[138:141], v[162:165], v[56:59]
	v_mfma_f32_16x16x32_bf16 v[40:43], v[130:133], v[170:173], v[40:43]
	v_mfma_f32_16x16x32_bf16 v[32:35], v[138:141], v[170:173], v[32:35]
	v_mfma_f32_16x16x32_bf16 v[16:19], v[130:133], v[178:181], v[16:19]
	v_mfma_f32_16x16x32_bf16 v[8:11], v[138:141], v[178:181], v[8:11]
	v_mfma_f32_16x16x32_bf16 v[4:7], v[130:133], v[186:189], v[4:7]
	v_mfma_f32_16x16x32_bf16 v[0:3], v[138:141], v[186:189], v[0:3]
	v_mfma_f32_16x16x32_bf16 v[60:63], v[134:137], v[166:169], v[60:63]
	v_mfma_f32_16x16x32_bf16 v[56:59], v[142:145], v[166:169], v[56:59]
	v_mfma_f32_16x16x32_bf16 v[40:43], v[134:137], v[174:177], v[40:43]
	v_mfma_f32_16x16x32_bf16 v[32:35], v[142:145], v[174:177], v[32:35]
	v_mfma_f32_16x16x32_bf16 v[16:19], v[134:137], v[182:185], v[16:19]
	v_mfma_f32_16x16x32_bf16 v[8:11], v[142:145], v[182:185], v[8:11]
	v_mfma_f32_16x16x32_bf16 v[4:7], v[134:137], v[230:233], v[4:7]
	v_mfma_f32_16x16x32_bf16 v[0:3], v[142:145], v[230:233], v[0:3]
	v_mfma_f32_16x16x32_bf16 v[44:47], v[146:149], v[162:165], v[44:47]
	v_mfma_f32_16x16x32_bf16 v[36:39], v[154:157], v[162:165], v[36:39]
	v_mfma_f32_16x16x32_bf16 v[20:23], v[146:149], v[170:173], v[20:23]
	v_mfma_f32_16x16x32_bf16 v[12:15], v[154:157], v[170:173], v[12:15]
	v_mfma_f32_16x16x32_bf16 v[52:55], v[146:149], v[178:181], v[52:55]
	v_mfma_f32_16x16x32_bf16 v[48:51], v[154:157], v[178:181], v[48:51]
	v_mfma_f32_16x16x32_bf16 v[28:31], v[146:149], v[186:189], v[28:31]
	v_mfma_f32_16x16x32_bf16 v[24:27], v[154:157], v[186:189], v[24:27]
	v_mfma_f32_16x16x32_bf16 v[44:47], v[150:153], v[166:169], v[44:47]
	v_mfma_f32_16x16x32_bf16 v[36:39], v[158:161], v[166:169], v[36:39]
	v_mfma_f32_16x16x32_bf16 v[20:23], v[150:153], v[174:177], v[20:23]
	v_mfma_f32_16x16x32_bf16 v[12:15], v[158:161], v[174:177], v[12:15]
	v_mfma_f32_16x16x32_bf16 v[52:55], v[150:153], v[182:185], v[52:55]
	v_mfma_f32_16x16x32_bf16 v[48:51], v[158:161], v[182:185], v[48:51]
	v_mfma_f32_16x16x32_bf16 v[28:31], v[150:153], v[230:233], v[28:31]
	v_mfma_f32_16x16x32_bf16 v[24:27], v[158:161], v[230:233], v[24:27]
	s_barrier
; #define PG8_STAGE(bufoff, gbase, voff) do { _Pragma("unroll") for (int _i = 0; _i < 2; ++_i) \
;         __builtin_amdgcn_global_load_lds((const __attribute__((address_space(1))) unsigned*)((const __attribute__((address_space(1))) char*)(gbase) + (unsigned)lnd_v((int)(voff)[_i])), (LAS unsigned*)(lds + (bufoff) + ldsw + _i * 8192), 16, 0, 0); } while (0)
; #define PG8_LDA(dst, b, h) do { _Pragma("unroll") for (int m = 0; m < 4; ++m) _Pragma("unroll") for (int k = 0; k < 2; ++k) dst[m][k] = *(const LAS bf16x8*)(lds + PG8_SA(b, h) + aoff + m * 2048 + k * 1024); } while (0)
; #define PG8_LDB(dst, b, h) do { _Pragma("unroll") for (int n = 0; n < 2; ++n) _Pragma("unroll") for (int k = 0; k < 2; ++k) dst[n][k] = *(const LAS bf16x8*)(lds + PG8_SB(b, h) + boff + n * 2048 + k * 1024); } while (0)
; #define PG8_MMA(ai, bj, At, Bt) do { __builtin_amdgcn_s_setprio(1); _Pragma("unroll") for (int m = 0; m < 4; ++m) _Pragma("unroll") for (int n = 0; n < 2; ++n) _Pragma("unroll") for (int k = 0; k < 2; ++k) \
;         acc[ai][bj][m][n] = __builtin_amdgcn_mfma_f32_16x16x32_bf16(Bt[n][k], At[m][k], acc[ai][bj][m][n], 0, 0, 0); __builtin_amdgcn_s_setprio(0); } while (0)
; #define PG8_WAIT_V(n) asm volatile("s_waitcnt vmcnt(" #n ")" ::: "memory")
; #define PG8_WAIT_L(n) asm volatile("s_waitcnt lgkmcnt(" #n ")" ::: "memory")
; #define PG8_BAR __builtin_amdgcn_s_barrier()
; #define PG8_SCHED __builtin_amdgcn_sched_barrier(0)
; template <class Desc, class Epi>
; __device__ __forceinline__ void gemm_phase(const int wv_, LAS unsigned char* lds, const Desc& d, const Epi& E) {
;     ...
;             PG8_LDB(B0, 1, 0); PG8_LDB(B1, 1, 1); PG8_SCHED; PG8_LDA(At, 1, 0); PG8_STAGE(PG8_SA(0, 1), a2, sA1);
;             PG8_WAIT_V(8); PG8_WAIT_L(0); PG8_BAR; PG8_MMA(0, 0, At, B0); PG8_MMA(0, 1, At, B1); PG8_BAR; PG8_SCHED;
	s_add_i32 s65, 0, 0x18000
	v_add_u32_e32 v96, s65, v197
	s_add_i32 s66, 0, 0x1c000
	ds_read_b128 v[130:133], v96
	ds_read_b128 v[134:137], v96 offset:1024
	ds_read_b128 v[138:141], v96 offset:2048
	ds_read_b128 v[142:145], v96 offset:3072
	v_add_u32_e32 v96, s66, v197
	ds_read_b128 v[146:149], v96
	ds_read_b128 v[150:153], v96 offset:1024
	ds_read_b128 v[154:157], v96 offset:2048
	ds_read_b128 v[158:161], v96 offset:3072
	v_mov_b32_e32 v96, v191
	s_mov_b32 m0, s57
	ds_read_b128 v[162:165], v228 offset:32768
	ds_read_b128 v[166:169], v228 offset:33792
	ds_read_b128 v[170:173], v228 offset:34816
	ds_read_b128 v[174:177], v228 offset:35840
	ds_read_b128 v[178:181], v228 offset:36864
	ds_read_b128 v[182:185], v228 offset:37888
	ds_read_b128 v[186:189], v228 offset:38912
	ds_read_b128 v[230:233], v228 offset:39936
	s_nop 0
	global_load_lds_dwordx4 v96, s[4:5]
	v_mov_b32_e32 v96, v194
	s_mov_b32 m0, s58
	s_nop 0
	global_load_lds_dwordx4 v96, s[4:5]
	s_waitcnt vmcnt(8)
	s_waitcnt lgkmcnt(0)
	s_barrier
	s_waitcnt lgkmcnt(0)
	v_mfma_f32_16x16x32_bf16 v[126:129], v[130:133], v[162:165], v[126:129]
	v_mfma_f32_16x16x32_bf16 v[122:125], v[138:141], v[162:165], v[122:125]
	v_mfma_f32_16x16x32_bf16 v[114:117], v[130:133], v[170:173], v[114:117]
	v_mfma_f32_16x16x32_bf16 v[106:109], v[138:141], v[170:173], v[106:109]
	v_mfma_f32_16x16x32_bf16 v[98:101], v[130:133], v[178:181], v[98:101]
	v_mfma_f32_16x16x32_bf16 v[88:91], v[138:141], v[178:181], v[88:91]
	v_mfma_f32_16x16x32_bf16 v[80:83], v[130:133], v[186:189], v[80:83]
	v_mfma_f32_16x16x32_bf16 v[72:75], v[138:141], v[186:189], v[72:75]
	v_mfma_f32_16x16x32_bf16 v[126:129], v[134:137], v[166:169], v[126:129]
	v_mfma_f32_16x16x32_bf16 v[122:125], v[142:145], v[166:169], v[122:125]
	v_mfma_f32_16x16x32_bf16 v[114:117], v[134:137], v[174:177], v[114:117]
	v_mfma_f32_16x16x32_bf16 v[106:109], v[142:145], v[174:177], v[106:109]
	v_mfma_f32_16x16x32_bf16 v[98:101], v[134:137], v[182:185], v[98:101]
	v_mfma_f32_16x16x32_bf16 v[88:91], v[142:145], v[182:185], v[88:91]
	v_mfma_f32_16x16x32_bf16 v[80:83], v[134:137], v[230:233], v[80:83]
	v_mfma_f32_16x16x32_bf16 v[72:75], v[142:145], v[230:233], v[72:75]
	v_mfma_f32_16x16x32_bf16 v[118:121], v[146:149], v[162:165], v[118:121]
	v_mfma_f32_16x16x32_bf16 v[110:113], v[154:157], v[162:165], v[110:113]
	v_mfma_f32_16x16x32_bf16 v[102:105], v[146:149], v[170:173], v[102:105]
	v_mfma_f32_16x16x32_bf16 v[92:95], v[154:157], v[170:173], v[92:95]
	v_mfma_f32_16x16x32_bf16 v[84:87], v[146:149], v[178:181], v[84:87]
	v_mfma_f32_16x16x32_bf16 v[76:79], v[154:157], v[178:181], v[76:79]
	v_mfma_f32_16x16x32_bf16 v[68:71], v[146:149], v[186:189], v[68:71]
	v_mfma_f32_16x16x32_bf16 v[64:67], v[154:157], v[186:189], v[64:67]
	v_mfma_f32_16x16x32_bf16 v[118:121], v[150:153], v[166:169], v[118:121]
	v_mfma_f32_16x16x32_bf16 v[110:113], v[158:161], v[166:169], v[110:113]
	v_mfma_f32_16x16x32_bf16 v[102:105], v[150:153], v[174:177], v[102:105]
	v_mfma_f32_16x16x32_bf16 v[92:95], v[158:161], v[174:177], v[92:95]
	v_mfma_f32_16x16x32_bf16 v[84:87], v[150:153], v[182:185], v[84:87]
	v_mfma_f32_16x16x32_bf16 v[76:79], v[158:161], v[182:185], v[76:79]
	v_mfma_f32_16x16x32_bf16 v[68:71], v[150:153], v[230:233], v[68:71]
	v_mfma_f32_16x16x32_bf16 v[64:67], v[158:161], v[230:233], v[64:67]
	s_barrier
; #define PG8_STAGE(bufoff, gbase, voff) do { _Pragma("unroll") for (int _i = 0; _i < 2; ++_i) \
;         __builtin_amdgcn_global_load_lds((const __attribute__((address_space(1))) unsigned*)((const __attribute__((address_space(1))) char*)(gbase) + (unsigned)lnd_v((int)(voff)[_i])), (LAS unsigned*)(lds + (bufoff) + ldsw + _i * 8192), 16, 0, 0); } while (0)
; #define PG8_LDA(dst, b, h) do { _Pragma("unroll") for (int m = 0; m < 4; ++m) _Pragma("unroll") for (int k = 0; k < 2; ++k) dst[m][k] = *(const LAS bf16x8*)(lds + PG8_SA(b, h) + aoff + m * 2048 + k * 1024); } while (0)
; #define PG8_MMA(ai, bj, At, Bt) do { __builtin_amdgcn_s_setprio(1); _Pragma("unroll") for (int m = 0; m < 4; ++m) _Pragma("unroll") for (int n = 0; n < 2; ++n) _Pragma("unroll") for (int k = 0; k < 2; ++k) \
;         acc[ai][bj][m][n] = __builtin_amdgcn_mfma_f32_16x16x32_bf16(Bt[n][k], At[m][k], acc[ai][bj][m][n], 0, 0, 0); __builtin_amdgcn_s_setprio(0); } while (0)
; #define PG8_WAIT_V(n) asm volatile("s_waitcnt vmcnt(" #n ")" ::: "memory")
; #define PG8_WAIT_L(n) asm volatile("s_waitcnt lgkmcnt(" #n ")" ::: "memory")
; #define PG8_BAR __builtin_amdgcn_s_barrier()
; #define PG8_SCHED __builtin_amdgcn_sched_barrier(0)
; template <class Desc, class Epi>
; __device__ __forceinline__ void gemm_phase(const int wv_, LAS unsigned char* lds, const Desc& d, const Epi& E) {
;     ...
;         for (int t = 0; t < nt; t += 2) {
;             const bool last = (t == nt - 2);
;             unsigned sA0[2], sA1[2];
;             if constexpr (Desc::GATHER) { sA0[0] = last ? voffAn[0] : voffA[0]; sA0[1] = last ? voffAn[1] : voffA[1]; sA1[0] = last ? voffAn1[0] : voffA1[0]; sA1[1] = last ? voffAn1[1] : voffA1[1]; }
;             else { sA0[0] = voffA[0]; sA0[1] = voffA[1]; sA1[0] = voffA1[0]; sA1[1] = voffA1[1]; }
;             const char* a1 = cA + (size_t)(t + 1) * kstep;
;             const char* a2 = last ? nA : cA + (size_t)(t + 2) * kstep; const char* b2 = last ? nB : cB + (size_t)(t + 2) * kstep;
;     ...
;             PG8_LDA(At, 1, 1); PG8_STAGE(PG8_SB(1, 0), b3, voffB); PG8_STAGE(PG8_SB(1, 1), b3 + hstepB, voffB); PG8_STAGE(PG8_SA(1, 0), a3, sA0);
;             PG8_WAIT_V(8); PG8_WAIT_L(0); PG8_BAR; PG8_MMA(1, 0, At, B0); PG8_MMA(1, 1, At, B1); PG8_BAR; PG8_SCHED;
;         }
	v_mov_b32_e32 v96, v192
	ds_read_b128 v[162:165], v228 offset:49152
	ds_read_b128 v[166:169], v228 offset:50176
	ds_read_b128 v[170:173], v228 offset:51200
	ds_read_b128 v[174:177], v228 offset:52224
	ds_read_b128 v[178:181], v228 offset:53248
	ds_read_b128 v[182:185], v228 offset:54272
	ds_read_b128 v[186:189], v228 offset:55296
	ds_read_b128 v[230:233], v228 offset:56320
	s_add_i32 s65, s65, s54
	v_lshl_add_u64 v[234:235], s[20:21], 0, v[96:97]
	v_lshl_add_u64 v[234:235], v[234:235], 0, s[30:31]
	s_mov_b32 m0, s65
	v_mov_b32_e32 v96, v195
	global_load_lds_dwordx4 v[234:235], off
	s_add_i32 m0, s65, 0x2000
	s_nop 0
	v_lshl_add_u64 v[234:235], s[20:21], 0, v[96:97]
	s_add_u32 s20, s20, 0x40080
	v_lshl_add_u64 v[234:235], v[234:235], 0, s[30:31]
	s_addc_u32 s21, s21, 0
	v_mov_b32_e32 v96, v192
	s_add_i32 s65, s66, s54
	global_load_lds_dwordx4 v[234:235], off
	s_mov_b32 m0, s65
	s_nop 0
	global_load_lds_dwordx4 v96, s[20:21]
	v_mov_b32_e32 v96, v195
	s_add_i32 m0, s65, 0x2000
	s_nop 0
	global_load_lds_dwordx4 v96, s[20:21]
	v_mov_b32_e32 v96, v190
	s_mov_b32 m0, s59
	v_lshl_add_u64 v[234:235], s[4:5], 0, v[96:97]
	v_lshl_add_u64 v[234:235], v[234:235], 0, s[30:31]
	v_mov_b32_e32 v96, v193
	global_load_lds_dwordx4 v[234:235], off
	s_mov_b32 m0, s60
	v_lshl_add_u64 v[234:235], s[4:5], 0, v[96:97]
	v_lshl_add_u64 v[234:235], v[234:235], 0, s[30:31]
	global_load_lds_dwordx4 v[234:235], off
	s_add_i32 s45, s45, 2
	s_add_u32 s2, s2, 0x100
	s_addc_u32 s3, s3, 0
	s_add_u32 s1, s1, 0x100
	s_addc_u32 s29, s29, 0
	s_add_u32 s4, s2, 0x80
	s_addc_u32 s5, s3, 0
	s_add_i32 s65, 0, 0x10000
	s_cmp_eq_u32 s45, 12
	s_cselect_b32 s5, s47, s5
	s_cselect_b32 s4, s46, s4
	v_add_u32_e32 v96, s65, v197
	s_cselect_b32 s21, s49, s29
	s_cselect_b32 s20, s48, s1
	s_add_i32 s68, 0, 0x14000
	s_waitcnt vmcnt(8)
	s_waitcnt lgkmcnt(0)
	s_barrier
	s_waitcnt lgkmcnt(0)
	v_mfma_f32_16x16x32_bf16 v[60:63], v[130:133], v[162:165], v[60:63]
	v_mfma_f32_16x16x32_bf16 v[56:59], v[138:141], v[162:165], v[56:59]
	v_mfma_f32_16x16x32_bf16 v[40:43], v[130:133], v[170:173], v[40:43]
	v_mfma_f32_16x16x32_bf16 v[32:35], v[138:141], v[170:173], v[32:35]
	v_mfma_f32_16x16x32_bf16 v[16:19], v[130:133], v[178:181], v[16:19]
	v_mfma_f32_16x16x32_bf16 v[8:11], v[138:141], v[178:181], v[8:11]
	v_mfma_f32_16x16x32_bf16 v[4:7], v[130:133], v[186:189], v[4:7]
	v_mfma_f32_16x16x32_bf16 v[0:3], v[138:141], v[186:189], v[0:3]
	v_mfma_f32_16x16x32_bf16 v[60:63], v[134:137], v[166:169], v[60:63]
	v_mfma_f32_16x16x32_bf16 v[56:59], v[142:145], v[166:169], v[56:59]
	v_mfma_f32_16x16x32_bf16 v[40:43], v[134:137], v[174:177], v[40:43]
	v_mfma_f32_16x16x32_bf16 v[32:35], v[142:145], v[174:177], v[32:35]
	v_mfma_f32_16x16x32_bf16 v[16:19], v[134:137], v[182:185], v[16:19]
	v_mfma_f32_16x16x32_bf16 v[8:11], v[142:145], v[182:185], v[8:11]
	v_mfma_f32_16x16x32_bf16 v[4:7], v[134:137], v[230:233], v[4:7]
	v_mfma_f32_16x16x32_bf16 v[0:3], v[142:145], v[230:233], v[0:3]
	v_mfma_f32_16x16x32_bf16 v[44:47], v[146:149], v[162:165], v[44:47]
	v_mfma_f32_16x16x32_bf16 v[36:39], v[154:157], v[162:165], v[36:39]
	v_mfma_f32_16x16x32_bf16 v[20:23], v[146:149], v[170:173], v[20:23]
	v_mfma_f32_16x16x32_bf16 v[12:15], v[154:157], v[170:173], v[12:15]
	v_mfma_f32_16x16x32_bf16 v[52:55], v[146:149], v[178:181], v[52:55]
	v_mfma_f32_16x16x32_bf16 v[48:51], v[154:157], v[178:181], v[48:51]
	v_mfma_f32_16x16x32_bf16 v[28:31], v[146:149], v[186:189], v[28:31]
	v_mfma_f32_16x16x32_bf16 v[24:27], v[154:157], v[186:189], v[24:27]
	v_mfma_f32_16x16x32_bf16 v[44:47], v[150:153], v[166:169], v[44:47]
	v_mfma_f32_16x16x32_bf16 v[36:39], v[158:161], v[166:169], v[36:39]
	v_mfma_f32_16x16x32_bf16 v[20:23], v[150:153], v[174:177], v[20:23]
	v_mfma_f32_16x16x32_bf16 v[12:15], v[158:161], v[174:177], v[12:15]
	v_mfma_f32_16x16x32_bf16 v[52:55], v[150:153], v[182:185], v[52:55]
	v_mfma_f32_16x16x32_bf16 v[48:51], v[158:161], v[182:185], v[48:51]
	v_mfma_f32_16x16x32_bf16 v[28:31], v[150:153], v[230:233], v[28:31]
	v_mfma_f32_16x16x32_bf16 v[24:27], v[158:161], v[230:233], v[24:27]
	s_barrier
	s_cmp_gt_u32 s45, 13
	s_cbranch_scc0 .Lkrot_1161
	s_and_b64 vcc, exec, s[42:43]
	s_cbranch_vccz .LBB0_1164
	s_barrier

; #define PG8_STAGE(bufoff, gbase, voff) do { _Pragma("unroll") for (int _i = 0; _i < 2; ++_i) \
;         __builtin_amdgcn_global_load_lds((const __attribute__((address_space(1))) unsigned*)((const __attribute__((address_space(1))) char*)(gbase) + (unsigned)lnd_v((int)(voff)[_i])), (LAS unsigned*)(lds + (bufoff) + ldsw + _i * 8192), 16, 0, 0); } while (0)
; #define PG8_LDA(dst, b, h) do { _Pragma("unroll") for (int m = 0; m < 4; ++m) _Pragma("unroll") for (int k = 0; k < 2; ++k) dst[m][k] = *(const LAS bf16x8*)(lds + PG8_SA(b, h) + aoff + m * 2048 + k * 1024); } while (0)
; #define PG8_LDB(dst, b, h) do { _Pragma("unroll") for (int n = 0; n < 2; ++n) _Pragma("unroll") for (int k = 0; k < 2; ++k) dst[n][k] = *(const LAS bf16x8*)(lds + PG8_SB(b, h) + boff + n * 2048 + k * 1024); } while (0)
; #define PG8_MMA(ai, bj, At, Bt) do { __builtin_amdgcn_s_setprio(1); _Pragma("unroll") for (int m = 0; m < 4; ++m) _Pragma("unroll") for (int n = 0; n < 2; ++n) _Pragma("unroll") for (int k = 0; k < 2; ++k) \
;         acc[ai][bj][m][n] = __builtin_amdgcn_mfma_f32_16x16x32_bf16(Bt[n][k], At[m][k], acc[ai][bj][m][n], 0, 0, 0); __builtin_amdgcn_s_setprio(0); } while (0)
; #define PG8_WAIT_V(n) asm volatile("s_waitcnt vmcnt(" #n ")" ::: "memory")
; #define PG8_WAIT_L(n) asm volatile("s_waitcnt lgkmcnt(" #n ")" ::: "memory")
; #define PG8_BAR __builtin_amdgcn_s_barrier()
; #define PG8_SCHED __builtin_amdgcn_sched_barrier(0)
; template <class Desc, class Epi>
; __device__ __forceinline__ void gemm_phase(const int wv_, LAS unsigned char* lds, const Desc& d, const Epi& E) {
;     ...
;             PG8_LDB(B0, 0, 0); PG8_LDB(B1, 0, 1); PG8_SCHED; PG8_LDA(At, 0, 0); PG8_STAGE(PG8_SA(1, 1), a1, voffA1);
;             PG8_WAIT_V(8); PG8_WAIT_L(0); PG8_BAR; PG8_MMA(0, 0, At, B0); PG8_MMA(0, 1, At, B1); PG8_BAR; PG8_SCHED;
;             PG8_LDA(At, 0, 1); PG8_STAGE(PG8_SB(0, 0), b2, voffB); PG8_STAGE(PG8_SB(0, 1), b2 + hstepB, voffB); PG8_STAGE(PG8_SA(0, 0), a2, sA0);
;             PG8_WAIT_V(8); PG8_WAIT_L(0); PG8_BAR; PG8_MMA(1, 0, At, B0); PG8_MMA(1, 1, At, B1); PG8_BAR; PG8_SCHED;
.Lkrot_1262:
	ds_read_b128 v[130:133], v96
	ds_read_b128 v[134:137], v96 offset:1024
	ds_read_b128 v[138:141], v96 offset:2048
	ds_read_b128 v[142:145], v96 offset:3072
	v_add_u32_e32 v96, s64, v213
	ds_read_b128 v[146:149], v96
	ds_read_b128 v[150:153], v96 offset:1024
	ds_read_b128 v[154:157], v96 offset:2048
	ds_read_b128 v[158:161], v96 offset:3072
	v_mov_b32_e32 v96, v207
	ds_read_b128 v[162:165], v221
	ds_read_b128 v[166:169], v221 offset:1024
	ds_read_b128 v[170:173], v221 offset:2048
	ds_read_b128 v[174:177], v221 offset:3072
	ds_read_b128 v[178:181], v221 offset:4096
	ds_read_b128 v[182:185], v221 offset:5120
	ds_read_b128 v[186:189], v221 offset:6144
	ds_read_b128 v[190:193], v221 offset:7168
	s_add_i32 m0, s53, 0xc000
	s_nop 0
	global_load_lds_dwordx4 v96, s[2:3]
	v_mov_b32_e32 v96, v210
	s_add_i32 m0, s53, 0xe000
	s_nop 0
	global_load_lds_dwordx4 v96, s[2:3]
	s_waitcnt vmcnt(8)
	s_waitcnt lgkmcnt(0)
	s_barrier
	s_waitcnt lgkmcnt(0)
	v_mfma_f32_16x16x32_bf16 v[126:129], v[130:133], v[162:165], v[126:129]
	v_mfma_f32_16x16x32_bf16 v[122:125], v[138:141], v[162:165], v[122:125]
	v_mfma_f32_16x16x32_bf16 v[110:113], v[130:133], v[170:173], v[110:113]
	v_mfma_f32_16x16x32_bf16 v[106:109], v[138:141], v[170:173], v[106:109]
	v_mfma_f32_16x16x32_bf16 v[92:95], v[130:133], v[178:181], v[92:95]
	v_mfma_f32_16x16x32_bf16 v[88:91], v[138:141], v[178:181], v[88:91]
	v_mfma_f32_16x16x32_bf16 v[76:79], v[130:133], v[186:189], v[76:79]
	v_mfma_f32_16x16x32_bf16 v[72:75], v[138:141], v[186:189], v[72:75]
	v_mfma_f32_16x16x32_bf16 v[126:129], v[134:137], v[166:169], v[126:129]
	v_mfma_f32_16x16x32_bf16 v[122:125], v[142:145], v[166:169], v[122:125]
	v_mfma_f32_16x16x32_bf16 v[110:113], v[134:137], v[174:177], v[110:113]
	v_mfma_f32_16x16x32_bf16 v[106:109], v[142:145], v[174:177], v[106:109]
	v_mfma_f32_16x16x32_bf16 v[92:95], v[134:137], v[182:185], v[92:95]
	v_mfma_f32_16x16x32_bf16 v[88:91], v[142:145], v[182:185], v[88:91]
	v_mfma_f32_16x16x32_bf16 v[76:79], v[134:137], v[190:193], v[76:79]
	v_mfma_f32_16x16x32_bf16 v[72:75], v[142:145], v[190:193], v[72:75]
	v_mfma_f32_16x16x32_bf16 v[118:121], v[146:149], v[162:165], v[118:121]
	v_mfma_f32_16x16x32_bf16 v[114:117], v[154:157], v[162:165], v[114:117]
	v_mfma_f32_16x16x32_bf16 v[102:105], v[146:149], v[170:173], v[102:105]
	v_mfma_f32_16x16x32_bf16 v[98:101], v[154:157], v[170:173], v[98:101]
	v_mfma_f32_16x16x32_bf16 v[84:87], v[146:149], v[178:181], v[84:87]
	v_mfma_f32_16x16x32_bf16 v[80:83], v[154:157], v[178:181], v[80:83]
	v_mfma_f32_16x16x32_bf16 v[68:71], v[146:149], v[186:189], v[68:71]
	v_mfma_f32_16x16x32_bf16 v[64:67], v[154:157], v[186:189], v[64:67]
	v_mfma_f32_16x16x32_bf16 v[118:121], v[150:153], v[166:169], v[118:121]
	v_mfma_f32_16x16x32_bf16 v[114:117], v[158:161], v[166:169], v[114:117]
	v_mfma_f32_16x16x32_bf16 v[102:105], v[150:153], v[174:177], v[102:105]
	v_mfma_f32_16x16x32_bf16 v[98:101], v[158:161], v[174:177], v[98:101]
	v_mfma_f32_16x16x32_bf16 v[84:87], v[150:153], v[182:185], v[84:87]
	v_mfma_f32_16x16x32_bf16 v[80:83], v[158:161], v[182:185], v[80:83]
	v_mfma_f32_16x16x32_bf16 v[68:71], v[150:153], v[190:193], v[68:71]
	v_mfma_f32_16x16x32_bf16 v[64:67], v[158:161], v[190:193], v[64:67]
	s_barrier
	v_mov_b32_e32 v96, v208
	s_add_i32 s62, s62, s52
	ds_read_b128 v[162:165], v221 offset:16384
	ds_read_b128 v[166:169], v221 offset:17408
	ds_read_b128 v[170:173], v221 offset:18432
	ds_read_b128 v[174:177], v221 offset:19456
	ds_read_b128 v[178:181], v221 offset:20480
	ds_read_b128 v[182:185], v221 offset:21504
	ds_read_b128 v[186:189], v221 offset:22528
	ds_read_b128 v[190:193], v221 offset:23552
	s_mov_b32 m0, s62
	s_nop 0
	global_load_lds_dwordx4 v96, s[20:21]
	v_mov_b32_e32 v96, v211
	s_add_i32 m0, s62, 0x2000
	s_add_u32 s62, s20, 0x40000
	global_load_lds_dwordx4 v96, s[20:21]
	s_addc_u32 s63, s21, 0
	v_mov_b32_e32 v96, v208
	s_add_i32 s64, s64, s52
	s_mov_b32 m0, s64
	s_nop 0
	global_load_lds_dwordx4 v96, s[62:63]
	v_mov_b32_e32 v96, v211
	s_add_i32 m0, s64, 0x2000
	s_nop 0
	global_load_lds_dwordx4 v96, s[62:63]
	v_mov_b32_e32 v96, v206
	s_mov_b32 m0, s53
	s_nop 0
	global_load_lds_dwordx4 v96, s[4:5]
	v_mov_b32_e32 v96, v209
	s_mov_b32 m0, s54
	s_nop 0
	global_load_lds_dwordx4 v96, s[4:5]
	s_waitcnt vmcnt(8)
	s_waitcnt lgkmcnt(0)
	s_barrier
	s_waitcnt lgkmcnt(0)
	v_mfma_f32_16x16x32_bf16 v[60:63], v[130:133], v[162:165], v[60:63]
	v_mfma_f32_16x16x32_bf16 v[56:59], v[138:141], v[162:165], v[56:59]
	v_mfma_f32_16x16x32_bf16 v[44:47], v[130:133], v[170:173], v[44:47]
	v_mfma_f32_16x16x32_bf16 v[40:43], v[138:141], v[170:173], v[40:43]
	v_mfma_f32_16x16x32_bf16 v[24:27], v[130:133], v[178:181], v[24:27]
	v_mfma_f32_16x16x32_bf16 v[16:19], v[138:141], v[178:181], v[16:19]
	v_mfma_f32_16x16x32_bf16 v[4:7], v[130:133], v[186:189], v[4:7]
	v_mfma_f32_16x16x32_bf16 v[0:3], v[138:141], v[186:189], v[0:3]
	v_mfma_f32_16x16x32_bf16 v[60:63], v[134:137], v[166:169], v[60:63]
	v_mfma_f32_16x16x32_bf16 v[56:59], v[142:145], v[166:169], v[56:59]
	v_mfma_f32_16x16x32_bf16 v[44:47], v[134:137], v[174:177], v[44:47]
	v_mfma_f32_16x16x32_bf16 v[40:43], v[142:145], v[174:177], v[40:43]
	v_mfma_f32_16x16x32_bf16 v[24:27], v[134:137], v[182:185], v[24:27]
	v_mfma_f32_16x16x32_bf16 v[16:19], v[142:145], v[182:185], v[16:19]
	v_mfma_f32_16x16x32_bf16 v[4:7], v[134:137], v[190:193], v[4:7]
	v_mfma_f32_16x16x32_bf16 v[0:3], v[142:145], v[190:193], v[0:3]
	v_mfma_f32_16x16x32_bf16 v[52:55], v[146:149], v[162:165], v[52:55]
	v_mfma_f32_16x16x32_bf16 v[48:51], v[154:157], v[162:165], v[48:51]
	v_mfma_f32_16x16x32_bf16 v[28:31], v[146:149], v[170:173], v[28:31]
	v_mfma_f32_16x16x32_bf16 v[20:23], v[154:157], v[170:173], v[20:23]
	v_mfma_f32_16x16x32_bf16 v[36:39], v[146:149], v[178:181], v[36:39]
	v_mfma_f32_16x16x32_bf16 v[32:35], v[154:157], v[178:181], v[32:35]
	v_mfma_f32_16x16x32_bf16 v[12:15], v[146:149], v[186:189], v[12:15]
	v_mfma_f32_16x16x32_bf16 v[8:11], v[154:157], v[186:189], v[8:11]
	v_mfma_f32_16x16x32_bf16 v[52:55], v[150:153], v[166:169], v[52:55]
	v_mfma_f32_16x16x32_bf16 v[48:51], v[158:161], v[166:169], v[48:51]
	v_mfma_f32_16x16x32_bf16 v[28:31], v[150:153], v[174:177], v[28:31]
	v_mfma_f32_16x16x32_bf16 v[20:23], v[158:161], v[174:177], v[20:23]
	v_mfma_f32_16x16x32_bf16 v[36:39], v[150:153], v[182:185], v[36:39]
	v_mfma_f32_16x16x32_bf16 v[32:35], v[158:161], v[182:185], v[32:35]
	v_mfma_f32_16x16x32_bf16 v[12:15], v[150:153], v[190:193], v[12:15]
	v_mfma_f32_16x16x32_bf16 v[8:11], v[158:161], v[190:193], v[8:11]
	s_barrier
; #define PG8_STAGE(bufoff, gbase, voff) do { _Pragma("unroll") for (int _i = 0; _i < 2; ++_i) \
;         __builtin_amdgcn_global_load_lds((const __attribute__((address_space(1))) unsigned*)((const __attribute__((address_space(1))) char*)(gbase) + (unsigned)lnd_v((int)(voff)[_i])), (LAS unsigned*)(lds + (bufoff) + ldsw + _i * 8192), 16, 0, 0); } while (0)
; #define PG8_LDA(dst, b, h) do { _Pragma("unroll") for (int m = 0; m < 4; ++m) _Pragma("unroll") for (int k = 0; k < 2; ++k) dst[m][k] = *(const LAS bf16x8*)(lds + PG8_SA(b, h) + aoff + m * 2048 + k * 1024); } while (0)
; #define PG8_LDB(dst, b, h) do { _Pragma("unroll") for (int n = 0; n < 2; ++n) _Pragma("unroll") for (int k = 0; k < 2; ++k) dst[n][k] = *(const LAS bf16x8*)(lds + PG8_SB(b, h) + boff + n * 2048 + k * 1024); } while (0)
; #define PG8_MMA(ai, bj, At, Bt) do { __builtin_amdgcn_s_setprio(1); _Pragma("unroll") for (int m = 0; m < 4; ++m) _Pragma("unroll") for (int n = 0; n < 2; ++n) _Pragma("unroll") for (int k = 0; k < 2; ++k) \
;         acc[ai][bj][m][n] = __builtin_amdgcn_mfma_f32_16x16x32_bf16(Bt[n][k], At[m][k], acc[ai][bj][m][n], 0, 0, 0); __builtin_amdgcn_s_setprio(0); } while (0)
; #define PG8_WAIT_V(n) asm volatile("s_waitcnt vmcnt(" #n ")" ::: "memory")
; #define PG8_WAIT_L(n) asm volatile("s_waitcnt lgkmcnt(" #n ")" ::: "memory")
; #define PG8_BAR __builtin_amdgcn_s_barrier()
; #define PG8_SCHED __builtin_amdgcn_sched_barrier(0)
; template <class Desc, class Epi>
; __device__ __forceinline__ void gemm_phase(const int wv_, LAS unsigned char* lds, const Desc& d, const Epi& E) {
;     ...
;             PG8_LDB(B0, 1, 0); PG8_LDB(B1, 1, 1); PG8_SCHED; PG8_LDA(At, 1, 0); PG8_STAGE(PG8_SA(0, 1), a2, sA1);
;             PG8_WAIT_V(8); PG8_WAIT_L(0); PG8_BAR; PG8_MMA(0, 0, At, B0); PG8_MMA(0, 1, At, B1); PG8_BAR; PG8_SCHED;
	s_add_i32 s62, 0, 0x18000
	v_add_u32_e32 v96, s62, v213
	s_add_i32 s63, 0, 0x1c000
	ds_read_b128 v[130:133], v96
	ds_read_b128 v[134:137], v96 offset:1024
	ds_read_b128 v[138:141], v96 offset:2048
	ds_read_b128 v[142:145], v96 offset:3072
	v_add_u32_e32 v96, s63, v213
	ds_read_b128 v[146:149], v96
	ds_read_b128 v[150:153], v96 offset:1024
	ds_read_b128 v[154:157], v96 offset:2048
	ds_read_b128 v[158:161], v96 offset:3072
	v_mov_b32_e32 v96, v207
	s_mov_b32 m0, s55
	ds_read_b128 v[162:165], v221 offset:32768
	ds_read_b128 v[166:169], v221 offset:33792
	ds_read_b128 v[170:173], v221 offset:34816
	ds_read_b128 v[174:177], v221 offset:35840
	ds_read_b128 v[178:181], v221 offset:36864
	ds_read_b128 v[182:185], v221 offset:37888
	ds_read_b128 v[186:189], v221 offset:38912
	ds_read_b128 v[190:193], v221 offset:39936
	s_nop 0
	global_load_lds_dwordx4 v96, s[4:5]
	v_mov_b32_e32 v96, v210
	s_mov_b32 m0, s56
	s_nop 0
	global_load_lds_dwordx4 v96, s[4:5]
	s_waitcnt vmcnt(8)
	s_waitcnt lgkmcnt(0)
	s_barrier
	s_waitcnt lgkmcnt(0)
	v_mfma_f32_16x16x32_bf16 v[126:129], v[130:133], v[162:165], v[126:129]
	v_mfma_f32_16x16x32_bf16 v[122:125], v[138:141], v[162:165], v[122:125]
	v_mfma_f32_16x16x32_bf16 v[110:113], v[130:133], v[170:173], v[110:113]
	v_mfma_f32_16x16x32_bf16 v[106:109], v[138:141], v[170:173], v[106:109]
	v_mfma_f32_16x16x32_bf16 v[92:95], v[130:133], v[178:181], v[92:95]
	v_mfma_f32_16x16x32_bf16 v[88:91], v[138:141], v[178:181], v[88:91]
	v_mfma_f32_16x16x32_bf16 v[76:79], v[130:133], v[186:189], v[76:79]
	v_mfma_f32_16x16x32_bf16 v[72:75], v[138:141], v[186:189], v[72:75]
	v_mfma_f32_16x16x32_bf16 v[126:129], v[134:137], v[166:169], v[126:129]
	v_mfma_f32_16x16x32_bf16 v[122:125], v[142:145], v[166:169], v[122:125]
	v_mfma_f32_16x16x32_bf16 v[110:113], v[134:137], v[174:177], v[110:113]
	v_mfma_f32_16x16x32_bf16 v[106:109], v[142:145], v[174:177], v[106:109]
	v_mfma_f32_16x16x32_bf16 v[92:95], v[134:137], v[182:185], v[92:95]
	v_mfma_f32_16x16x32_bf16 v[88:91], v[142:145], v[182:185], v[88:91]
	v_mfma_f32_16x16x32_bf16 v[76:79], v[134:137], v[190:193], v[76:79]
	v_mfma_f32_16x16x32_bf16 v[72:75], v[142:145], v[190:193], v[72:75]
	v_mfma_f32_16x16x32_bf16 v[118:121], v[146:149], v[162:165], v[118:121]
	v_mfma_f32_16x16x32_bf16 v[114:117], v[154:157], v[162:165], v[114:117]
	v_mfma_f32_16x16x32_bf16 v[102:105], v[146:149], v[170:173], v[102:105]
	v_mfma_f32_16x16x32_bf16 v[98:101], v[154:157], v[170:173], v[98:101]
	v_mfma_f32_16x16x32_bf16 v[84:87], v[146:149], v[178:181], v[84:87]
	v_mfma_f32_16x16x32_bf16 v[80:83], v[154:157], v[178:181], v[80:83]
	v_mfma_f32_16x16x32_bf16 v[68:71], v[146:149], v[186:189], v[68:71]
	v_mfma_f32_16x16x32_bf16 v[64:67], v[154:157], v[186:189], v[64:67]
	v_mfma_f32_16x16x32_bf16 v[118:121], v[150:153], v[166:169], v[118:121]
	v_mfma_f32_16x16x32_bf16 v[114:117], v[158:161], v[166:169], v[114:117]
	v_mfma_f32_16x16x32_bf16 v[102:105], v[150:153], v[174:177], v[102:105]
	v_mfma_f32_16x16x32_bf16 v[98:101], v[158:161], v[174:177], v[98:101]
	v_mfma_f32_16x16x32_bf16 v[84:87], v[150:153], v[182:185], v[84:87]
	v_mfma_f32_16x16x32_bf16 v[80:83], v[158:161], v[182:185], v[80:83]
	v_mfma_f32_16x16x32_bf16 v[68:71], v[150:153], v[190:193], v[68:71]
	v_mfma_f32_16x16x32_bf16 v[64:67], v[158:161], v[190:193], v[64:67]
	s_barrier
; #define PG8_AOFF(ord, U, O0, O1) do { _Pragma("unroll") for (int _i = 0; _i < 2; ++_i) { \
;         O0[_i] = d.rowbyte(U, (int)tix[(ord) * 256 + Rr[_i]]) + (unsigned)(Cc[_i] * 2); O1[_i] = d.rowbyte(U, (int)tix[(ord) * 256 + HALF + Rr[_i]]) + (unsigned)(Cc[_i] * 2); } } while (0)
; #define PG8_STAGE(bufoff, gbase, voff) do { _Pragma("unroll") for (int _i = 0; _i < 2; ++_i) \
;         __builtin_amdgcn_global_load_lds((const __attribute__((address_space(1))) unsigned*)((const __attribute__((address_space(1))) char*)(gbase) + (unsigned)lnd_v((int)(voff)[_i])), (LAS unsigned*)(lds + (bufoff) + ldsw + _i * 8192), 16, 0, 0); } while (0)
; #define PG8_LDA(dst, b, h) do { _Pragma("unroll") for (int m = 0; m < 4; ++m) _Pragma("unroll") for (int k = 0; k < 2; ++k) dst[m][k] = *(const LAS bf16x8*)(lds + PG8_SA(b, h) + aoff + m * 2048 + k * 1024); } while (0)
; template <class Desc, class Epi>
; __device__ __forceinline__ void gemm_phase(const int wv_, LAS unsigned char* lds, const Desc& d, const Epi& E) {
;     ...
;         const int inext = bid + (ui + 1) * nblk; const bool has_next = inext < d.nunits;
;         if (has_next) d.unit(inext, nxt);
;         if constexpr (Desc::GATHER) { if (has_next) PG8_AOFF(ui + 1, nxt, voffAn, voffAn1); else { voffAn[0] = voffA[0]; voffAn[1] = voffA[1]; voffAn1[0] = voffA1[0]; voffAn1[1] = voffA1[1]; } }
;         const char* nA = has_next ? (const char*)nxt.a : cA; const char* nB = has_next ? (const char*)nxt.b : cB;
;         for (int t = 0; t < nt; t += 2) {
;             const bool last = (t == nt - 2);
;             unsigned sA0[2], sA1[2];
;             if constexpr (Desc::GATHER) { sA0[0] = last ? voffAn[0] : voffA[0]; sA0[1] = last ? voffAn[1] : voffA[1]; sA1[0] = last ? voffAn1[0] : voffA1[0]; sA1[1] = last ? voffAn1[1] : voffA1[1]; }
;             else { sA0[0] = voffA[0]; sA0[1] = voffA[1]; sA1[0] = voffA1[0]; sA1[1] = voffA1[1]; }
;             const char* a1 = cA + (size_t)(t + 1) * kstep;
;             const char* a2 = last ? nA : cA + (size_t)(t + 2) * kstep; const char* b2 = last ? nB : cB + (size_t)(t + 2) * kstep;
;     ...
;             PG8_LDA(At, 1, 1); PG8_STAGE(PG8_SB(1, 0), b3, voffB); PG8_STAGE(PG8_SB(1, 1), b3 + hstepB, voffB); PG8_STAGE(PG8_SA(1, 0), a3, sA0);
;             PG8_WAIT_V(8); PG8_WAIT_L(0); PG8_BAR; PG8_MMA(1, 0, At, B0); PG8_MMA(1, 1, At, B1); PG8_BAR; PG8_SCHED;
;         }
	v_mov_b32_e32 v96, v208
	ds_read_b128 v[162:165], v221 offset:49152
	ds_read_b128 v[166:169], v221 offset:50176
	ds_read_b128 v[170:173], v221 offset:51200
	ds_read_b128 v[174:177], v221 offset:52224
	ds_read_b128 v[178:181], v221 offset:53248
	ds_read_b128 v[182:185], v221 offset:54272
	ds_read_b128 v[186:189], v221 offset:55296
	ds_read_b128 v[190:193], v221 offset:56320
	s_add_i32 s62, s62, s52
	v_lshl_add_u64 v[194:195], s[20:21], 0, v[96:97]
	v_lshl_add_u64 v[194:195], v[194:195], 0, s[30:31]
	s_mov_b32 m0, s62
	v_mov_b32_e32 v96, v211
	global_load_lds_dwordx4 v[194:195], off
	s_add_i32 m0, s62, 0x2000
	s_nop 0
	v_lshl_add_u64 v[194:195], s[20:21], 0, v[96:97]
	s_add_u32 s20, s20, 0x40080
	v_lshl_add_u64 v[194:195], v[194:195], 0, s[30:31]
	s_addc_u32 s21, s21, 0
	v_mov_b32_e32 v96, v208
	s_add_i32 s62, s63, s52
	global_load_lds_dwordx4 v[194:195], off
	s_mov_b32 m0, s62
	s_nop 0
	global_load_lds_dwordx4 v96, s[20:21]
	v_mov_b32_e32 v96, v211
	s_add_i32 m0, s62, 0x2000
	s_nop 0
	global_load_lds_dwordx4 v96, s[20:21]
	v_mov_b32_e32 v96, v206
	s_mov_b32 m0, s57
	v_lshl_add_u64 v[194:195], s[4:5], 0, v[96:97]
	v_lshl_add_u64 v[194:195], v[194:195], 0, s[30:31]
	v_mov_b32_e32 v96, v209
	global_load_lds_dwordx4 v[194:195], off
	s_mov_b32 m0, s58
	v_lshl_add_u64 v[194:195], s[4:5], 0, v[96:97]
	v_lshl_add_u64 v[194:195], v[194:195], 0, s[30:31]
	global_load_lds_dwordx4 v[194:195], off
	s_add_i32 s61, s61, 2
	s_add_u32 s2, s2, 0x100
	s_addc_u32 s3, s3, 0
	s_add_u32 s29, s29, 0x100
	s_addc_u32 s43, s43, 0
	s_add_u32 s4, s2, 0x80
	s_addc_u32 s5, s3, 0
	s_add_i32 s62, 0, 0x10000
	s_cmp_eq_u32 s61, 12
	s_cselect_b32 s5, s45, s5
	s_cselect_b32 s4, s44, s4
	v_add_u32_e32 v96, s62, v213
	s_cselect_b32 s21, s47, s43
	s_cselect_b32 s20, s46, s29
	s_add_i32 s64, 0, 0x14000
	s_waitcnt vmcnt(8)
	s_waitcnt lgkmcnt(0)
	s_barrier
	s_waitcnt lgkmcnt(0)
	v_mfma_f32_16x16x32_bf16 v[60:63], v[130:133], v[162:165], v[60:63]
	v_mfma_f32_16x16x32_bf16 v[56:59], v[138:141], v[162:165], v[56:59]
	v_mfma_f32_16x16x32_bf16 v[44:47], v[130:133], v[170:173], v[44:47]
	v_mfma_f32_16x16x32_bf16 v[40:43], v[138:141], v[170:173], v[40:43]
	v_mfma_f32_16x16x32_bf16 v[24:27], v[130:133], v[178:181], v[24:27]
	v_mfma_f32_16x16x32_bf16 v[16:19], v[138:141], v[178:181], v[16:19]
	v_mfma_f32_16x16x32_bf16 v[4:7], v[130:133], v[186:189], v[4:7]
	v_mfma_f32_16x16x32_bf16 v[0:3], v[138:141], v[186:189], v[0:3]
	v_mfma_f32_16x16x32_bf16 v[60:63], v[134:137], v[166:169], v[60:63]
	v_mfma_f32_16x16x32_bf16 v[56:59], v[142:145], v[166:169], v[56:59]
	v_mfma_f32_16x16x32_bf16 v[44:47], v[134:137], v[174:177], v[44:47]
	v_mfma_f32_16x16x32_bf16 v[40:43], v[142:145], v[174:177], v[40:43]
	v_mfma_f32_16x16x32_bf16 v[24:27], v[134:137], v[182:185], v[24:27]
	v_mfma_f32_16x16x32_bf16 v[16:19], v[142:145], v[182:185], v[16:19]
	v_mfma_f32_16x16x32_bf16 v[4:7], v[134:137], v[190:193], v[4:7]
	v_mfma_f32_16x16x32_bf16 v[0:3], v[142:145], v[190:193], v[0:3]
	v_mfma_f32_16x16x32_bf16 v[52:55], v[146:149], v[162:165], v[52:55]
	v_mfma_f32_16x16x32_bf16 v[48:51], v[154:157], v[162:165], v[48:51]
	v_mfma_f32_16x16x32_bf16 v[28:31], v[146:149], v[170:173], v[28:31]
	v_mfma_f32_16x16x32_bf16 v[20:23], v[154:157], v[170:173], v[20:23]
	v_mfma_f32_16x16x32_bf16 v[36:39], v[146:149], v[178:181], v[36:39]
	v_mfma_f32_16x16x32_bf16 v[32:35], v[154:157], v[178:181], v[32:35]
	v_mfma_f32_16x16x32_bf16 v[12:15], v[146:149], v[186:189], v[12:15]
	v_mfma_f32_16x16x32_bf16 v[8:11], v[154:157], v[186:189], v[8:11]
	v_mfma_f32_16x16x32_bf16 v[52:55], v[150:153], v[166:169], v[52:55]
	v_mfma_f32_16x16x32_bf16 v[48:51], v[158:161], v[166:169], v[48:51]
	v_mfma_f32_16x16x32_bf16 v[28:31], v[150:153], v[174:177], v[28:31]
	v_mfma_f32_16x16x32_bf16 v[20:23], v[158:161], v[174:177], v[20:23]
	v_mfma_f32_16x16x32_bf16 v[36:39], v[150:153], v[182:185], v[36:39]
	v_mfma_f32_16x16x32_bf16 v[32:35], v[158:161], v[182:185], v[32:35]
	v_mfma_f32_16x16x32_bf16 v[12:15], v[150:153], v[190:193], v[12:15]
	v_mfma_f32_16x16x32_bf16 v[8:11], v[158:161], v[190:193], v[8:11]
	s_barrier
	s_cmp_gt_u32 s61, 13
	s_cbranch_scc0 .Lkrot_1262
	s_and_b64 vcc, exec, s[40:41]
	s_cbranch_vccz .LBB0_1265
	s_barrier

; #define PG8_AOFF(ord, U, O0, O1) do { _Pragma("unroll") for (int _i = 0; _i < 2; ++_i) { \
;         O0[_i] = d.rowbyte(U, (int)tix[(ord) * 256 + Rr[_i]]) + (unsigned)(Cc[_i] * 2); O1[_i] = d.rowbyte(U, (int)tix[(ord) * 256 + HALF + Rr[_i]]) + (unsigned)(Cc[_i] * 2); } } while (0)
; #define PG8_STAGE(bufoff, gbase, voff) do { _Pragma("unroll") for (int _i = 0; _i < 2; ++_i) \
;         __builtin_amdgcn_global_load_lds((const __attribute__((address_space(1))) unsigned*)((const __attribute__((address_space(1))) char*)(gbase) + (unsigned)lnd_v((int)(voff)[_i])), (LAS unsigned*)(lds + (bufoff) + ldsw + _i * 8192), 16, 0, 0); } while (0)
; #define PG8_LDA(dst, b, h) do { _Pragma("unroll") for (int m = 0; m < 4; ++m) _Pragma("unroll") for (int k = 0; k < 2; ++k) dst[m][k] = *(const LAS bf16x8*)(lds + PG8_SA(b, h) + aoff + m * 2048 + k * 1024); } while (0)
; #define PG8_LDB(dst, b, h) do { _Pragma("unroll") for (int n = 0; n < 2; ++n) _Pragma("unroll") for (int k = 0; k < 2; ++k) dst[n][k] = *(const LAS bf16x8*)(lds + PG8_SB(b, h) + boff + n * 2048 + k * 1024); } while (0)
; template <class Desc, class Epi>
; __device__ __forceinline__ void gemm_phase(const int wv_, LAS unsigned char* lds, const Desc& d, const Epi& E) {
;     ...
;         if constexpr (Desc::GATHER) { if (has_next) PG8_AOFF(ui + 1, nxt, voffAn, voffAn1); else { voffAn[0] = voffA[0]; voffAn[1] = voffA[1]; voffAn1[0] = voffA1[0]; voffAn1[1] = voffA1[1]; } }
;         const char* nA = has_next ? (const char*)nxt.a : cA; const char* nB = has_next ? (const char*)nxt.b : cB;
;         for (int t = 0; t < nt; t += 2) {
;             const bool last = (t == nt - 2);
;             unsigned sA0[2], sA1[2];
;             if constexpr (Desc::GATHER) { sA0[0] = last ? voffAn[0] : voffA[0]; sA0[1] = last ? voffAn[1] : voffA[1]; sA1[0] = last ? voffAn1[0] : voffA1[0]; sA1[1] = last ? voffAn1[1] : voffA1[1]; }
;     ...
;             PG8_LDB(B0, 0, 0); PG8_LDB(B1, 0, 1); PG8_SCHED; PG8_LDA(At, 0, 0); PG8_STAGE(PG8_SA(1, 1), a1, voffA1);
;             PG8_WAIT_V(8); PG8_WAIT_L(0); PG8_BAR; PG8_MMA(0, 0, At, B0); PG8_MMA(0, 1, At, B1); PG8_BAR; PG8_SCHED;
;             PG8_LDA(At, 0, 1); PG8_STAGE(PG8_SB(0, 0), b2, voffB); PG8_STAGE(PG8_SB(0, 1), b2 + hstepB, voffB); PG8_STAGE(PG8_SA(0, 0), a2, sA0);
;             PG8_WAIT_V(8); PG8_WAIT_L(0); PG8_BAR; PG8_MMA(1, 0, At, B0); PG8_MMA(1, 1, At, B1); PG8_BAR; PG8_SCHED;
.Lkrot_1565:
	ds_read_b128 v[160:163], v135
	ds_read_b128 v[164:167], v135 offset:1024
	ds_read_b128 v[168:171], v135 offset:2048
	ds_read_b128 v[172:175], v135 offset:3072
	v_add_u32_e32 v135, s77, v143
	ds_read_b128 v[176:179], v135
	ds_read_b128 v[180:183], v135 offset:1024
	ds_read_b128 v[184:187], v135 offset:2048
	ds_read_b128 v[188:191], v135 offset:3072
	v_cndmask_b32_e32 v134, v157, v153, vcc
	v_cndmask_b32_e32 v132, v159, v154, vcc
	v_cndmask_b32_e32 v96, v131, v155, vcc
	v_cndmask_b32_e32 v133, v158, v156, vcc
	s_add_i32 m0, s64, 0xc000
	v_mov_b32_e32 v135, v131
	s_add_u32 s2, s40, s2
	ds_read_b128 v[192:195], v152
	ds_read_b128 v[196:199], v152 offset:1024
	ds_read_b128 v[200:203], v152 offset:2048
	ds_read_b128 v[204:207], v152 offset:3072
	ds_read_b128 v[208:211], v152 offset:4096
	ds_read_b128 v[212:215], v152 offset:5120
	ds_read_b128 v[220:223], v152 offset:6144
	ds_read_b128 v[224:227], v152 offset:7168
	s_addc_u32 s3, s41, s3
	global_load_lds_dwordx4 v135, s[2:3]
	v_mov_b32_e32 v135, v158
	s_add_i32 m0, s64, 0xe000
	s_nop 0
	global_load_lds_dwordx4 v135, s[2:3]
	s_waitcnt vmcnt(8)
	s_waitcnt lgkmcnt(0)
	s_barrier
	s_waitcnt lgkmcnt(0)
	v_mfma_f32_16x16x32_bf16 v[122:125], v[160:163], v[192:195], v[122:125]
	v_mfma_f32_16x16x32_bf16 v[114:117], v[168:171], v[192:195], v[114:117]
	v_mfma_f32_16x16x32_bf16 v[106:109], v[160:163], v[200:203], v[106:109]
	v_mfma_f32_16x16x32_bf16 v[98:101], v[168:171], v[200:203], v[98:101]
	v_mfma_f32_16x16x32_bf16 v[88:91], v[160:163], v[208:211], v[88:91]
	v_mfma_f32_16x16x32_bf16 v[80:83], v[168:171], v[208:211], v[80:83]
	v_mfma_f32_16x16x32_bf16 v[72:75], v[160:163], v[220:223], v[72:75]
	v_mfma_f32_16x16x32_bf16 v[64:67], v[168:171], v[220:223], v[64:67]
	v_mfma_f32_16x16x32_bf16 v[122:125], v[164:167], v[196:199], v[122:125]
	v_mfma_f32_16x16x32_bf16 v[114:117], v[172:175], v[196:199], v[114:117]
	v_mfma_f32_16x16x32_bf16 v[106:109], v[164:167], v[204:207], v[106:109]
	v_mfma_f32_16x16x32_bf16 v[98:101], v[172:175], v[204:207], v[98:101]
	v_mfma_f32_16x16x32_bf16 v[88:91], v[164:167], v[212:215], v[88:91]
	v_mfma_f32_16x16x32_bf16 v[80:83], v[172:175], v[212:215], v[80:83]
	v_mfma_f32_16x16x32_bf16 v[72:75], v[164:167], v[224:227], v[72:75]
	v_mfma_f32_16x16x32_bf16 v[64:67], v[172:175], v[224:227], v[64:67]
	v_mfma_f32_16x16x32_bf16 v[126:129], v[176:179], v[192:195], v[126:129]
	v_mfma_f32_16x16x32_bf16 v[118:121], v[184:187], v[192:195], v[118:121]
	v_mfma_f32_16x16x32_bf16 v[110:113], v[176:179], v[200:203], v[110:113]
	v_mfma_f32_16x16x32_bf16 v[102:105], v[184:187], v[200:203], v[102:105]
	v_mfma_f32_16x16x32_bf16 v[92:95], v[176:179], v[208:211], v[92:95]
	v_mfma_f32_16x16x32_bf16 v[84:87], v[184:187], v[208:211], v[84:87]
	v_mfma_f32_16x16x32_bf16 v[76:79], v[176:179], v[220:223], v[76:79]
	v_mfma_f32_16x16x32_bf16 v[68:71], v[184:187], v[220:223], v[68:71]
	v_mfma_f32_16x16x32_bf16 v[126:129], v[180:183], v[196:199], v[126:129]
	v_mfma_f32_16x16x32_bf16 v[118:121], v[188:191], v[196:199], v[118:121]
	v_mfma_f32_16x16x32_bf16 v[110:113], v[180:183], v[204:207], v[110:113]
	v_mfma_f32_16x16x32_bf16 v[102:105], v[188:191], v[204:207], v[102:105]
	v_mfma_f32_16x16x32_bf16 v[92:95], v[180:183], v[212:215], v[92:95]
	v_mfma_f32_16x16x32_bf16 v[84:87], v[188:191], v[212:215], v[84:87]
	v_mfma_f32_16x16x32_bf16 v[76:79], v[180:183], v[224:227], v[76:79]
	v_mfma_f32_16x16x32_bf16 v[68:71], v[188:191], v[224:227], v[68:71]
	s_barrier
	v_mov_b32_e32 v135, v138
	s_add_i32 s2, s76, s63
	ds_read_b128 v[192:195], v152 offset:16384
	ds_read_b128 v[196:199], v152 offset:17408
	ds_read_b128 v[200:203], v152 offset:18432
	ds_read_b128 v[204:207], v152 offset:19456
	ds_read_b128 v[208:211], v152 offset:20480
	ds_read_b128 v[212:215], v152 offset:21504
	ds_read_b128 v[220:223], v152 offset:22528
	ds_read_b128 v[224:227], v152 offset:23552
	s_mov_b32 m0, s2
	s_nop 0
	global_load_lds_dwordx4 v135, s[22:23]
	v_mov_b32_e32 v135, v141
	s_add_i32 m0, s2, 0x2000
	s_add_u32 s2, s22, 0x40000
	global_load_lds_dwordx4 v135, s[22:23]
	s_addc_u32 s3, s23, 0
	v_mov_b32_e32 v135, v138
	s_add_i32 s76, s77, s63
	s_mov_b32 m0, s76
	s_nop 0
	global_load_lds_dwordx4 v135, s[2:3]
	v_mov_b32_e32 v135, v141
	s_add_i32 m0, s76, 0x2000
	s_nop 0
	global_load_lds_dwordx4 v135, s[2:3]
	v_mov_b32_e32 v135, v134
	s_mov_b32 m0, s64
	s_nop 0
	global_load_lds_dwordx4 v135, s[20:21]
	v_mov_b32_e32 v135, v132
	s_mov_b32 m0, s65
	s_nop 0
	global_load_lds_dwordx4 v135, s[20:21]
	s_waitcnt vmcnt(8)
	s_waitcnt lgkmcnt(0)
	s_barrier
	s_waitcnt lgkmcnt(0)
	v_mfma_f32_16x16x32_bf16 v[56:59], v[160:163], v[192:195], v[56:59]
	v_mfma_f32_16x16x32_bf16 v[48:51], v[168:171], v[192:195], v[48:51]
	v_mfma_f32_16x16x32_bf16 v[40:43], v[160:163], v[200:203], v[40:43]
	v_mfma_f32_16x16x32_bf16 v[32:35], v[168:171], v[200:203], v[32:35]
	v_mfma_f32_16x16x32_bf16 v[24:27], v[160:163], v[208:211], v[24:27]
	v_mfma_f32_16x16x32_bf16 v[16:19], v[168:171], v[208:211], v[16:19]
	v_mfma_f32_16x16x32_bf16 v[8:11], v[160:163], v[220:223], v[8:11]
	v_mfma_f32_16x16x32_bf16 v[4:7], v[168:171], v[220:223], v[4:7]
	v_mfma_f32_16x16x32_bf16 v[56:59], v[164:167], v[196:199], v[56:59]
	v_mfma_f32_16x16x32_bf16 v[48:51], v[172:175], v[196:199], v[48:51]
	v_mfma_f32_16x16x32_bf16 v[40:43], v[164:167], v[204:207], v[40:43]
	v_mfma_f32_16x16x32_bf16 v[32:35], v[172:175], v[204:207], v[32:35]
	v_mfma_f32_16x16x32_bf16 v[24:27], v[164:167], v[212:215], v[24:27]
	v_mfma_f32_16x16x32_bf16 v[16:19], v[172:175], v[212:215], v[16:19]
	v_mfma_f32_16x16x32_bf16 v[8:11], v[164:167], v[224:227], v[8:11]
	v_mfma_f32_16x16x32_bf16 v[4:7], v[172:175], v[224:227], v[4:7]
	v_mfma_f32_16x16x32_bf16 v[60:63], v[176:179], v[192:195], v[60:63]
	v_mfma_f32_16x16x32_bf16 v[52:55], v[184:187], v[192:195], v[52:55]
	v_mfma_f32_16x16x32_bf16 v[44:47], v[176:179], v[200:203], v[44:47]
	v_mfma_f32_16x16x32_bf16 v[36:39], v[184:187], v[200:203], v[36:39]
	v_mfma_f32_16x16x32_bf16 v[28:31], v[176:179], v[208:211], v[28:31]
	v_mfma_f32_16x16x32_bf16 v[20:23], v[184:187], v[208:211], v[20:23]
	v_mfma_f32_16x16x32_bf16 v[12:15], v[176:179], v[220:223], v[12:15]
	v_mfma_f32_16x16x32_bf16 v[0:3], v[184:187], v[220:223], v[0:3]
	v_mfma_f32_16x16x32_bf16 v[60:63], v[180:183], v[196:199], v[60:63]
	v_mfma_f32_16x16x32_bf16 v[52:55], v[188:191], v[196:199], v[52:55]
	v_mfma_f32_16x16x32_bf16 v[44:47], v[180:183], v[204:207], v[44:47]
	v_mfma_f32_16x16x32_bf16 v[36:39], v[188:191], v[204:207], v[36:39]
	v_mfma_f32_16x16x32_bf16 v[28:31], v[180:183], v[212:215], v[28:31]
	v_mfma_f32_16x16x32_bf16 v[20:23], v[188:191], v[212:215], v[20:23]
	v_mfma_f32_16x16x32_bf16 v[12:15], v[180:183], v[224:227], v[12:15]
	v_mfma_f32_16x16x32_bf16 v[0:3], v[188:191], v[224:227], v[0:3]
	s_barrier
; #define PG8_STAGE(bufoff, gbase, voff) do { _Pragma("unroll") for (int _i = 0; _i < 2; ++_i) \
;         __builtin_amdgcn_global_load_lds((const __attribute__((address_space(1))) unsigned*)((const __attribute__((address_space(1))) char*)(gbase) + (unsigned)lnd_v((int)(voff)[_i])), (LAS unsigned*)(lds + (bufoff) + ldsw + _i * 8192), 16, 0, 0); } while (0)
; #define PG8_LDA(dst, b, h) do { _Pragma("unroll") for (int m = 0; m < 4; ++m) _Pragma("unroll") for (int k = 0; k < 2; ++k) dst[m][k] = *(const LAS bf16x8*)(lds + PG8_SA(b, h) + aoff + m * 2048 + k * 1024); } while (0)
; #define PG8_LDB(dst, b, h) do { _Pragma("unroll") for (int n = 0; n < 2; ++n) _Pragma("unroll") for (int k = 0; k < 2; ++k) dst[n][k] = *(const LAS bf16x8*)(lds + PG8_SB(b, h) + boff + n * 2048 + k * 1024); } while (0)
; #define PG8_MMA(ai, bj, At, Bt) do { __builtin_amdgcn_s_setprio(1); _Pragma("unroll") for (int m = 0; m < 4; ++m) _Pragma("unroll") for (int n = 0; n < 2; ++n) _Pragma("unroll") for (int k = 0; k < 2; ++k) \
;         acc[ai][bj][m][n] = __builtin_amdgcn_mfma_f32_16x16x32_bf16(Bt[n][k], At[m][k], acc[ai][bj][m][n], 0, 0, 0); __builtin_amdgcn_s_setprio(0); } while (0)
; #define PG8_WAIT_V(n) asm volatile("s_waitcnt vmcnt(" #n ")" ::: "memory")
; #define PG8_WAIT_L(n) asm volatile("s_waitcnt lgkmcnt(" #n ")" ::: "memory")
; #define PG8_BAR __builtin_amdgcn_s_barrier()
; #define PG8_SCHED __builtin_amdgcn_sched_barrier(0)
; template <class Desc, class Epi>
; __device__ __forceinline__ void gemm_phase(const int wv_, LAS unsigned char* lds, const Desc& d, const Epi& E) {
;     ...
;             PG8_LDB(B0, 1, 0); PG8_LDB(B1, 1, 1); PG8_SCHED; PG8_LDA(At, 1, 0); PG8_STAGE(PG8_SA(0, 1), a2, sA1);
;             PG8_WAIT_V(8); PG8_WAIT_L(0); PG8_BAR; PG8_MMA(0, 0, At, B0); PG8_MMA(0, 1, At, B1); PG8_BAR; PG8_SCHED;
	s_add_i32 s2, 0, 0x18000
	v_add_u32_e32 v135, s2, v143
	s_add_i32 s76, 0, 0x1c000
	ds_read_b128 v[160:163], v135
	ds_read_b128 v[164:167], v135 offset:1024
	ds_read_b128 v[168:171], v135 offset:2048
	ds_read_b128 v[172:175], v135 offset:3072
	v_add_u32_e32 v135, s76, v143
	ds_read_b128 v[176:179], v135
	ds_read_b128 v[180:183], v135 offset:1024
	ds_read_b128 v[184:187], v135 offset:2048
	ds_read_b128 v[188:191], v135 offset:3072
	s_mov_b32 m0, s68
	ds_read_b128 v[192:195], v152 offset:32768
	ds_read_b128 v[196:199], v152 offset:33792
	ds_read_b128 v[200:203], v152 offset:34816
	ds_read_b128 v[204:207], v152 offset:35840
	ds_read_b128 v[208:211], v152 offset:36864
	ds_read_b128 v[212:215], v152 offset:37888
	ds_read_b128 v[220:223], v152 offset:38912
	ds_read_b128 v[224:227], v152 offset:39936
	s_nop 0
	global_load_lds_dwordx4 v96, s[20:21]
	s_mov_b32 m0, s69
	s_nop 0
	global_load_lds_dwordx4 v133, s[20:21]
	s_waitcnt vmcnt(8)
	s_waitcnt lgkmcnt(0)
	s_barrier
	s_waitcnt lgkmcnt(0)
	v_mfma_f32_16x16x32_bf16 v[122:125], v[160:163], v[192:195], v[122:125]
	v_mfma_f32_16x16x32_bf16 v[114:117], v[168:171], v[192:195], v[114:117]
	v_mfma_f32_16x16x32_bf16 v[106:109], v[160:163], v[200:203], v[106:109]
	v_mfma_f32_16x16x32_bf16 v[98:101], v[168:171], v[200:203], v[98:101]
	v_mfma_f32_16x16x32_bf16 v[88:91], v[160:163], v[208:211], v[88:91]
	v_mfma_f32_16x16x32_bf16 v[80:83], v[168:171], v[208:211], v[80:83]
	v_mfma_f32_16x16x32_bf16 v[72:75], v[160:163], v[220:223], v[72:75]
	v_mfma_f32_16x16x32_bf16 v[64:67], v[168:171], v[220:223], v[64:67]
	v_mfma_f32_16x16x32_bf16 v[122:125], v[164:167], v[196:199], v[122:125]
	v_mfma_f32_16x16x32_bf16 v[114:117], v[172:175], v[196:199], v[114:117]
	v_mfma_f32_16x16x32_bf16 v[106:109], v[164:167], v[204:207], v[106:109]
	v_mfma_f32_16x16x32_bf16 v[98:101], v[172:175], v[204:207], v[98:101]
	v_mfma_f32_16x16x32_bf16 v[88:91], v[164:167], v[212:215], v[88:91]
	v_mfma_f32_16x16x32_bf16 v[80:83], v[172:175], v[212:215], v[80:83]
	v_mfma_f32_16x16x32_bf16 v[72:75], v[164:167], v[224:227], v[72:75]
	v_mfma_f32_16x16x32_bf16 v[64:67], v[172:175], v[224:227], v[64:67]
	v_mfma_f32_16x16x32_bf16 v[126:129], v[176:179], v[192:195], v[126:129]
	v_mfma_f32_16x16x32_bf16 v[118:121], v[184:187], v[192:195], v[118:121]
	v_mfma_f32_16x16x32_bf16 v[110:113], v[176:179], v[200:203], v[110:113]
	v_mfma_f32_16x16x32_bf16 v[102:105], v[184:187], v[200:203], v[102:105]
	v_mfma_f32_16x16x32_bf16 v[92:95], v[176:179], v[208:211], v[92:95]
	v_mfma_f32_16x16x32_bf16 v[84:87], v[184:187], v[208:211], v[84:87]
	v_mfma_f32_16x16x32_bf16 v[76:79], v[176:179], v[220:223], v[76:79]
	v_mfma_f32_16x16x32_bf16 v[68:71], v[184:187], v[220:223], v[68:71]
	v_mfma_f32_16x16x32_bf16 v[126:129], v[180:183], v[196:199], v[126:129]
	v_mfma_f32_16x16x32_bf16 v[118:121], v[188:191], v[196:199], v[118:121]
	v_mfma_f32_16x16x32_bf16 v[110:113], v[180:183], v[204:207], v[110:113]
	v_mfma_f32_16x16x32_bf16 v[102:105], v[188:191], v[204:207], v[102:105]
	v_mfma_f32_16x16x32_bf16 v[92:95], v[180:183], v[212:215], v[92:95]
	v_mfma_f32_16x16x32_bf16 v[84:87], v[188:191], v[212:215], v[84:87]
	v_mfma_f32_16x16x32_bf16 v[76:79], v[180:183], v[224:227], v[76:79]
	v_mfma_f32_16x16x32_bf16 v[68:71], v[188:191], v[224:227], v[68:71]
	s_barrier
; #define PG8_AOFF(ord, U, O0, O1) do { _Pragma("unroll") for (int _i = 0; _i < 2; ++_i) { \
;         O0[_i] = d.rowbyte(U, (int)tix[(ord) * 256 + Rr[_i]]) + (unsigned)(Cc[_i] * 2); O1[_i] = d.rowbyte(U, (int)tix[(ord) * 256 + HALF + Rr[_i]]) + (unsigned)(Cc[_i] * 2); } } while (0)
; #define PG8_STAGE(bufoff, gbase, voff) do { _Pragma("unroll") for (int _i = 0; _i < 2; ++_i) \
;         __builtin_amdgcn_global_load_lds((const __attribute__((address_space(1))) unsigned*)((const __attribute__((address_space(1))) char*)(gbase) + (unsigned)lnd_v((int)(voff)[_i])), (LAS unsigned*)(lds + (bufoff) + ldsw + _i * 8192), 16, 0, 0); } while (0)
; #define PG8_LDA(dst, b, h) do { _Pragma("unroll") for (int m = 0; m < 4; ++m) _Pragma("unroll") for (int k = 0; k < 2; ++k) dst[m][k] = *(const LAS bf16x8*)(lds + PG8_SA(b, h) + aoff + m * 2048 + k * 1024); } while (0)
; template <class Desc, class Epi>
; __device__ __forceinline__ void gemm_phase(const int wv_, LAS unsigned char* lds, const Desc& d, const Epi& E) {
;     ...
;         const int inext = bid + (ui + 1) * nblk; const bool has_next = inext < d.nunits;
;         if (has_next) d.unit(inext, nxt);
;         if constexpr (Desc::GATHER) { if (has_next) PG8_AOFF(ui + 1, nxt, voffAn, voffAn1); else { voffAn[0] = voffA[0]; voffAn[1] = voffA[1]; voffAn1[0] = voffA1[0]; voffAn1[1] = voffA1[1]; } }
;         const char* nA = has_next ? (const char*)nxt.a : cA; const char* nB = has_next ? (const char*)nxt.b : cB;
;         for (int t = 0; t < nt; t += 2) {
;             const bool last = (t == nt - 2);
;             unsigned sA0[2], sA1[2];
;             if constexpr (Desc::GATHER) { sA0[0] = last ? voffAn[0] : voffA[0]; sA0[1] = last ? voffAn[1] : voffA[1]; sA1[0] = last ? voffAn1[0] : voffA1[0]; sA1[1] = last ? voffAn1[1] : voffA1[1]; }
;             else { sA0[0] = voffA[0]; sA0[1] = voffA[1]; sA1[0] = voffA1[0]; sA1[1] = voffA1[1]; }
;             const char* a1 = cA + (size_t)(t + 1) * kstep;
;             const char* a2 = last ? nA : cA + (size_t)(t + 2) * kstep; const char* b2 = last ? nB : cB + (size_t)(t + 2) * kstep;
;     ...
;             PG8_LDA(At, 1, 1); PG8_STAGE(PG8_SB(1, 0), b3, voffB); PG8_STAGE(PG8_SB(1, 1), b3 + hstepB, voffB); PG8_STAGE(PG8_SA(1, 0), a3, sA0);
;             PG8_WAIT_V(8); PG8_WAIT_L(0); PG8_BAR; PG8_MMA(1, 0, At, B0); PG8_MMA(1, 1, At, B1); PG8_BAR; PG8_SCHED;
;         }
	v_mov_b32_e32 v96, v138
	ds_read_b128 v[192:195], v152 offset:49152
	ds_read_b128 v[196:199], v152 offset:50176
	ds_read_b128 v[200:203], v152 offset:51200
	ds_read_b128 v[204:207], v152 offset:52224
	ds_read_b128 v[208:211], v152 offset:53248
	ds_read_b128 v[212:215], v152 offset:54272
	ds_read_b128 v[220:223], v152 offset:55296
	ds_read_b128 v[224:227], v152 offset:56320
	s_add_i32 s2, s2, s63
	v_lshl_add_u64 v[228:229], s[22:23], 0, v[96:97]
	v_lshl_add_u64 v[228:229], v[228:229], 0, s[30:31]
	s_mov_b32 m0, s2
	v_mov_b32_e32 v96, v141
	global_load_lds_dwordx4 v[228:229], off
	s_add_i32 m0, s2, 0x2000
	s_add_u32 s2, s22, 0x40080
	v_lshl_add_u64 v[228:229], s[22:23], 0, v[96:97]
	v_lshl_add_u64 v[228:229], v[228:229], 0, s[30:31]
	s_addc_u32 s3, s23, 0
	v_mov_b32_e32 v96, v138
	s_add_i32 s22, s76, s63
	global_load_lds_dwordx4 v[228:229], off
	s_mov_b32 m0, s22
	v_mov_b32_e32 v135, v97
	global_load_lds_dwordx4 v96, s[2:3]
	v_mov_b32_e32 v96, v141
	s_add_i32 m0, s22, 0x2000
	v_mov_b32_e32 v133, v97
	global_load_lds_dwordx4 v96, s[2:3]
	s_mov_b32 m0, s70
	v_lshl_add_u64 v[134:135], s[20:21], 0, v[134:135]
	v_lshl_add_u64 v[134:135], v[134:135], 0, s[30:31]
	global_load_lds_dwordx4 v[134:135], off
	s_mov_b32 m0, s71
	v_lshl_add_u64 v[132:133], s[20:21], 0, v[132:133]
	v_lshl_add_u64 v[132:133], v[132:133], 0, s[30:31]
	global_load_lds_dwordx4 v[132:133], off
	s_add_i32 s75, s75, 2
	s_mov_b64 s[2:3], s[4:5]
	s_add_u32 s4, s2, 0x100
	s_addc_u32 s5, s3, 0
	s_add_u32 s22, s29, s2
	s_addc_u32 s23, s59, s3
	s_cmp_eq_u32 s75, 12
	s_cselect_b64 vcc, -1, 0
	s_and_b64 s[20:21], vcc, exec
	s_cselect_b32 s20, 0, s4
	s_cselect_b32 s21, 0, s5
	s_cselect_b32 s22, s54, s22
	s_cselect_b32 s23, s55, s23
	s_add_u32 s20, s42, s20
	s_addc_u32 s21, s43, s21
	s_add_i32 s76, 0, 0x10000
	v_add_u32_e32 v135, s76, v143
	s_add_i32 s77, 0, 0x14000
	s_waitcnt vmcnt(8)
	s_waitcnt lgkmcnt(0)
	s_barrier
	s_waitcnt lgkmcnt(0)
	v_mfma_f32_16x16x32_bf16 v[56:59], v[160:163], v[192:195], v[56:59]
	v_mfma_f32_16x16x32_bf16 v[48:51], v[168:171], v[192:195], v[48:51]
	v_mfma_f32_16x16x32_bf16 v[40:43], v[160:163], v[200:203], v[40:43]
	v_mfma_f32_16x16x32_bf16 v[32:35], v[168:171], v[200:203], v[32:35]
	v_mfma_f32_16x16x32_bf16 v[24:27], v[160:163], v[208:211], v[24:27]
	v_mfma_f32_16x16x32_bf16 v[16:19], v[168:171], v[208:211], v[16:19]
	v_mfma_f32_16x16x32_bf16 v[8:11], v[160:163], v[220:223], v[8:11]
	v_mfma_f32_16x16x32_bf16 v[4:7], v[168:171], v[220:223], v[4:7]
	v_mfma_f32_16x16x32_bf16 v[56:59], v[164:167], v[196:199], v[56:59]
	v_mfma_f32_16x16x32_bf16 v[48:51], v[172:175], v[196:199], v[48:51]
	v_mfma_f32_16x16x32_bf16 v[40:43], v[164:167], v[204:207], v[40:43]
	v_mfma_f32_16x16x32_bf16 v[32:35], v[172:175], v[204:207], v[32:35]
	v_mfma_f32_16x16x32_bf16 v[24:27], v[164:167], v[212:215], v[24:27]
	v_mfma_f32_16x16x32_bf16 v[16:19], v[172:175], v[212:215], v[16:19]
	v_mfma_f32_16x16x32_bf16 v[8:11], v[164:167], v[224:227], v[8:11]
	v_mfma_f32_16x16x32_bf16 v[4:7], v[172:175], v[224:227], v[4:7]
	v_mfma_f32_16x16x32_bf16 v[60:63], v[176:179], v[192:195], v[60:63]
	v_mfma_f32_16x16x32_bf16 v[52:55], v[184:187], v[192:195], v[52:55]
	v_mfma_f32_16x16x32_bf16 v[44:47], v[176:179], v[200:203], v[44:47]
	v_mfma_f32_16x16x32_bf16 v[36:39], v[184:187], v[200:203], v[36:39]
	v_mfma_f32_16x16x32_bf16 v[28:31], v[176:179], v[208:211], v[28:31]
	v_mfma_f32_16x16x32_bf16 v[20:23], v[184:187], v[208:211], v[20:23]
	v_mfma_f32_16x16x32_bf16 v[12:15], v[176:179], v[220:223], v[12:15]
	v_mfma_f32_16x16x32_bf16 v[0:3], v[184:187], v[220:223], v[0:3]
	v_mfma_f32_16x16x32_bf16 v[60:63], v[180:183], v[196:199], v[60:63]
	v_mfma_f32_16x16x32_bf16 v[52:55], v[188:191], v[196:199], v[52:55]
	v_mfma_f32_16x16x32_bf16 v[44:47], v[180:183], v[204:207], v[44:47]
	v_mfma_f32_16x16x32_bf16 v[36:39], v[188:191], v[204:207], v[36:39]
	v_mfma_f32_16x16x32_bf16 v[28:31], v[180:183], v[212:215], v[28:31]
	v_mfma_f32_16x16x32_bf16 v[20:23], v[188:191], v[212:215], v[20:23]
	v_mfma_f32_16x16x32_bf16 v[12:15], v[180:183], v[224:227], v[12:15]
	v_mfma_f32_16x16x32_bf16 v[0:3], v[188:191], v[224:227], v[0:3]
	s_barrier
	s_cmp_gt_u32 s75, 13
	s_cbranch_scc0 .Lkrot_1565
	s_and_b64 vcc, exec, s[52:53]
	s_cbranch_vccz .LBB0_1568
	s_barrier

; #define PG8_AOFF(ord, U, O0, O1) do { _Pragma("unroll") for (int _i = 0; _i < 2; ++_i) { \
;         O0[_i] = d.rowbyte(U, (int)tix[(ord) * 256 + Rr[_i]]) + (unsigned)(Cc[_i] * 2); O1[_i] = d.rowbyte(U, (int)tix[(ord) * 256 + HALF + Rr[_i]]) + (unsigned)(Cc[_i] * 2); } } while (0)
; #define PG8_STAGE(bufoff, gbase, voff) do { _Pragma("unroll") for (int _i = 0; _i < 2; ++_i) \
;         __builtin_amdgcn_global_load_lds((const __attribute__((address_space(1))) unsigned*)((const __attribute__((address_space(1))) char*)(gbase) + (unsigned)lnd_v((int)(voff)[_i])), (LAS unsigned*)(lds + (bufoff) + ldsw + _i * 8192), 16, 0, 0); } while (0)
; #define PG8_LDA(dst, b, h) do { _Pragma("unroll") for (int m = 0; m < 4; ++m) _Pragma("unroll") for (int k = 0; k < 2; ++k) dst[m][k] = *(const LAS bf16x8*)(lds + PG8_SA(b, h) + aoff + m * 2048 + k * 1024); } while (0)
; #define PG8_LDB(dst, b, h) do { _Pragma("unroll") for (int n = 0; n < 2; ++n) _Pragma("unroll") for (int k = 0; k < 2; ++k) dst[n][k] = *(const LAS bf16x8*)(lds + PG8_SB(b, h) + boff + n * 2048 + k * 1024); } while (0)
; template <class Desc, class Epi>
; __device__ __forceinline__ void gemm_phase(const int wv_, LAS unsigned char* lds, const Desc& d, const Epi& E) {
;     ...
;         if constexpr (Desc::GATHER) { if (has_next) PG8_AOFF(ui + 1, nxt, voffAn, voffAn1); else { voffAn[0] = voffA[0]; voffAn[1] = voffA[1]; voffAn1[0] = voffA1[0]; voffAn1[1] = voffA1[1]; } }
;         const char* nA = has_next ? (const char*)nxt.a : cA; const char* nB = has_next ? (const char*)nxt.b : cB;
;         for (int t = 0; t < nt; t += 2) {
;             const bool last = (t == nt - 2);
;             unsigned sA0[2], sA1[2];
;             if constexpr (Desc::GATHER) { sA0[0] = last ? voffAn[0] : voffA[0]; sA0[1] = last ? voffAn[1] : voffA[1]; sA1[0] = last ? voffAn1[0] : voffA1[0]; sA1[1] = last ? voffAn1[1] : voffA1[1]; }
;     ...
;             PG8_LDB(B0, 0, 0); PG8_LDB(B1, 0, 1); PG8_SCHED; PG8_LDA(At, 0, 0); PG8_STAGE(PG8_SA(1, 1), a1, voffA1);
;             PG8_WAIT_V(8); PG8_WAIT_L(0); PG8_BAR; PG8_MMA(0, 0, At, B0); PG8_MMA(0, 1, At, B1); PG8_BAR; PG8_SCHED;
;             PG8_LDA(At, 0, 1); PG8_STAGE(PG8_SB(0, 0), b2, voffB); PG8_STAGE(PG8_SB(0, 1), b2 + hstepB, voffB); PG8_STAGE(PG8_SA(0, 0), a2, sA0);
;             PG8_WAIT_V(8); PG8_WAIT_L(0); PG8_BAR; PG8_MMA(1, 0, At, B0); PG8_MMA(1, 1, At, B1); PG8_BAR; PG8_SCHED;
.Lkrot_1861:
	ds_read_b128 v[160:163], v135
	ds_read_b128 v[164:167], v135 offset:1024
	ds_read_b128 v[168:171], v135 offset:2048
	ds_read_b128 v[172:175], v135 offset:3072
	v_add_u32_e32 v135, s68, v143
	ds_read_b128 v[176:179], v135
	ds_read_b128 v[180:183], v135 offset:1024
	ds_read_b128 v[184:187], v135 offset:2048
	ds_read_b128 v[188:191], v135 offset:3072
	v_cndmask_b32_e32 v134, v157, v153, vcc
	v_cndmask_b32_e32 v132, v159, v154, vcc
	v_cndmask_b32_e32 v96, v131, v155, vcc
	v_cndmask_b32_e32 v133, v158, v156, vcc
	s_add_i32 m0, s57, 0xc000
	v_mov_b32_e32 v135, v131
	s_add_u32 s2, s38, s2
	ds_read_b128 v[192:195], v152
	ds_read_b128 v[196:199], v152 offset:1024
	ds_read_b128 v[200:203], v152 offset:2048
	ds_read_b128 v[204:207], v152 offset:3072
	ds_read_b128 v[208:211], v152 offset:4096
	ds_read_b128 v[212:215], v152 offset:5120
	ds_read_b128 v[220:223], v152 offset:6144
	ds_read_b128 v[224:227], v152 offset:7168
	s_addc_u32 s3, s39, s3
	global_load_lds_dwordx4 v135, s[2:3]
	v_mov_b32_e32 v135, v158
	s_add_i32 m0, s57, 0xe000
	s_nop 0
	global_load_lds_dwordx4 v135, s[2:3]
	s_waitcnt vmcnt(8)
	s_waitcnt lgkmcnt(0)
	s_barrier
	s_waitcnt lgkmcnt(0)
	v_mfma_f32_16x16x32_bf16 v[122:125], v[160:163], v[192:195], v[122:125]
	v_mfma_f32_16x16x32_bf16 v[114:117], v[168:171], v[192:195], v[114:117]
	v_mfma_f32_16x16x32_bf16 v[106:109], v[160:163], v[200:203], v[106:109]
	v_mfma_f32_16x16x32_bf16 v[98:101], v[168:171], v[200:203], v[98:101]
	v_mfma_f32_16x16x32_bf16 v[88:91], v[160:163], v[208:211], v[88:91]
	v_mfma_f32_16x16x32_bf16 v[80:83], v[168:171], v[208:211], v[80:83]
	v_mfma_f32_16x16x32_bf16 v[72:75], v[160:163], v[220:223], v[72:75]
	v_mfma_f32_16x16x32_bf16 v[64:67], v[168:171], v[220:223], v[64:67]
	v_mfma_f32_16x16x32_bf16 v[122:125], v[164:167], v[196:199], v[122:125]
	v_mfma_f32_16x16x32_bf16 v[114:117], v[172:175], v[196:199], v[114:117]
	v_mfma_f32_16x16x32_bf16 v[106:109], v[164:167], v[204:207], v[106:109]
	v_mfma_f32_16x16x32_bf16 v[98:101], v[172:175], v[204:207], v[98:101]
	v_mfma_f32_16x16x32_bf16 v[88:91], v[164:167], v[212:215], v[88:91]
	v_mfma_f32_16x16x32_bf16 v[80:83], v[172:175], v[212:215], v[80:83]
	v_mfma_f32_16x16x32_bf16 v[72:75], v[164:167], v[224:227], v[72:75]
	v_mfma_f32_16x16x32_bf16 v[64:67], v[172:175], v[224:227], v[64:67]
	v_mfma_f32_16x16x32_bf16 v[126:129], v[176:179], v[192:195], v[126:129]
	v_mfma_f32_16x16x32_bf16 v[118:121], v[184:187], v[192:195], v[118:121]
	v_mfma_f32_16x16x32_bf16 v[110:113], v[176:179], v[200:203], v[110:113]
	v_mfma_f32_16x16x32_bf16 v[102:105], v[184:187], v[200:203], v[102:105]
	v_mfma_f32_16x16x32_bf16 v[92:95], v[176:179], v[208:211], v[92:95]
	v_mfma_f32_16x16x32_bf16 v[84:87], v[184:187], v[208:211], v[84:87]
	v_mfma_f32_16x16x32_bf16 v[76:79], v[176:179], v[220:223], v[76:79]
	v_mfma_f32_16x16x32_bf16 v[68:71], v[184:187], v[220:223], v[68:71]
	v_mfma_f32_16x16x32_bf16 v[126:129], v[180:183], v[196:199], v[126:129]
	v_mfma_f32_16x16x32_bf16 v[118:121], v[188:191], v[196:199], v[118:121]
	v_mfma_f32_16x16x32_bf16 v[110:113], v[180:183], v[204:207], v[110:113]
	v_mfma_f32_16x16x32_bf16 v[102:105], v[188:191], v[204:207], v[102:105]
	v_mfma_f32_16x16x32_bf16 v[92:95], v[180:183], v[212:215], v[92:95]
	v_mfma_f32_16x16x32_bf16 v[84:87], v[188:191], v[212:215], v[84:87]
	v_mfma_f32_16x16x32_bf16 v[76:79], v[180:183], v[224:227], v[76:79]
	v_mfma_f32_16x16x32_bf16 v[68:71], v[188:191], v[224:227], v[68:71]
	s_barrier
	v_mov_b32_e32 v135, v138
	s_add_i32 s2, s67, s56
	ds_read_b128 v[192:195], v152 offset:16384
	ds_read_b128 v[196:199], v152 offset:17408
	ds_read_b128 v[200:203], v152 offset:18432
	ds_read_b128 v[204:207], v152 offset:19456
	ds_read_b128 v[208:211], v152 offset:20480
	ds_read_b128 v[212:215], v152 offset:21504
	ds_read_b128 v[220:223], v152 offset:22528
	ds_read_b128 v[224:227], v152 offset:23552
	s_mov_b32 m0, s2
	s_nop 0
	global_load_lds_dwordx4 v135, s[22:23]
	v_mov_b32_e32 v135, v141
	s_add_i32 m0, s2, 0x2000
	s_add_u32 s2, s22, 0x40000
	global_load_lds_dwordx4 v135, s[22:23]
	s_addc_u32 s3, s23, 0
	v_mov_b32_e32 v135, v138
	s_add_i32 s67, s68, s56
	s_mov_b32 m0, s67
	s_nop 0
	global_load_lds_dwordx4 v135, s[2:3]
	v_mov_b32_e32 v135, v141
	s_add_i32 m0, s67, 0x2000
	s_nop 0
	global_load_lds_dwordx4 v135, s[2:3]
	v_mov_b32_e32 v135, v134
	s_mov_b32 m0, s57
	s_nop 0
	global_load_lds_dwordx4 v135, s[20:21]
	v_mov_b32_e32 v135, v132
	s_mov_b32 m0, s58
	s_nop 0
	global_load_lds_dwordx4 v135, s[20:21]
	s_waitcnt vmcnt(8)
	s_waitcnt lgkmcnt(0)
	s_barrier
	s_waitcnt lgkmcnt(0)
	v_mfma_f32_16x16x32_bf16 v[56:59], v[160:163], v[192:195], v[56:59]
	v_mfma_f32_16x16x32_bf16 v[48:51], v[168:171], v[192:195], v[48:51]
	v_mfma_f32_16x16x32_bf16 v[40:43], v[160:163], v[200:203], v[40:43]
	v_mfma_f32_16x16x32_bf16 v[32:35], v[168:171], v[200:203], v[32:35]
	v_mfma_f32_16x16x32_bf16 v[24:27], v[160:163], v[208:211], v[24:27]
	v_mfma_f32_16x16x32_bf16 v[16:19], v[168:171], v[208:211], v[16:19]
	v_mfma_f32_16x16x32_bf16 v[8:11], v[160:163], v[220:223], v[8:11]
	v_mfma_f32_16x16x32_bf16 v[4:7], v[168:171], v[220:223], v[4:7]
	v_mfma_f32_16x16x32_bf16 v[56:59], v[164:167], v[196:199], v[56:59]
	v_mfma_f32_16x16x32_bf16 v[48:51], v[172:175], v[196:199], v[48:51]
	v_mfma_f32_16x16x32_bf16 v[40:43], v[164:167], v[204:207], v[40:43]
	v_mfma_f32_16x16x32_bf16 v[32:35], v[172:175], v[204:207], v[32:35]
	v_mfma_f32_16x16x32_bf16 v[24:27], v[164:167], v[212:215], v[24:27]
	v_mfma_f32_16x16x32_bf16 v[16:19], v[172:175], v[212:215], v[16:19]
	v_mfma_f32_16x16x32_bf16 v[8:11], v[164:167], v[224:227], v[8:11]
	v_mfma_f32_16x16x32_bf16 v[4:7], v[172:175], v[224:227], v[4:7]
	v_mfma_f32_16x16x32_bf16 v[60:63], v[176:179], v[192:195], v[60:63]
	v_mfma_f32_16x16x32_bf16 v[52:55], v[184:187], v[192:195], v[52:55]
	v_mfma_f32_16x16x32_bf16 v[44:47], v[176:179], v[200:203], v[44:47]
	v_mfma_f32_16x16x32_bf16 v[36:39], v[184:187], v[200:203], v[36:39]
	v_mfma_f32_16x16x32_bf16 v[28:31], v[176:179], v[208:211], v[28:31]
	v_mfma_f32_16x16x32_bf16 v[20:23], v[184:187], v[208:211], v[20:23]
	v_mfma_f32_16x16x32_bf16 v[12:15], v[176:179], v[220:223], v[12:15]
	v_mfma_f32_16x16x32_bf16 v[0:3], v[184:187], v[220:223], v[0:3]
	v_mfma_f32_16x16x32_bf16 v[60:63], v[180:183], v[196:199], v[60:63]
	v_mfma_f32_16x16x32_bf16 v[52:55], v[188:191], v[196:199], v[52:55]
	v_mfma_f32_16x16x32_bf16 v[44:47], v[180:183], v[204:207], v[44:47]
	v_mfma_f32_16x16x32_bf16 v[36:39], v[188:191], v[204:207], v[36:39]
	v_mfma_f32_16x16x32_bf16 v[28:31], v[180:183], v[212:215], v[28:31]
	v_mfma_f32_16x16x32_bf16 v[20:23], v[188:191], v[212:215], v[20:23]
	v_mfma_f32_16x16x32_bf16 v[12:15], v[180:183], v[224:227], v[12:15]
	v_mfma_f32_16x16x32_bf16 v[0:3], v[188:191], v[224:227], v[0:3]
	s_barrier
; #define PG8_STAGE(bufoff, gbase, voff) do { _Pragma("unroll") for (int _i = 0; _i < 2; ++_i) \
;         __builtin_amdgcn_global_load_lds((const __attribute__((address_space(1))) unsigned*)((const __attribute__((address_space(1))) char*)(gbase) + (unsigned)lnd_v((int)(voff)[_i])), (LAS unsigned*)(lds + (bufoff) + ldsw + _i * 8192), 16, 0, 0); } while (0)
; #define PG8_LDA(dst, b, h) do { _Pragma("unroll") for (int m = 0; m < 4; ++m) _Pragma("unroll") for (int k = 0; k < 2; ++k) dst[m][k] = *(const LAS bf16x8*)(lds + PG8_SA(b, h) + aoff + m * 2048 + k * 1024); } while (0)
; #define PG8_LDB(dst, b, h) do { _Pragma("unroll") for (int n = 0; n < 2; ++n) _Pragma("unroll") for (int k = 0; k < 2; ++k) dst[n][k] = *(const LAS bf16x8*)(lds + PG8_SB(b, h) + boff + n * 2048 + k * 1024); } while (0)
; #define PG8_MMA(ai, bj, At, Bt) do { __builtin_amdgcn_s_setprio(1); _Pragma("unroll") for (int m = 0; m < 4; ++m) _Pragma("unroll") for (int n = 0; n < 2; ++n) _Pragma("unroll") for (int k = 0; k < 2; ++k) \
;         acc[ai][bj][m][n] = __builtin_amdgcn_mfma_f32_16x16x32_bf16(Bt[n][k], At[m][k], acc[ai][bj][m][n], 0, 0, 0); __builtin_amdgcn_s_setprio(0); } while (0)
; #define PG8_WAIT_V(n) asm volatile("s_waitcnt vmcnt(" #n ")" ::: "memory")
; #define PG8_WAIT_L(n) asm volatile("s_waitcnt lgkmcnt(" #n ")" ::: "memory")
; #define PG8_BAR __builtin_amdgcn_s_barrier()
; #define PG8_SCHED __builtin_amdgcn_sched_barrier(0)
; template <class Desc, class Epi>
; __device__ __forceinline__ void gemm_phase(const int wv_, LAS unsigned char* lds, const Desc& d, const Epi& E) {
;     ...
;             PG8_LDB(B0, 1, 0); PG8_LDB(B1, 1, 1); PG8_SCHED; PG8_LDA(At, 1, 0); PG8_STAGE(PG8_SA(0, 1), a2, sA1);
;             PG8_WAIT_V(8); PG8_WAIT_L(0); PG8_BAR; PG8_MMA(0, 0, At, B0); PG8_MMA(0, 1, At, B1); PG8_BAR; PG8_SCHED;
	s_add_i32 s2, 0, 0x18000
	v_add_u32_e32 v135, s2, v143
	s_add_i32 s67, 0, 0x1c000
	ds_read_b128 v[160:163], v135
	ds_read_b128 v[164:167], v135 offset:1024
	ds_read_b128 v[168:171], v135 offset:2048
	ds_read_b128 v[172:175], v135 offset:3072
	v_add_u32_e32 v135, s67, v143
	ds_read_b128 v[176:179], v135
	ds_read_b128 v[180:183], v135 offset:1024
	ds_read_b128 v[184:187], v135 offset:2048
	ds_read_b128 v[188:191], v135 offset:3072
	s_mov_b32 m0, s59
	ds_read_b128 v[192:195], v152 offset:32768
	ds_read_b128 v[196:199], v152 offset:33792
	ds_read_b128 v[200:203], v152 offset:34816
	ds_read_b128 v[204:207], v152 offset:35840
	ds_read_b128 v[208:211], v152 offset:36864
	ds_read_b128 v[212:215], v152 offset:37888
	ds_read_b128 v[220:223], v152 offset:38912
	ds_read_b128 v[224:227], v152 offset:39936
	s_nop 0
	global_load_lds_dwordx4 v96, s[20:21]
	s_mov_b32 m0, s60
	s_nop 0
	global_load_lds_dwordx4 v133, s[20:21]
	s_waitcnt vmcnt(8)
	s_waitcnt lgkmcnt(0)
	s_barrier
	s_waitcnt lgkmcnt(0)
	v_mfma_f32_16x16x32_bf16 v[122:125], v[160:163], v[192:195], v[122:125]
	v_mfma_f32_16x16x32_bf16 v[114:117], v[168:171], v[192:195], v[114:117]
	v_mfma_f32_16x16x32_bf16 v[106:109], v[160:163], v[200:203], v[106:109]
	v_mfma_f32_16x16x32_bf16 v[98:101], v[168:171], v[200:203], v[98:101]
	v_mfma_f32_16x16x32_bf16 v[88:91], v[160:163], v[208:211], v[88:91]
	v_mfma_f32_16x16x32_bf16 v[80:83], v[168:171], v[208:211], v[80:83]
	v_mfma_f32_16x16x32_bf16 v[72:75], v[160:163], v[220:223], v[72:75]
	v_mfma_f32_16x16x32_bf16 v[64:67], v[168:171], v[220:223], v[64:67]
	v_mfma_f32_16x16x32_bf16 v[122:125], v[164:167], v[196:199], v[122:125]
	v_mfma_f32_16x16x32_bf16 v[114:117], v[172:175], v[196:199], v[114:117]
	v_mfma_f32_16x16x32_bf16 v[106:109], v[164:167], v[204:207], v[106:109]
	v_mfma_f32_16x16x32_bf16 v[98:101], v[172:175], v[204:207], v[98:101]
	v_mfma_f32_16x16x32_bf16 v[88:91], v[164:167], v[212:215], v[88:91]
	v_mfma_f32_16x16x32_bf16 v[80:83], v[172:175], v[212:215], v[80:83]
	v_mfma_f32_16x16x32_bf16 v[72:75], v[164:167], v[224:227], v[72:75]
	v_mfma_f32_16x16x32_bf16 v[64:67], v[172:175], v[224:227], v[64:67]
	v_mfma_f32_16x16x32_bf16 v[126:129], v[176:179], v[192:195], v[126:129]
	v_mfma_f32_16x16x32_bf16 v[118:121], v[184:187], v[192:195], v[118:121]
	v_mfma_f32_16x16x32_bf16 v[110:113], v[176:179], v[200:203], v[110:113]
	v_mfma_f32_16x16x32_bf16 v[102:105], v[184:187], v[200:203], v[102:105]
	v_mfma_f32_16x16x32_bf16 v[92:95], v[176:179], v[208:211], v[92:95]
	v_mfma_f32_16x16x32_bf16 v[84:87], v[184:187], v[208:211], v[84:87]
	v_mfma_f32_16x16x32_bf16 v[76:79], v[176:179], v[220:223], v[76:79]
	v_mfma_f32_16x16x32_bf16 v[68:71], v[184:187], v[220:223], v[68:71]
	v_mfma_f32_16x16x32_bf16 v[126:129], v[180:183], v[196:199], v[126:129]
	v_mfma_f32_16x16x32_bf16 v[118:121], v[188:191], v[196:199], v[118:121]
	v_mfma_f32_16x16x32_bf16 v[110:113], v[180:183], v[204:207], v[110:113]
	v_mfma_f32_16x16x32_bf16 v[102:105], v[188:191], v[204:207], v[102:105]
	v_mfma_f32_16x16x32_bf16 v[92:95], v[180:183], v[212:215], v[92:95]
	v_mfma_f32_16x16x32_bf16 v[84:87], v[188:191], v[212:215], v[84:87]
	v_mfma_f32_16x16x32_bf16 v[76:79], v[180:183], v[224:227], v[76:79]
	v_mfma_f32_16x16x32_bf16 v[68:71], v[188:191], v[224:227], v[68:71]
	s_barrier
; #define PG8_AOFF(ord, U, O0, O1) do { _Pragma("unroll") for (int _i = 0; _i < 2; ++_i) { \
;         O0[_i] = d.rowbyte(U, (int)tix[(ord) * 256 + Rr[_i]]) + (unsigned)(Cc[_i] * 2); O1[_i] = d.rowbyte(U, (int)tix[(ord) * 256 + HALF + Rr[_i]]) + (unsigned)(Cc[_i] * 2); } } while (0)
; #define PG8_STAGE(bufoff, gbase, voff) do { _Pragma("unroll") for (int _i = 0; _i < 2; ++_i) \
;         __builtin_amdgcn_global_load_lds((const __attribute__((address_space(1))) unsigned*)((const __attribute__((address_space(1))) char*)(gbase) + (unsigned)lnd_v((int)(voff)[_i])), (LAS unsigned*)(lds + (bufoff) + ldsw + _i * 8192), 16, 0, 0); } while (0)
; #define PG8_LDA(dst, b, h) do { _Pragma("unroll") for (int m = 0; m < 4; ++m) _Pragma("unroll") for (int k = 0; k < 2; ++k) dst[m][k] = *(const LAS bf16x8*)(lds + PG8_SA(b, h) + aoff + m * 2048 + k * 1024); } while (0)
; template <class Desc, class Epi>
; __device__ __forceinline__ void gemm_phase(const int wv_, LAS unsigned char* lds, const Desc& d, const Epi& E) {
;     ...
;         const int inext = bid + (ui + 1) * nblk; const bool has_next = inext < d.nunits;
;         if (has_next) d.unit(inext, nxt);
;         if constexpr (Desc::GATHER) { if (has_next) PG8_AOFF(ui + 1, nxt, voffAn, voffAn1); else { voffAn[0] = voffA[0]; voffAn[1] = voffA[1]; voffAn1[0] = voffA1[0]; voffAn1[1] = voffA1[1]; } }
;         const char* nA = has_next ? (const char*)nxt.a : cA; const char* nB = has_next ? (const char*)nxt.b : cB;
;         for (int t = 0; t < nt; t += 2) {
;             const bool last = (t == nt - 2);
;             unsigned sA0[2], sA1[2];
;             if constexpr (Desc::GATHER) { sA0[0] = last ? voffAn[0] : voffA[0]; sA0[1] = last ? voffAn[1] : voffA[1]; sA1[0] = last ? voffAn1[0] : voffA1[0]; sA1[1] = last ? voffAn1[1] : voffA1[1]; }
;             else { sA0[0] = voffA[0]; sA0[1] = voffA[1]; sA1[0] = voffA1[0]; sA1[1] = voffA1[1]; }
;             const char* a1 = cA + (size_t)(t + 1) * kstep;
;             const char* a2 = last ? nA : cA + (size_t)(t + 2) * kstep; const char* b2 = last ? nB : cB + (size_t)(t + 2) * kstep;
;     ...
;             PG8_LDA(At, 1, 1); PG8_STAGE(PG8_SB(1, 0), b3, voffB); PG8_STAGE(PG8_SB(1, 1), b3 + hstepB, voffB); PG8_STAGE(PG8_SA(1, 0), a3, sA0);
;             PG8_WAIT_V(8); PG8_WAIT_L(0); PG8_BAR; PG8_MMA(1, 0, At, B0); PG8_MMA(1, 1, At, B1); PG8_BAR; PG8_SCHED;
;         }
	v_mov_b32_e32 v96, v138
	ds_read_b128 v[192:195], v152 offset:49152
	ds_read_b128 v[196:199], v152 offset:50176
	ds_read_b128 v[200:203], v152 offset:51200
	ds_read_b128 v[204:207], v152 offset:52224
	ds_read_b128 v[208:211], v152 offset:53248
	ds_read_b128 v[212:215], v152 offset:54272
	ds_read_b128 v[220:223], v152 offset:55296
	ds_read_b128 v[224:227], v152 offset:56320
	s_add_i32 s2, s2, s56
	v_lshl_add_u64 v[228:229], s[22:23], 0, v[96:97]
	v_lshl_add_u64 v[228:229], v[228:229], 0, s[30:31]
	s_mov_b32 m0, s2
	v_mov_b32_e32 v96, v141
	global_load_lds_dwordx4 v[228:229], off
	s_add_i32 m0, s2, 0x2000
	s_add_u32 s2, s22, 0x40080
	v_lshl_add_u64 v[228:229], s[22:23], 0, v[96:97]
	v_lshl_add_u64 v[228:229], v[228:229], 0, s[30:31]
	s_addc_u32 s3, s23, 0
	v_mov_b32_e32 v96, v138
	s_add_i32 s22, s67, s56
	global_load_lds_dwordx4 v[228:229], off
	s_mov_b32 m0, s22
	v_mov_b32_e32 v135, v97
	global_load_lds_dwordx4 v96, s[2:3]
	v_mov_b32_e32 v96, v141
	s_add_i32 m0, s22, 0x2000
	v_mov_b32_e32 v133, v97
	global_load_lds_dwordx4 v96, s[2:3]
	s_mov_b32 m0, s61
	v_lshl_add_u64 v[134:135], s[20:21], 0, v[134:135]
	v_lshl_add_u64 v[134:135], v[134:135], 0, s[30:31]
	global_load_lds_dwordx4 v[134:135], off
	s_mov_b32 m0, s62
	v_lshl_add_u64 v[132:133], s[20:21], 0, v[132:133]
	v_lshl_add_u64 v[132:133], v[132:133], 0, s[30:31]
	global_load_lds_dwordx4 v[132:133], off
	s_add_i32 s66, s66, 2
	s_mov_b64 s[2:3], s[4:5]
	s_add_u32 s4, s2, 0x100
	s_addc_u32 s5, s3, 0
	s_add_u32 s22, s29, s2
	s_addc_u32 s23, s51, s3
	s_cmp_eq_u32 s66, 12
	s_cselect_b64 vcc, -1, 0
	s_and_b64 s[20:21], vcc, exec
	s_cselect_b32 s20, 0, s4
	s_cselect_b32 s21, 0, s5
	s_cselect_b32 s22, s46, s22
	s_cselect_b32 s23, s47, s23
	s_add_u32 s20, s42, s20
	s_addc_u32 s21, s43, s21
	s_add_i32 s67, 0, 0x10000
	v_add_u32_e32 v135, s67, v143
	s_add_i32 s68, 0, 0x14000
	s_waitcnt vmcnt(8)
	s_waitcnt lgkmcnt(0)
	s_barrier
	s_waitcnt lgkmcnt(0)
	v_mfma_f32_16x16x32_bf16 v[56:59], v[160:163], v[192:195], v[56:59]
	v_mfma_f32_16x16x32_bf16 v[48:51], v[168:171], v[192:195], v[48:51]
	v_mfma_f32_16x16x32_bf16 v[40:43], v[160:163], v[200:203], v[40:43]
	v_mfma_f32_16x16x32_bf16 v[32:35], v[168:171], v[200:203], v[32:35]
	v_mfma_f32_16x16x32_bf16 v[24:27], v[160:163], v[208:211], v[24:27]
	v_mfma_f32_16x16x32_bf16 v[16:19], v[168:171], v[208:211], v[16:19]
	v_mfma_f32_16x16x32_bf16 v[8:11], v[160:163], v[220:223], v[8:11]
	v_mfma_f32_16x16x32_bf16 v[4:7], v[168:171], v[220:223], v[4:7]
	v_mfma_f32_16x16x32_bf16 v[56:59], v[164:167], v[196:199], v[56:59]
	v_mfma_f32_16x16x32_bf16 v[48:51], v[172:175], v[196:199], v[48:51]
	v_mfma_f32_16x16x32_bf16 v[40:43], v[164:167], v[204:207], v[40:43]
	v_mfma_f32_16x16x32_bf16 v[32:35], v[172:175], v[204:207], v[32:35]
	v_mfma_f32_16x16x32_bf16 v[24:27], v[164:167], v[212:215], v[24:27]
	v_mfma_f32_16x16x32_bf16 v[16:19], v[172:175], v[212:215], v[16:19]
	v_mfma_f32_16x16x32_bf16 v[8:11], v[164:167], v[224:227], v[8:11]
	v_mfma_f32_16x16x32_bf16 v[4:7], v[172:175], v[224:227], v[4:7]
	v_mfma_f32_16x16x32_bf16 v[60:63], v[176:179], v[192:195], v[60:63]
	v_mfma_f32_16x16x32_bf16 v[52:55], v[184:187], v[192:195], v[52:55]
	v_mfma_f32_16x16x32_bf16 v[44:47], v[176:179], v[200:203], v[44:47]
	v_mfma_f32_16x16x32_bf16 v[36:39], v[184:187], v[200:203], v[36:39]
	v_mfma_f32_16x16x32_bf16 v[28:31], v[176:179], v[208:211], v[28:31]
	v_mfma_f32_16x16x32_bf16 v[20:23], v[184:187], v[208:211], v[20:23]
	v_mfma_f32_16x16x32_bf16 v[12:15], v[176:179], v[220:223], v[12:15]
	v_mfma_f32_16x16x32_bf16 v[0:3], v[184:187], v[220:223], v[0:3]
	v_mfma_f32_16x16x32_bf16 v[60:63], v[180:183], v[196:199], v[60:63]
	v_mfma_f32_16x16x32_bf16 v[52:55], v[188:191], v[196:199], v[52:55]
	v_mfma_f32_16x16x32_bf16 v[44:47], v[180:183], v[204:207], v[44:47]
	v_mfma_f32_16x16x32_bf16 v[36:39], v[188:191], v[204:207], v[36:39]
	v_mfma_f32_16x16x32_bf16 v[28:31], v[180:183], v[212:215], v[28:31]
	v_mfma_f32_16x16x32_bf16 v[20:23], v[188:191], v[212:215], v[20:23]
	v_mfma_f32_16x16x32_bf16 v[12:15], v[180:183], v[224:227], v[12:15]
	v_mfma_f32_16x16x32_bf16 v[0:3], v[188:191], v[224:227], v[0:3]
	s_barrier
	s_cmp_gt_u32 s66, 13
	s_cbranch_scc0 .Lkrot_1861
	s_and_b64 vcc, exec, s[40:41]
	s_cbranch_vccz .LBB0_1864
	s_barrier

; #define PG8_STAGE(bufoff, gbase, voff) do { _Pragma("unroll") for (int _i = 0; _i < 2; ++_i) \
;         __builtin_amdgcn_global_load_lds((const __attribute__((address_space(1))) unsigned*)((const __attribute__((address_space(1))) char*)(gbase) + (unsigned)lnd_v((int)(voff)[_i])), (LAS unsigned*)(lds + (bufoff) + ldsw + _i * 8192), 16, 0, 0); } while (0)
; #define PG8_LDA(dst, b, h) do { _Pragma("unroll") for (int m = 0; m < 4; ++m) _Pragma("unroll") for (int k = 0; k < 2; ++k) dst[m][k] = *(const LAS bf16x8*)(lds + PG8_SA(b, h) + aoff + m * 2048 + k * 1024); } while (0)
; #define PG8_LDB(dst, b, h) do { _Pragma("unroll") for (int n = 0; n < 2; ++n) _Pragma("unroll") for (int k = 0; k < 2; ++k) dst[n][k] = *(const LAS bf16x8*)(lds + PG8_SB(b, h) + boff + n * 2048 + k * 1024); } while (0)
; #define PG8_MMA(ai, bj, At, Bt) do { __builtin_amdgcn_s_setprio(1); _Pragma("unroll") for (int m = 0; m < 4; ++m) _Pragma("unroll") for (int n = 0; n < 2; ++n) _Pragma("unroll") for (int k = 0; k < 2; ++k) \
;         acc[ai][bj][m][n] = __builtin_amdgcn_mfma_f32_16x16x32_bf16(Bt[n][k], At[m][k], acc[ai][bj][m][n], 0, 0, 0); __builtin_amdgcn_s_setprio(0); } while (0)
; #define PG8_WAIT_V(n) asm volatile("s_waitcnt vmcnt(" #n ")" ::: "memory")
; #define PG8_WAIT_L(n) asm volatile("s_waitcnt lgkmcnt(" #n ")" ::: "memory")
; #define PG8_BAR __builtin_amdgcn_s_barrier()
; #define PG8_SCHED __builtin_amdgcn_sched_barrier(0)
; template <class Desc, class Epi>
; __device__ __forceinline__ void gemm_phase(const int wv_, LAS unsigned char* lds, const Desc& d, const Epi& E) {
;     ...
;             PG8_LDB(B0, 0, 0); PG8_LDB(B1, 0, 1); PG8_SCHED; PG8_LDA(At, 0, 0); PG8_STAGE(PG8_SA(1, 1), a1, voffA1);
;             PG8_WAIT_V(8); PG8_WAIT_L(0); PG8_BAR; PG8_MMA(0, 0, At, B0); PG8_MMA(0, 1, At, B1); PG8_BAR; PG8_SCHED;
;             PG8_LDA(At, 0, 1); PG8_STAGE(PG8_SB(0, 0), b2, voffB); PG8_STAGE(PG8_SB(0, 1), b2 + hstepB, voffB); PG8_STAGE(PG8_SA(0, 0), a2, sA0);
;             PG8_WAIT_V(8); PG8_WAIT_L(0); PG8_BAR; PG8_MMA(1, 0, At, B0); PG8_MMA(1, 1, At, B1); PG8_BAR; PG8_SCHED;
.Lkrot_1942:
	ds_read_b128 v[150:153], v96
	ds_read_b128 v[154:157], v96 offset:1024
	ds_read_b128 v[158:161], v96 offset:2048
	ds_read_b128 v[162:165], v96 offset:3072
	v_add_u32_e32 v96, s66, v139
	ds_read_b128 v[166:169], v96
	ds_read_b128 v[170:173], v96 offset:1024
	ds_read_b128 v[174:177], v96 offset:2048
	ds_read_b128 v[178:181], v96 offset:3072
	v_mov_b32_e32 v96, v133
	ds_read_b128 v[182:185], v149
	ds_read_b128 v[186:189], v149 offset:1024
	ds_read_b128 v[190:193], v149 offset:2048
	ds_read_b128 v[194:197], v149 offset:3072
	ds_read_b128 v[198:201], v149 offset:4096
	ds_read_b128 v[202:205], v149 offset:5120
	ds_read_b128 v[206:209], v149 offset:6144
	ds_read_b128 v[210:213], v149 offset:7168
	s_add_i32 m0, s53, 0xc000
	s_nop 0
	global_load_lds_dwordx4 v96, s[2:3]
	v_mov_b32_e32 v96, v136
	s_add_i32 m0, s53, 0xe000
	s_nop 0
	global_load_lds_dwordx4 v96, s[2:3]
	s_waitcnt vmcnt(8)
	s_waitcnt lgkmcnt(0)
	s_barrier
	s_waitcnt lgkmcnt(0)
	v_mfma_f32_16x16x32_bf16 v[126:129], v[150:153], v[182:185], v[126:129]
	v_mfma_f32_16x16x32_bf16 v[122:125], v[158:161], v[182:185], v[122:125]
	v_mfma_f32_16x16x32_bf16 v[110:113], v[150:153], v[190:193], v[110:113]
	v_mfma_f32_16x16x32_bf16 v[106:109], v[158:161], v[190:193], v[106:109]
	v_mfma_f32_16x16x32_bf16 v[92:95], v[150:153], v[198:201], v[92:95]
	v_mfma_f32_16x16x32_bf16 v[88:91], v[158:161], v[198:201], v[88:91]
	v_mfma_f32_16x16x32_bf16 v[76:79], v[150:153], v[206:209], v[76:79]
	v_mfma_f32_16x16x32_bf16 v[72:75], v[158:161], v[206:209], v[72:75]
	v_mfma_f32_16x16x32_bf16 v[126:129], v[154:157], v[186:189], v[126:129]
	v_mfma_f32_16x16x32_bf16 v[122:125], v[162:165], v[186:189], v[122:125]
	v_mfma_f32_16x16x32_bf16 v[110:113], v[154:157], v[194:197], v[110:113]
	v_mfma_f32_16x16x32_bf16 v[106:109], v[162:165], v[194:197], v[106:109]
	v_mfma_f32_16x16x32_bf16 v[92:95], v[154:157], v[202:205], v[92:95]
	v_mfma_f32_16x16x32_bf16 v[88:91], v[162:165], v[202:205], v[88:91]
	v_mfma_f32_16x16x32_bf16 v[76:79], v[154:157], v[210:213], v[76:79]
	v_mfma_f32_16x16x32_bf16 v[72:75], v[162:165], v[210:213], v[72:75]
	v_mfma_f32_16x16x32_bf16 v[118:121], v[166:169], v[182:185], v[118:121]
	v_mfma_f32_16x16x32_bf16 v[114:117], v[174:177], v[182:185], v[114:117]
	v_mfma_f32_16x16x32_bf16 v[102:105], v[166:169], v[190:193], v[102:105]
	v_mfma_f32_16x16x32_bf16 v[98:101], v[174:177], v[190:193], v[98:101]
	v_mfma_f32_16x16x32_bf16 v[84:87], v[166:169], v[198:201], v[84:87]
	v_mfma_f32_16x16x32_bf16 v[80:83], v[174:177], v[198:201], v[80:83]
	v_mfma_f32_16x16x32_bf16 v[68:71], v[166:169], v[206:209], v[68:71]
	v_mfma_f32_16x16x32_bf16 v[64:67], v[174:177], v[206:209], v[64:67]
	v_mfma_f32_16x16x32_bf16 v[118:121], v[170:173], v[186:189], v[118:121]
	v_mfma_f32_16x16x32_bf16 v[114:117], v[178:181], v[186:189], v[114:117]
	v_mfma_f32_16x16x32_bf16 v[102:105], v[170:173], v[194:197], v[102:105]
	v_mfma_f32_16x16x32_bf16 v[98:101], v[178:181], v[194:197], v[98:101]
	v_mfma_f32_16x16x32_bf16 v[84:87], v[170:173], v[202:205], v[84:87]
	v_mfma_f32_16x16x32_bf16 v[80:83], v[178:181], v[202:205], v[80:83]
	v_mfma_f32_16x16x32_bf16 v[68:71], v[170:173], v[210:213], v[68:71]
	v_mfma_f32_16x16x32_bf16 v[64:67], v[178:181], v[210:213], v[64:67]
	s_barrier
	v_mov_b32_e32 v96, v134
	s_add_i32 s63, s63, s52
	ds_read_b128 v[182:185], v149 offset:16384
	ds_read_b128 v[186:189], v149 offset:17408
	ds_read_b128 v[190:193], v149 offset:18432
	ds_read_b128 v[194:197], v149 offset:19456
	ds_read_b128 v[198:201], v149 offset:20480
	ds_read_b128 v[202:205], v149 offset:21504
	ds_read_b128 v[206:209], v149 offset:22528
	ds_read_b128 v[210:213], v149 offset:23552
	s_mov_b32 m0, s63
	s_nop 0
	global_load_lds_dwordx4 v96, s[20:21]
	v_mov_b32_e32 v96, v137
	s_add_i32 m0, s63, 0x2000
	s_add_u32 s64, s20, 0x80000
	global_load_lds_dwordx4 v96, s[20:21]
	s_addc_u32 s65, s21, 0
	v_mov_b32_e32 v96, v134
	s_add_i32 s63, s66, s52
	s_mov_b32 m0, s63
	s_nop 0
	global_load_lds_dwordx4 v96, s[64:65]
	v_mov_b32_e32 v96, v137
	s_add_i32 m0, s63, 0x2000
	s_nop 0
	global_load_lds_dwordx4 v96, s[64:65]
	v_mov_b32_e32 v96, v132
	s_mov_b32 m0, s53
	s_nop 0
	global_load_lds_dwordx4 v96, s[4:5]
	v_mov_b32_e32 v96, v135
	s_mov_b32 m0, s54
	s_nop 0
	global_load_lds_dwordx4 v96, s[4:5]
	s_waitcnt vmcnt(8)
	s_waitcnt lgkmcnt(0)
	s_barrier
	s_waitcnt lgkmcnt(0)
	v_mfma_f32_16x16x32_bf16 v[60:63], v[150:153], v[182:185], v[60:63]
	v_mfma_f32_16x16x32_bf16 v[56:59], v[158:161], v[182:185], v[56:59]
	v_mfma_f32_16x16x32_bf16 v[44:47], v[150:153], v[190:193], v[44:47]
	v_mfma_f32_16x16x32_bf16 v[32:35], v[158:161], v[190:193], v[32:35]
	v_mfma_f32_16x16x32_bf16 v[16:19], v[150:153], v[198:201], v[16:19]
	v_mfma_f32_16x16x32_bf16 v[8:11], v[158:161], v[198:201], v[8:11]
	v_mfma_f32_16x16x32_bf16 v[4:7], v[150:153], v[206:209], v[4:7]
	v_mfma_f32_16x16x32_bf16 v[0:3], v[158:161], v[206:209], v[0:3]
	v_mfma_f32_16x16x32_bf16 v[60:63], v[154:157], v[186:189], v[60:63]
	v_mfma_f32_16x16x32_bf16 v[56:59], v[162:165], v[186:189], v[56:59]
	v_mfma_f32_16x16x32_bf16 v[44:47], v[154:157], v[194:197], v[44:47]
	v_mfma_f32_16x16x32_bf16 v[32:35], v[162:165], v[194:197], v[32:35]
	v_mfma_f32_16x16x32_bf16 v[16:19], v[154:157], v[202:205], v[16:19]
	v_mfma_f32_16x16x32_bf16 v[8:11], v[162:165], v[202:205], v[8:11]
	v_mfma_f32_16x16x32_bf16 v[4:7], v[154:157], v[210:213], v[4:7]
	v_mfma_f32_16x16x32_bf16 v[0:3], v[162:165], v[210:213], v[0:3]
	v_mfma_f32_16x16x32_bf16 v[52:55], v[166:169], v[182:185], v[52:55]
	v_mfma_f32_16x16x32_bf16 v[48:51], v[174:177], v[182:185], v[48:51]
	v_mfma_f32_16x16x32_bf16 v[28:31], v[166:169], v[190:193], v[28:31]
	v_mfma_f32_16x16x32_bf16 v[12:15], v[174:177], v[190:193], v[12:15]
	v_mfma_f32_16x16x32_bf16 v[36:39], v[166:169], v[198:201], v[36:39]
	v_mfma_f32_16x16x32_bf16 v[40:43], v[174:177], v[198:201], v[40:43]
	v_mfma_f32_16x16x32_bf16 v[20:23], v[166:169], v[206:209], v[20:23]
	v_mfma_f32_16x16x32_bf16 v[24:27], v[174:177], v[206:209], v[24:27]
	v_mfma_f32_16x16x32_bf16 v[52:55], v[170:173], v[186:189], v[52:55]
	v_mfma_f32_16x16x32_bf16 v[48:51], v[178:181], v[186:189], v[48:51]
	v_mfma_f32_16x16x32_bf16 v[28:31], v[170:173], v[194:197], v[28:31]
	v_mfma_f32_16x16x32_bf16 v[12:15], v[178:181], v[194:197], v[12:15]
	v_mfma_f32_16x16x32_bf16 v[36:39], v[170:173], v[202:205], v[36:39]
	v_mfma_f32_16x16x32_bf16 v[40:43], v[178:181], v[202:205], v[40:43]
	v_mfma_f32_16x16x32_bf16 v[20:23], v[170:173], v[210:213], v[20:23]
	v_mfma_f32_16x16x32_bf16 v[24:27], v[178:181], v[210:213], v[24:27]
	s_barrier
; #define PG8_STAGE(bufoff, gbase, voff) do { _Pragma("unroll") for (int _i = 0; _i < 2; ++_i) \
;         __builtin_amdgcn_global_load_lds((const __attribute__((address_space(1))) unsigned*)((const __attribute__((address_space(1))) char*)(gbase) + (unsigned)lnd_v((int)(voff)[_i])), (LAS unsigned*)(lds + (bufoff) + ldsw + _i * 8192), 16, 0, 0); } while (0)
; #define PG8_LDA(dst, b, h) do { _Pragma("unroll") for (int m = 0; m < 4; ++m) _Pragma("unroll") for (int k = 0; k < 2; ++k) dst[m][k] = *(const LAS bf16x8*)(lds + PG8_SA(b, h) + aoff + m * 2048 + k * 1024); } while (0)
; #define PG8_LDB(dst, b, h) do { _Pragma("unroll") for (int n = 0; n < 2; ++n) _Pragma("unroll") for (int k = 0; k < 2; ++k) dst[n][k] = *(const LAS bf16x8*)(lds + PG8_SB(b, h) + boff + n * 2048 + k * 1024); } while (0)
; #define PG8_MMA(ai, bj, At, Bt) do { __builtin_amdgcn_s_setprio(1); _Pragma("unroll") for (int m = 0; m < 4; ++m) _Pragma("unroll") for (int n = 0; n < 2; ++n) _Pragma("unroll") for (int k = 0; k < 2; ++k) \
;         acc[ai][bj][m][n] = __builtin_amdgcn_mfma_f32_16x16x32_bf16(Bt[n][k], At[m][k], acc[ai][bj][m][n], 0, 0, 0); __builtin_amdgcn_s_setprio(0); } while (0)
; #define PG8_WAIT_V(n) asm volatile("s_waitcnt vmcnt(" #n ")" ::: "memory")
; #define PG8_WAIT_L(n) asm volatile("s_waitcnt lgkmcnt(" #n ")" ::: "memory")
; #define PG8_BAR __builtin_amdgcn_s_barrier()
; #define PG8_SCHED __builtin_amdgcn_sched_barrier(0)
; template <class Desc, class Epi>
; __device__ __forceinline__ void gemm_phase(const int wv_, LAS unsigned char* lds, const Desc& d, const Epi& E) {
;     ...
;             PG8_LDB(B0, 1, 0); PG8_LDB(B1, 1, 1); PG8_SCHED; PG8_LDA(At, 1, 0); PG8_STAGE(PG8_SA(0, 1), a2, sA1);
;             PG8_WAIT_V(8); PG8_WAIT_L(0); PG8_BAR; PG8_MMA(0, 0, At, B0); PG8_MMA(0, 1, At, B1); PG8_BAR; PG8_SCHED;
	s_add_i32 s63, 0, 0x18000
	v_add_u32_e32 v96, s63, v139
	s_add_i32 s64, 0, 0x1c000
	ds_read_b128 v[150:153], v96
	ds_read_b128 v[154:157], v96 offset:1024
	ds_read_b128 v[158:161], v96 offset:2048
	ds_read_b128 v[162:165], v96 offset:3072
	v_add_u32_e32 v96, s64, v139
	ds_read_b128 v[166:169], v96
	ds_read_b128 v[170:173], v96 offset:1024
	ds_read_b128 v[174:177], v96 offset:2048
	ds_read_b128 v[178:181], v96 offset:3072
	v_mov_b32_e32 v96, v133
	s_mov_b32 m0, s55
	ds_read_b128 v[182:185], v149 offset:32768
	ds_read_b128 v[186:189], v149 offset:33792
	ds_read_b128 v[190:193], v149 offset:34816
	ds_read_b128 v[194:197], v149 offset:35840
	ds_read_b128 v[198:201], v149 offset:36864
	ds_read_b128 v[202:205], v149 offset:37888
	ds_read_b128 v[206:209], v149 offset:38912
	ds_read_b128 v[210:213], v149 offset:39936
	s_nop 0
	global_load_lds_dwordx4 v96, s[4:5]
	v_mov_b32_e32 v96, v136
	s_mov_b32 m0, s56
	s_nop 0
	global_load_lds_dwordx4 v96, s[4:5]
	s_waitcnt vmcnt(8)
	s_waitcnt lgkmcnt(0)
	s_barrier
	s_waitcnt lgkmcnt(0)
	v_mfma_f32_16x16x32_bf16 v[126:129], v[150:153], v[182:185], v[126:129]
	v_mfma_f32_16x16x32_bf16 v[122:125], v[158:161], v[182:185], v[122:125]
	v_mfma_f32_16x16x32_bf16 v[110:113], v[150:153], v[190:193], v[110:113]
	v_mfma_f32_16x16x32_bf16 v[106:109], v[158:161], v[190:193], v[106:109]
	v_mfma_f32_16x16x32_bf16 v[92:95], v[150:153], v[198:201], v[92:95]
	v_mfma_f32_16x16x32_bf16 v[88:91], v[158:161], v[198:201], v[88:91]
	v_mfma_f32_16x16x32_bf16 v[76:79], v[150:153], v[206:209], v[76:79]
	v_mfma_f32_16x16x32_bf16 v[72:75], v[158:161], v[206:209], v[72:75]
	v_mfma_f32_16x16x32_bf16 v[126:129], v[154:157], v[186:189], v[126:129]
	v_mfma_f32_16x16x32_bf16 v[122:125], v[162:165], v[186:189], v[122:125]
	v_mfma_f32_16x16x32_bf16 v[110:113], v[154:157], v[194:197], v[110:113]
	v_mfma_f32_16x16x32_bf16 v[106:109], v[162:165], v[194:197], v[106:109]
	v_mfma_f32_16x16x32_bf16 v[92:95], v[154:157], v[202:205], v[92:95]
	v_mfma_f32_16x16x32_bf16 v[88:91], v[162:165], v[202:205], v[88:91]
	v_mfma_f32_16x16x32_bf16 v[76:79], v[154:157], v[210:213], v[76:79]
	v_mfma_f32_16x16x32_bf16 v[72:75], v[162:165], v[210:213], v[72:75]
	v_mfma_f32_16x16x32_bf16 v[118:121], v[166:169], v[182:185], v[118:121]
	v_mfma_f32_16x16x32_bf16 v[114:117], v[174:177], v[182:185], v[114:117]
	v_mfma_f32_16x16x32_bf16 v[102:105], v[166:169], v[190:193], v[102:105]
	v_mfma_f32_16x16x32_bf16 v[98:101], v[174:177], v[190:193], v[98:101]
	v_mfma_f32_16x16x32_bf16 v[84:87], v[166:169], v[198:201], v[84:87]
	v_mfma_f32_16x16x32_bf16 v[80:83], v[174:177], v[198:201], v[80:83]
	v_mfma_f32_16x16x32_bf16 v[68:71], v[166:169], v[206:209], v[68:71]
	v_mfma_f32_16x16x32_bf16 v[64:67], v[174:177], v[206:209], v[64:67]
	v_mfma_f32_16x16x32_bf16 v[118:121], v[170:173], v[186:189], v[118:121]
	v_mfma_f32_16x16x32_bf16 v[114:117], v[178:181], v[186:189], v[114:117]
	v_mfma_f32_16x16x32_bf16 v[102:105], v[170:173], v[194:197], v[102:105]
	v_mfma_f32_16x16x32_bf16 v[98:101], v[178:181], v[194:197], v[98:101]
	v_mfma_f32_16x16x32_bf16 v[84:87], v[170:173], v[202:205], v[84:87]
	v_mfma_f32_16x16x32_bf16 v[80:83], v[178:181], v[202:205], v[80:83]
	v_mfma_f32_16x16x32_bf16 v[68:71], v[170:173], v[210:213], v[68:71]
	v_mfma_f32_16x16x32_bf16 v[64:67], v[178:181], v[210:213], v[64:67]
	s_barrier
; #define PG8_AOFF(ord, U, O0, O1) do { _Pragma("unroll") for (int _i = 0; _i < 2; ++_i) { \
;         O0[_i] = d.rowbyte(U, (int)tix[(ord) * 256 + Rr[_i]]) + (unsigned)(Cc[_i] * 2); O1[_i] = d.rowbyte(U, (int)tix[(ord) * 256 + HALF + Rr[_i]]) + (unsigned)(Cc[_i] * 2); } } while (0)
; #define PG8_STAGE(bufoff, gbase, voff) do { _Pragma("unroll") for (int _i = 0; _i < 2; ++_i) \
;         __builtin_amdgcn_global_load_lds((const __attribute__((address_space(1))) unsigned*)((const __attribute__((address_space(1))) char*)(gbase) + (unsigned)lnd_v((int)(voff)[_i])), (LAS unsigned*)(lds + (bufoff) + ldsw + _i * 8192), 16, 0, 0); } while (0)
; #define PG8_LDA(dst, b, h) do { _Pragma("unroll") for (int m = 0; m < 4; ++m) _Pragma("unroll") for (int k = 0; k < 2; ++k) dst[m][k] = *(const LAS bf16x8*)(lds + PG8_SA(b, h) + aoff + m * 2048 + k * 1024); } while (0)
; template <class Desc, class Epi>
; __device__ __forceinline__ void gemm_phase(const int wv_, LAS unsigned char* lds, const Desc& d, const Epi& E) {
;     ...
;         const int inext = bid + (ui + 1) * nblk; const bool has_next = inext < d.nunits;
;         if (has_next) d.unit(inext, nxt);
;         if constexpr (Desc::GATHER) { if (has_next) PG8_AOFF(ui + 1, nxt, voffAn, voffAn1); else { voffAn[0] = voffA[0]; voffAn[1] = voffA[1]; voffAn1[0] = voffA1[0]; voffAn1[1] = voffA1[1]; } }
;         const char* nA = has_next ? (const char*)nxt.a : cA; const char* nB = has_next ? (const char*)nxt.b : cB;
;         for (int t = 0; t < nt; t += 2) {
;             const bool last = (t == nt - 2);
;             unsigned sA0[2], sA1[2];
;             if constexpr (Desc::GATHER) { sA0[0] = last ? voffAn[0] : voffA[0]; sA0[1] = last ? voffAn[1] : voffA[1]; sA1[0] = last ? voffAn1[0] : voffA1[0]; sA1[1] = last ? voffAn1[1] : voffA1[1]; }
;             else { sA0[0] = voffA[0]; sA0[1] = voffA[1]; sA1[0] = voffA1[0]; sA1[1] = voffA1[1]; }
;             const char* a1 = cA + (size_t)(t + 1) * kstep;
;             const char* a2 = last ? nA : cA + (size_t)(t + 2) * kstep; const char* b2 = last ? nB : cB + (size_t)(t + 2) * kstep;
;     ...
;             PG8_LDA(At, 1, 1); PG8_STAGE(PG8_SB(1, 0), b3, voffB); PG8_STAGE(PG8_SB(1, 1), b3 + hstepB, voffB); PG8_STAGE(PG8_SA(1, 0), a3, sA0);
;             PG8_WAIT_V(8); PG8_WAIT_L(0); PG8_BAR; PG8_MMA(1, 0, At, B0); PG8_MMA(1, 1, At, B1); PG8_BAR; PG8_SCHED;
;         }
	v_mov_b32_e32 v96, v134
	ds_read_b128 v[182:185], v149 offset:49152
	ds_read_b128 v[186:189], v149 offset:50176
	ds_read_b128 v[190:193], v149 offset:51200
	ds_read_b128 v[194:197], v149 offset:52224
	ds_read_b128 v[198:201], v149 offset:53248
	ds_read_b128 v[202:205], v149 offset:54272
	ds_read_b128 v[206:209], v149 offset:55296
	ds_read_b128 v[210:213], v149 offset:56320
	s_add_i32 s63, s63, s52
	v_lshl_add_u64 v[130:131], s[20:21], 0, v[96:97]
	v_lshl_add_u64 v[130:131], v[130:131], 0, s[30:31]
	s_mov_b32 m0, s63
	v_mov_b32_e32 v96, v137
	global_load_lds_dwordx4 v[130:131], off
	s_add_i32 m0, s63, 0x2000
	s_nop 0
	v_lshl_add_u64 v[130:131], s[20:21], 0, v[96:97]
	s_add_u32 s20, s20, 0x80080
	v_lshl_add_u64 v[130:131], v[130:131], 0, s[30:31]
	s_addc_u32 s21, s21, 0
	v_mov_b32_e32 v96, v134
	s_add_i32 s63, s64, s52
	global_load_lds_dwordx4 v[130:131], off
	s_mov_b32 m0, s63
	s_nop 0
	global_load_lds_dwordx4 v96, s[20:21]
	v_mov_b32_e32 v96, v137
	s_add_i32 m0, s63, 0x2000
	s_nop 0
	global_load_lds_dwordx4 v96, s[20:21]
	v_mov_b32_e32 v96, v132
	s_mov_b32 m0, s57
	v_lshl_add_u64 v[130:131], s[4:5], 0, v[96:97]
	v_lshl_add_u64 v[130:131], v[130:131], 0, s[30:31]
	v_mov_b32_e32 v96, v135
	global_load_lds_dwordx4 v[130:131], off
	s_mov_b32 m0, s58
	v_lshl_add_u64 v[130:131], s[4:5], 0, v[96:97]
	v_lshl_add_u64 v[130:131], v[130:131], 0, s[30:31]
	global_load_lds_dwordx4 v[130:131], off
	s_add_i32 s62, s62, 2
	s_add_u32 s2, s2, 0x100
	s_addc_u32 s3, s3, 0
	s_add_u32 s29, s29, 0x100
	s_addc_u32 s43, s43, 0
	s_add_u32 s4, s2, 0x80
	s_addc_u32 s5, s3, 0
	s_add_i32 s63, 0, 0x10000
	s_cmp_eq_u32 s62, 28
	s_cselect_b32 s5, s47, s5
	s_cselect_b32 s4, s46, s4
	v_add_u32_e32 v96, s63, v139
	s_cselect_b32 s21, s45, s43
	s_cselect_b32 s20, s44, s29
	s_add_i32 s66, 0, 0x14000
	s_waitcnt vmcnt(8)
	s_waitcnt lgkmcnt(0)
	s_barrier
	s_waitcnt lgkmcnt(0)
	v_mfma_f32_16x16x32_bf16 v[60:63], v[150:153], v[182:185], v[60:63]
	v_mfma_f32_16x16x32_bf16 v[56:59], v[158:161], v[182:185], v[56:59]
	v_mfma_f32_16x16x32_bf16 v[44:47], v[150:153], v[190:193], v[44:47]
	v_mfma_f32_16x16x32_bf16 v[32:35], v[158:161], v[190:193], v[32:35]
	v_mfma_f32_16x16x32_bf16 v[16:19], v[150:153], v[198:201], v[16:19]
	v_mfma_f32_16x16x32_bf16 v[8:11], v[158:161], v[198:201], v[8:11]
	v_mfma_f32_16x16x32_bf16 v[4:7], v[150:153], v[206:209], v[4:7]
	v_mfma_f32_16x16x32_bf16 v[0:3], v[158:161], v[206:209], v[0:3]
	v_mfma_f32_16x16x32_bf16 v[60:63], v[154:157], v[186:189], v[60:63]
	v_mfma_f32_16x16x32_bf16 v[56:59], v[162:165], v[186:189], v[56:59]
	v_mfma_f32_16x16x32_bf16 v[44:47], v[154:157], v[194:197], v[44:47]
	v_mfma_f32_16x16x32_bf16 v[32:35], v[162:165], v[194:197], v[32:35]
	v_mfma_f32_16x16x32_bf16 v[16:19], v[154:157], v[202:205], v[16:19]
	v_mfma_f32_16x16x32_bf16 v[8:11], v[162:165], v[202:205], v[8:11]
	v_mfma_f32_16x16x32_bf16 v[4:7], v[154:157], v[210:213], v[4:7]
	v_mfma_f32_16x16x32_bf16 v[0:3], v[162:165], v[210:213], v[0:3]
	v_mfma_f32_16x16x32_bf16 v[52:55], v[166:169], v[182:185], v[52:55]
	v_mfma_f32_16x16x32_bf16 v[48:51], v[174:177], v[182:185], v[48:51]
	v_mfma_f32_16x16x32_bf16 v[28:31], v[166:169], v[190:193], v[28:31]
	v_mfma_f32_16x16x32_bf16 v[12:15], v[174:177], v[190:193], v[12:15]
	v_mfma_f32_16x16x32_bf16 v[36:39], v[166:169], v[198:201], v[36:39]
	v_mfma_f32_16x16x32_bf16 v[40:43], v[174:177], v[198:201], v[40:43]
	v_mfma_f32_16x16x32_bf16 v[20:23], v[166:169], v[206:209], v[20:23]
	v_mfma_f32_16x16x32_bf16 v[24:27], v[174:177], v[206:209], v[24:27]
	v_mfma_f32_16x16x32_bf16 v[52:55], v[170:173], v[186:189], v[52:55]
	v_mfma_f32_16x16x32_bf16 v[48:51], v[178:181], v[186:189], v[48:51]
	v_mfma_f32_16x16x32_bf16 v[28:31], v[170:173], v[194:197], v[28:31]
	v_mfma_f32_16x16x32_bf16 v[12:15], v[178:181], v[194:197], v[12:15]
	v_mfma_f32_16x16x32_bf16 v[36:39], v[170:173], v[202:205], v[36:39]
	v_mfma_f32_16x16x32_bf16 v[40:43], v[178:181], v[202:205], v[40:43]
	v_mfma_f32_16x16x32_bf16 v[20:23], v[170:173], v[210:213], v[20:23]
	v_mfma_f32_16x16x32_bf16 v[24:27], v[178:181], v[210:213], v[24:27]
	s_barrier
	s_cmp_gt_u32 s62, 29
	s_cbranch_scc0 .Lkrot_1942
	s_and_b64 vcc, exec, s[40:41]
	s_cbranch_vccz .LBB0_1945
	s_barrier
